# v15: + DIFF V-fragment prefetch, MLA wait trim, GEMM wait merge
# speedup vs baseline: 1.0042x; 1.0042x over previous
; #define PG8_STAGE(bufoff, gbase, voff) do { _Pragma("unroll") for (int _i = 0; _i < 2; ++_i) \
;         __builtin_amdgcn_global_load_lds((const unsigned*)((const char*)(gbase) + (voff)[_i]), (PG8_LAS unsigned*)(lds + (bufoff) + ldsw + _i * 8192), 16, 0, 0); } while (0)
; #define PG8_LDA(dst, b, h) do { _Pragma("unroll") for (int m = 0; m < 4; ++m) _Pragma("unroll") for (int k = 0; k < 2; ++k) dst[m][k] = *(const PG8_LAS bf16x8*)(lds + PG8_SA(b, h) + aoff + m * 2048 + k * 1024); } while (0)
; #define PG8_LDB(dst, b, h) do { _Pragma("unroll") for (int n = 0; n < 2; ++n) _Pragma("unroll") for (int k = 0; k < 2; ++k) dst[n][k] = *(const PG8_LAS bf16x8*)(lds + PG8_SB(b, h) + boff + n * 2048 + k * 1024); } while (0)
; #define PG8_MMA(ai, bj, At, Bt) do { __builtin_amdgcn_s_setprio(1); _Pragma("unroll") for (int m = 0; m < 4; ++m) _Pragma("unroll") for (int n = 0; n < 2; ++n) _Pragma("unroll") for (int k = 0; k < 2; ++k) \
;         acc[ai][bj][m][n] = __builtin_amdgcn_mfma_f32_16x16x32_bf16(Bt[n][k], At[m][k], acc[ai][bj][m][n], 0, 0, 0); __builtin_amdgcn_s_setprio(0); } while (0)
; #define PG8_WAIT_V(n) asm volatile("s_waitcnt vmcnt(" #n ")" ::: "memory")
; #define PG8_BAR __builtin_amdgcn_s_barrier()
; template <class Epi, class Sched, bool ALIGN_EPI = false, bool SP2 = false>
; __device__ __forceinline__ void gemm_phase(PG8_LAS unsigned char* lds, const Gemm g, const Sched& S, const Epi& E, const int wid) {
;     ...
;         for (int t = 0; t < nt; t += 2) {
;             const bool last = (t == nt - 2);
;             const char* a1 = cA + (size_t)(t + 1) * kstep;
;             const char* a2 = last ? nA : cA + (size_t)(t + 2) * kstep; const char* b2 = last ? nB : cB + (size_t)(t + 2) * kstep;
;             const char* a3 = a2 + kstep; const char* b3 = b2 + kstep;
;             if (last && has_next) S.a_ready(nxt);
;             if constexpr (SP2) {
;             PG8_LDB(B0, 0, 0); PG8_LDB(B1, 0, 1); PG8_SCHED; PG8_LDA(At, 0, 0); PG8_STAGE(PG8_SA(1, 1), a1 + hstepA, voffA);
;             PG8_WAIT_V(8); PG8_WAIT_L(0); PG8_BAR; PG8_MMA(0, 0, At, B0); PG8_MMA(0, 1, At, B1); PG8_BAR; PG8_SCHED;
;             PG8_LDA(At, 0, 1); PG8_STAGE(PG8_SB(0, 0), b2, voffB); PG8_STAGE(PG8_SB(0, 1), b2 + hstepB, voffB); PG8_STAGE(PG8_SA(0, 0), a2, voffA);
;             PG8_WAIT_V(8); PG8_WAIT_L(0); PG8_BAR; PG8_MMA(1, 0, At, B0); PG8_MMA(1, 1, At, B1); PG8_BAR; PG8_SCHED;
.LBB0_349:
	ds_read_b128 v[128:131], v183
	ds_read_b128 v[150:153], v183 offset:1024
	ds_read_b128 v[154:157], v183 offset:2048
	ds_read_b128 v[158:161], v183 offset:3072
	ds_read_b128 v[162:165], v184
	ds_read_b128 v[166:169], v184 offset:1024
	ds_read_b128 v[170:173], v184 offset:2048
	ds_read_b128 v[188:191], v184 offset:3072
	s_add_u32 s36, s8, 0xfffc0080
	s_addc_u32 s37, s9, -1
	s_cmp_eq_u32 s75, 12
	s_cselect_b32 s41, s7, s37
	s_cselect_b32 s40, s27, s36
	s_cselect_b32 s37, s25, s74
	s_cselect_b32 s36, s35, s73
	s_add_i32 m0, s46, 0xc000
	ds_read_b128 v[192:195], v185
	ds_read_b128 v[196:199], v185 offset:1024
	ds_read_b128 v[200:203], v185 offset:2048
	ds_read_b128 v[204:207], v185 offset:3072
	ds_read_b128 v[208:211], v185 offset:4096
	ds_read_b128 v[212:215], v185 offset:5120
	ds_read_b128 v[216:219], v185 offset:6144
	ds_read_b128 v[220:223], v185 offset:7168
	global_load_lds_dwordx4 v142, s[8:9]
	s_add_i32 m0, s46, 0xe000
	s_nop 0
	global_load_lds_dwordx4 v144, s[8:9]
	s_waitcnt vmcnt(8) lgkmcnt(0)
	s_barrier
	s_setprio 1
	v_mfma_f32_16x16x32_bf16 v[124:127], v[128:131], v[192:195], v[124:127]
	v_mfma_f32_16x16x32_bf16 v[120:123], v[154:157], v[192:195], v[120:123]
	v_mfma_f32_16x16x32_bf16 v[108:111], v[128:131], v[200:203], v[108:111]
	v_mfma_f32_16x16x32_bf16 v[104:107], v[154:157], v[200:203], v[104:107]
	v_mfma_f32_16x16x32_bf16 v[92:95], v[128:131], v[208:211], v[92:95]
	v_mfma_f32_16x16x32_bf16 v[88:91], v[154:157], v[208:211], v[88:91]
	v_mfma_f32_16x16x32_bf16 v[76:79], v[128:131], v[216:219], v[76:79]
	v_mfma_f32_16x16x32_bf16 v[72:75], v[154:157], v[216:219], v[72:75]
	v_mfma_f32_16x16x32_bf16 v[124:127], v[150:153], v[196:199], v[124:127]
	v_mfma_f32_16x16x32_bf16 v[120:123], v[158:161], v[196:199], v[120:123]
	v_mfma_f32_16x16x32_bf16 v[108:111], v[150:153], v[204:207], v[108:111]
	v_mfma_f32_16x16x32_bf16 v[104:107], v[158:161], v[204:207], v[104:107]
	v_mfma_f32_16x16x32_bf16 v[92:95], v[150:153], v[212:215], v[92:95]
	v_mfma_f32_16x16x32_bf16 v[88:91], v[158:161], v[212:215], v[88:91]
	v_mfma_f32_16x16x32_bf16 v[76:79], v[150:153], v[220:223], v[76:79]
	v_mfma_f32_16x16x32_bf16 v[72:75], v[158:161], v[220:223], v[72:75]
	s_setprio 0
	s_setprio 1
	v_mfma_f32_16x16x32_bf16 v[116:119], v[162:165], v[192:195], v[116:119]
	v_mfma_f32_16x16x32_bf16 v[112:115], v[170:173], v[192:195], v[112:115]
	v_mfma_f32_16x16x32_bf16 v[100:103], v[162:165], v[200:203], v[100:103]
	v_mfma_f32_16x16x32_bf16 v[96:99], v[170:173], v[200:203], v[96:99]
	v_mfma_f32_16x16x32_bf16 v[84:87], v[162:165], v[208:211], v[84:87]
	v_mfma_f32_16x16x32_bf16 v[80:83], v[170:173], v[208:211], v[80:83]
	v_mfma_f32_16x16x32_bf16 v[68:71], v[162:165], v[216:219], v[68:71]
	v_mfma_f32_16x16x32_bf16 v[64:67], v[170:173], v[216:219], v[64:67]
	v_mfma_f32_16x16x32_bf16 v[116:119], v[166:169], v[196:199], v[116:119]
	v_mfma_f32_16x16x32_bf16 v[112:115], v[188:191], v[196:199], v[112:115]
	v_mfma_f32_16x16x32_bf16 v[100:103], v[166:169], v[204:207], v[100:103]
	v_mfma_f32_16x16x32_bf16 v[96:99], v[188:191], v[204:207], v[96:99]
	v_mfma_f32_16x16x32_bf16 v[84:87], v[166:169], v[212:215], v[84:87]
	v_mfma_f32_16x16x32_bf16 v[80:83], v[188:191], v[212:215], v[80:83]
	v_mfma_f32_16x16x32_bf16 v[68:71], v[166:169], v[220:223], v[68:71]
	v_mfma_f32_16x16x32_bf16 v[64:67], v[188:191], v[220:223], v[64:67]
	s_setprio 0
	s_barrier
	s_add_i32 s76, s69, s45
	v_lshl_add_u64 v[174:175], s[36:37], 0, v[134:135]
	s_mov_b32 m0, s76
	ds_read_b128 v[192:195], v185 offset:16384
	ds_read_b128 v[196:199], v185 offset:17408
	ds_read_b128 v[200:203], v185 offset:18432
	ds_read_b128 v[204:207], v185 offset:19456
	ds_read_b128 v[208:211], v185 offset:20480
	ds_read_b128 v[212:215], v185 offset:21504
	ds_read_b128 v[216:219], v185 offset:22528
	ds_read_b128 v[220:223], v185 offset:23552
	global_load_lds_dwordx4 v134, s[36:37]
	s_add_i32 m0, s76, 0x2000
	s_add_u32 s76, s36, 0x40000
	v_lshl_add_u64 v[224:225], s[36:37], 0, v[138:139]
	s_addc_u32 s77, s37, 0
	s_add_i32 s78, s70, s45
	global_load_lds_dwordx4 v138, s[36:37]
	s_mov_b32 m0, s78
	v_lshl_add_u64 v[228:229], s[40:41], 0, v[136:137]
	global_load_lds_dwordx4 v134, s[76:77]
	s_add_i32 m0, s78, 0x2000
	s_nop 0
	global_load_lds_dwordx4 v138, s[76:77]
	v_lshl_add_u64 v[226:227], s[40:41], 0, v[132:133]
	s_mov_b32 m0, s46
	s_nop 0
	global_load_lds_dwordx4 v132, s[40:41]
	s_mov_b32 m0, s47
	s_nop 0
	global_load_lds_dwordx4 v136, s[40:41]
	s_waitcnt vmcnt(8) lgkmcnt(0)
	s_barrier
	s_setprio 1
	v_mfma_f32_16x16x32_bf16 v[60:63], v[128:131], v[192:195], v[60:63]
	v_mfma_f32_16x16x32_bf16 v[56:59], v[154:157], v[192:195], v[56:59]
	v_mfma_f32_16x16x32_bf16 v[44:47], v[128:131], v[200:203], v[44:47]
	v_mfma_f32_16x16x32_bf16 v[40:43], v[154:157], v[200:203], v[40:43]
	v_mfma_f32_16x16x32_bf16 v[28:31], v[128:131], v[208:211], v[28:31]
	v_mfma_f32_16x16x32_bf16 v[24:27], v[154:157], v[208:211], v[24:27]
	v_mfma_f32_16x16x32_bf16 v[12:15], v[128:131], v[216:219], v[12:15]
	v_mfma_f32_16x16x32_bf16 v[8:11], v[154:157], v[216:219], v[8:11]
	v_mfma_f32_16x16x32_bf16 v[60:63], v[150:153], v[196:199], v[60:63]
	v_mfma_f32_16x16x32_bf16 v[56:59], v[158:161], v[196:199], v[56:59]
	v_mfma_f32_16x16x32_bf16 v[44:47], v[150:153], v[204:207], v[44:47]
	v_mfma_f32_16x16x32_bf16 v[40:43], v[158:161], v[204:207], v[40:43]
	v_mfma_f32_16x16x32_bf16 v[28:31], v[150:153], v[212:215], v[28:31]
	v_mfma_f32_16x16x32_bf16 v[24:27], v[158:161], v[212:215], v[24:27]
	v_mfma_f32_16x16x32_bf16 v[12:15], v[150:153], v[220:223], v[12:15]
	v_mfma_f32_16x16x32_bf16 v[8:11], v[158:161], v[220:223], v[8:11]
	s_setprio 0
	s_setprio 1
	v_mfma_f32_16x16x32_bf16 v[52:55], v[162:165], v[192:195], v[52:55]
	v_mfma_f32_16x16x32_bf16 v[48:51], v[170:173], v[192:195], v[48:51]
	v_mfma_f32_16x16x32_bf16 v[36:39], v[162:165], v[200:203], v[36:39]
	v_mfma_f32_16x16x32_bf16 v[32:35], v[170:173], v[200:203], v[32:35]
	v_mfma_f32_16x16x32_bf16 v[20:23], v[162:165], v[208:211], v[20:23]
	v_mfma_f32_16x16x32_bf16 v[16:19], v[170:173], v[208:211], v[16:19]
	v_mfma_f32_16x16x32_bf16 v[4:7], v[162:165], v[216:219], v[4:7]
	v_mfma_f32_16x16x32_bf16 v[0:3], v[170:173], v[216:219], v[0:3]
	v_mfma_f32_16x16x32_bf16 v[52:55], v[166:169], v[196:199], v[52:55]
	v_mfma_f32_16x16x32_bf16 v[48:51], v[188:191], v[196:199], v[48:51]
	v_mfma_f32_16x16x32_bf16 v[36:39], v[166:169], v[204:207], v[36:39]
	v_mfma_f32_16x16x32_bf16 v[32:35], v[188:191], v[204:207], v[32:35]
	v_mfma_f32_16x16x32_bf16 v[20:23], v[166:169], v[212:215], v[20:23]
	v_mfma_f32_16x16x32_bf16 v[16:19], v[188:191], v[212:215], v[16:19]
	v_mfma_f32_16x16x32_bf16 v[4:7], v[166:169], v[220:223], v[4:7]
	v_mfma_f32_16x16x32_bf16 v[0:3], v[188:191], v[220:223], v[0:3]
	s_setprio 0
	s_barrier
; #define PG8_STAGE(bufoff, gbase, voff) do { _Pragma("unroll") for (int _i = 0; _i < 2; ++_i) \
;         __builtin_amdgcn_global_load_lds((const unsigned*)((const char*)(gbase) + (voff)[_i]), (PG8_LAS unsigned*)(lds + (bufoff) + ldsw + _i * 8192), 16, 0, 0); } while (0)
; #define PG8_LDA(dst, b, h) do { _Pragma("unroll") for (int m = 0; m < 4; ++m) _Pragma("unroll") for (int k = 0; k < 2; ++k) dst[m][k] = *(const PG8_LAS bf16x8*)(lds + PG8_SA(b, h) + aoff + m * 2048 + k * 1024); } while (0)
; #define PG8_LDB(dst, b, h) do { _Pragma("unroll") for (int n = 0; n < 2; ++n) _Pragma("unroll") for (int k = 0; k < 2; ++k) dst[n][k] = *(const PG8_LAS bf16x8*)(lds + PG8_SB(b, h) + boff + n * 2048 + k * 1024); } while (0)
; #define PG8_MMA(ai, bj, At, Bt) do { __builtin_amdgcn_s_setprio(1); _Pragma("unroll") for (int m = 0; m < 4; ++m) _Pragma("unroll") for (int n = 0; n < 2; ++n) _Pragma("unroll") for (int k = 0; k < 2; ++k) \
;         acc[ai][bj][m][n] = __builtin_amdgcn_mfma_f32_16x16x32_bf16(Bt[n][k], At[m][k], acc[ai][bj][m][n], 0, 0, 0); __builtin_amdgcn_s_setprio(0); } while (0)
; #define PG8_WAIT_V(n) asm volatile("s_waitcnt vmcnt(" #n ")" ::: "memory")
; #define PG8_WAIT_L(n) asm volatile("s_waitcnt lgkmcnt(" #n ")" ::: "memory")
; #define PG8_BAR __builtin_amdgcn_s_barrier()
; #define PG8_SCHED __builtin_amdgcn_sched_barrier(0)
; template <class Epi, class Sched, bool ALIGN_EPI = false, bool SP2 = false>
; __device__ __forceinline__ void gemm_phase(PG8_LAS unsigned char* lds, const Gemm g, const Sched& S, const Epi& E, const int wid) {
;     ...
;         for (int t = 0; t < nt; t += 2) {
;             const bool last = (t == nt - 2);
;             const char* a1 = cA + (size_t)(t + 1) * kstep;
;             const char* a2 = last ? nA : cA + (size_t)(t + 2) * kstep; const char* b2 = last ? nB : cB + (size_t)(t + 2) * kstep;
;     ...
;             PG8_LDB(B0, 1, 0); PG8_LDB(B1, 1, 1); PG8_SCHED; PG8_LDA(At, 1, 0); PG8_STAGE(PG8_SA(0, 1), a2 + hstepA, voffA);
;             PG8_WAIT_V(8); PG8_WAIT_L(0); PG8_BAR; PG8_MMA(0, 0, At, B0); PG8_MMA(0, 1, At, B1); PG8_BAR; PG8_SCHED;
;             PG8_LDA(At, 1, 1); PG8_STAGE(PG8_SB(1, 0), b3, voffB); PG8_STAGE(PG8_SB(1, 1), b3 + hstepB, voffB); PG8_STAGE(PG8_SA(1, 0), a3, voffA);
;             PG8_WAIT_V(8); PG8_WAIT_L(0); PG8_BAR; PG8_MMA(1, 0, At, B0); PG8_MMA(1, 1, At, B1); PG8_BAR; PG8_SCHED;
	s_add_i32 s76, 0, 0x18000
	s_add_i32 s77, 0, 0x1c000
	v_add_u32_e32 v158, s76, v178
	v_add_u32_e32 v188, s77, v178
	ds_read_b128 v[128:131], v158
	ds_read_b128 v[150:153], v158 offset:1024
	ds_read_b128 v[154:157], v158 offset:2048
	ds_read_b128 v[158:161], v158 offset:3072
	ds_read_b128 v[162:165], v188
	ds_read_b128 v[166:169], v188 offset:1024
	ds_read_b128 v[170:173], v188 offset:2048
	ds_read_b128 v[188:191], v188 offset:3072
	s_add_u32 s40, s40, 0x40000
	s_addc_u32 s41, s41, 0
	s_mov_b32 m0, s48
	ds_read_b128 v[192:195], v185 offset:32768
	ds_read_b128 v[196:199], v185 offset:33792
	ds_read_b128 v[200:203], v185 offset:34816
	ds_read_b128 v[204:207], v185 offset:35840
	ds_read_b128 v[208:211], v185 offset:36864
	ds_read_b128 v[212:215], v185 offset:37888
	ds_read_b128 v[216:219], v185 offset:38912
	ds_read_b128 v[220:223], v185 offset:39936
	global_load_lds_dwordx4 v132, s[40:41]
	s_mov_b32 m0, s49
	s_nop 0
	global_load_lds_dwordx4 v136, s[40:41]
	s_waitcnt vmcnt(8) lgkmcnt(0)
	s_barrier
	s_setprio 1
	v_mfma_f32_16x16x32_bf16 v[124:127], v[128:131], v[192:195], v[124:127]
	v_mfma_f32_16x16x32_bf16 v[120:123], v[154:157], v[192:195], v[120:123]
	v_mfma_f32_16x16x32_bf16 v[108:111], v[128:131], v[200:203], v[108:111]
	v_mfma_f32_16x16x32_bf16 v[104:107], v[154:157], v[200:203], v[104:107]
	v_mfma_f32_16x16x32_bf16 v[92:95], v[128:131], v[208:211], v[92:95]
	v_mfma_f32_16x16x32_bf16 v[88:91], v[154:157], v[208:211], v[88:91]
	v_mfma_f32_16x16x32_bf16 v[76:79], v[128:131], v[216:219], v[76:79]
	v_mfma_f32_16x16x32_bf16 v[72:75], v[154:157], v[216:219], v[72:75]
	v_mfma_f32_16x16x32_bf16 v[124:127], v[150:153], v[196:199], v[124:127]
	v_mfma_f32_16x16x32_bf16 v[120:123], v[158:161], v[196:199], v[120:123]
	v_mfma_f32_16x16x32_bf16 v[108:111], v[150:153], v[204:207], v[108:111]
	v_mfma_f32_16x16x32_bf16 v[104:107], v[158:161], v[204:207], v[104:107]
	v_mfma_f32_16x16x32_bf16 v[92:95], v[150:153], v[212:215], v[92:95]
	v_mfma_f32_16x16x32_bf16 v[88:91], v[158:161], v[212:215], v[88:91]
	v_mfma_f32_16x16x32_bf16 v[76:79], v[150:153], v[220:223], v[76:79]
	v_mfma_f32_16x16x32_bf16 v[72:75], v[158:161], v[220:223], v[72:75]
	s_setprio 0
	s_setprio 1
	v_mfma_f32_16x16x32_bf16 v[116:119], v[162:165], v[192:195], v[116:119]
	v_mfma_f32_16x16x32_bf16 v[112:115], v[170:173], v[192:195], v[112:115]
	v_mfma_f32_16x16x32_bf16 v[100:103], v[162:165], v[200:203], v[100:103]
	v_mfma_f32_16x16x32_bf16 v[96:99], v[170:173], v[200:203], v[96:99]
	v_mfma_f32_16x16x32_bf16 v[84:87], v[162:165], v[208:211], v[84:87]
	v_mfma_f32_16x16x32_bf16 v[80:83], v[170:173], v[208:211], v[80:83]
	v_mfma_f32_16x16x32_bf16 v[68:71], v[162:165], v[216:219], v[68:71]
	v_mfma_f32_16x16x32_bf16 v[64:67], v[170:173], v[216:219], v[64:67]
	v_mfma_f32_16x16x32_bf16 v[116:119], v[166:169], v[196:199], v[116:119]
	v_mfma_f32_16x16x32_bf16 v[112:115], v[188:191], v[196:199], v[112:115]
	v_mfma_f32_16x16x32_bf16 v[100:103], v[166:169], v[204:207], v[100:103]
	v_mfma_f32_16x16x32_bf16 v[96:99], v[188:191], v[204:207], v[96:99]
	v_mfma_f32_16x16x32_bf16 v[84:87], v[166:169], v[212:215], v[84:87]
	v_mfma_f32_16x16x32_bf16 v[80:83], v[188:191], v[212:215], v[80:83]
	v_mfma_f32_16x16x32_bf16 v[68:71], v[166:169], v[220:223], v[68:71]
	v_mfma_f32_16x16x32_bf16 v[64:67], v[188:191], v[220:223], v[64:67]
	s_setprio 0
	s_barrier
	s_add_i32 s40, s76, s45
	v_lshl_add_u64 v[174:175], v[174:175], 0, s[18:19]
	s_mov_b32 m0, s40
	ds_read_b128 v[192:195], v185 offset:49152
	ds_read_b128 v[196:199], v185 offset:50176
	ds_read_b128 v[200:203], v185 offset:51200
	ds_read_b128 v[204:207], v185 offset:52224
	ds_read_b128 v[208:211], v185 offset:53248
	ds_read_b128 v[212:215], v185 offset:54272
	ds_read_b128 v[216:219], v185 offset:55296
	ds_read_b128 v[220:223], v185 offset:56320
	global_load_lds_dwordx4 v[174:175], off
	s_add_i32 m0, s40, 0x2000
	s_add_u32 s36, s36, 0x40080
	v_lshl_add_u64 v[174:175], v[224:225], 0, s[18:19]
	s_addc_u32 s37, s37, 0
	s_add_i32 s40, s77, s45
	global_load_lds_dwordx4 v[174:175], off
	s_mov_b32 m0, s40
	s_nop 0
	global_load_lds_dwordx4 v134, s[36:37]
	v_lshl_add_u64 v[174:175], s[36:37], 0, v[138:139]
	s_add_i32 m0, s40, 0x2000
	s_nop 0
	global_load_lds_dwordx4 v138, s[36:37]
	v_lshl_add_u64 v[174:175], v[226:227], 0, s[18:19]
	s_mov_b32 m0, s64
	s_nop 0
	global_load_lds_dwordx4 v[174:175], off
	v_lshl_add_u64 v[174:175], v[228:229], 0, s[18:19]
	s_mov_b32 m0, s65
	s_nop 0
	global_load_lds_dwordx4 v[174:175], off
	s_waitcnt vmcnt(8) lgkmcnt(0)
	s_barrier
	s_setprio 1
	v_mfma_f32_16x16x32_bf16 v[60:63], v[128:131], v[192:195], v[60:63]
	v_mfma_f32_16x16x32_bf16 v[56:59], v[154:157], v[192:195], v[56:59]
	v_mfma_f32_16x16x32_bf16 v[44:47], v[128:131], v[200:203], v[44:47]
	v_mfma_f32_16x16x32_bf16 v[40:43], v[154:157], v[200:203], v[40:43]
	v_mfma_f32_16x16x32_bf16 v[28:31], v[128:131], v[208:211], v[28:31]
	v_mfma_f32_16x16x32_bf16 v[24:27], v[154:157], v[208:211], v[24:27]
	v_mfma_f32_16x16x32_bf16 v[12:15], v[128:131], v[216:219], v[12:15]
	v_mfma_f32_16x16x32_bf16 v[8:11], v[154:157], v[216:219], v[8:11]
	v_mfma_f32_16x16x32_bf16 v[60:63], v[150:153], v[196:199], v[60:63]
	v_mfma_f32_16x16x32_bf16 v[56:59], v[158:161], v[196:199], v[56:59]
	v_mfma_f32_16x16x32_bf16 v[44:47], v[150:153], v[204:207], v[44:47]
	v_mfma_f32_16x16x32_bf16 v[40:43], v[158:161], v[204:207], v[40:43]
	v_mfma_f32_16x16x32_bf16 v[28:31], v[150:153], v[212:215], v[28:31]
	v_mfma_f32_16x16x32_bf16 v[24:27], v[158:161], v[212:215], v[24:27]
	v_mfma_f32_16x16x32_bf16 v[12:15], v[150:153], v[220:223], v[12:15]
	v_mfma_f32_16x16x32_bf16 v[8:11], v[158:161], v[220:223], v[8:11]
	s_setprio 0
	s_setprio 1
	v_mfma_f32_16x16x32_bf16 v[52:55], v[162:165], v[192:195], v[52:55]
	v_mfma_f32_16x16x32_bf16 v[48:51], v[170:173], v[192:195], v[48:51]
	v_mfma_f32_16x16x32_bf16 v[36:39], v[162:165], v[200:203], v[36:39]
	v_mfma_f32_16x16x32_bf16 v[32:35], v[170:173], v[200:203], v[32:35]
	v_mfma_f32_16x16x32_bf16 v[20:23], v[162:165], v[208:211], v[20:23]
	v_mfma_f32_16x16x32_bf16 v[16:19], v[170:173], v[208:211], v[16:19]
	v_mfma_f32_16x16x32_bf16 v[4:7], v[162:165], v[216:219], v[4:7]
	v_mfma_f32_16x16x32_bf16 v[0:3], v[170:173], v[216:219], v[0:3]
	v_mfma_f32_16x16x32_bf16 v[52:55], v[166:169], v[196:199], v[52:55]
	v_mfma_f32_16x16x32_bf16 v[48:51], v[188:191], v[196:199], v[48:51]
	v_mfma_f32_16x16x32_bf16 v[36:39], v[166:169], v[204:207], v[36:39]
	v_mfma_f32_16x16x32_bf16 v[32:35], v[188:191], v[204:207], v[32:35]
	v_mfma_f32_16x16x32_bf16 v[20:23], v[166:169], v[212:215], v[20:23]
	v_mfma_f32_16x16x32_bf16 v[16:19], v[188:191], v[212:215], v[16:19]
	v_mfma_f32_16x16x32_bf16 v[4:7], v[166:169], v[220:223], v[4:7]
	v_mfma_f32_16x16x32_bf16 v[0:3], v[188:191], v[220:223], v[0:3]
	s_setprio 0
	s_barrier
	s_add_i32 s75, s75, 2
	s_add_u32 s8, s8, 0x100
	s_addc_u32 s9, s9, 0
	s_add_u32 s73, s73, 0x100
	s_addc_u32 s74, s74, 0
	s_cmp_gt_u32 s75, 13
	s_cbranch_scc0 .LBB0_349
	s_and_b64 vcc, exec, s[20:21]
	s_cbranch_vccz .LBB0_352
	s_barrier

; #define PG8_STAGE(bufoff, gbase, voff) do { _Pragma("unroll") for (int _i = 0; _i < 2; ++_i) \
;         __builtin_amdgcn_global_load_lds((const unsigned*)((const char*)(gbase) + (voff)[_i]), (PG8_LAS unsigned*)(lds + (bufoff) + ldsw + _i * 8192), 16, 0, 0); } while (0)
; #define PG8_LDA(dst, b, h) do { _Pragma("unroll") for (int m = 0; m < 4; ++m) _Pragma("unroll") for (int k = 0; k < 2; ++k) dst[m][k] = *(const PG8_LAS bf16x8*)(lds + PG8_SA(b, h) + aoff + m * 2048 + k * 1024); } while (0)
; #define PG8_LDB(dst, b, h) do { _Pragma("unroll") for (int n = 0; n < 2; ++n) _Pragma("unroll") for (int k = 0; k < 2; ++k) dst[n][k] = *(const PG8_LAS bf16x8*)(lds + PG8_SB(b, h) + boff + n * 2048 + k * 1024); } while (0)
; #define PG8_MMA(ai, bj, At, Bt) do { __builtin_amdgcn_s_setprio(1); _Pragma("unroll") for (int m = 0; m < 4; ++m) _Pragma("unroll") for (int n = 0; n < 2; ++n) _Pragma("unroll") for (int k = 0; k < 2; ++k) \
;         acc[ai][bj][m][n] = __builtin_amdgcn_mfma_f32_16x16x32_bf16(Bt[n][k], At[m][k], acc[ai][bj][m][n], 0, 0, 0); __builtin_amdgcn_s_setprio(0); } while (0)
; #define PG8_WAIT_V(n) asm volatile("s_waitcnt vmcnt(" #n ")" ::: "memory")
; #define PG8_BAR __builtin_amdgcn_s_barrier()
; template <class Epi, class Sched, bool ALIGN_EPI = false, bool SP2 = false>
; __device__ __forceinline__ void gemm_phase(PG8_LAS unsigned char* lds, const Gemm g, const Sched& S, const Epi& E, const int wid) {
;     ...
;         for (int t = 0; t < nt; t += 2) {
;             const bool last = (t == nt - 2);
;             const char* a1 = cA + (size_t)(t + 1) * kstep;
;             const char* a2 = last ? nA : cA + (size_t)(t + 2) * kstep; const char* b2 = last ? nB : cB + (size_t)(t + 2) * kstep;
;             const char* a3 = a2 + kstep; const char* b3 = b2 + kstep;
;             if (last && has_next) S.a_ready(nxt);
;             if constexpr (SP2) {
;             PG8_LDB(B0, 0, 0); PG8_LDB(B1, 0, 1); PG8_SCHED; PG8_LDA(At, 0, 0); PG8_STAGE(PG8_SA(1, 1), a1 + hstepA, voffA);
;             PG8_WAIT_V(8); PG8_WAIT_L(0); PG8_BAR; PG8_MMA(0, 0, At, B0); PG8_MMA(0, 1, At, B1); PG8_BAR; PG8_SCHED;
;             PG8_LDA(At, 0, 1); PG8_STAGE(PG8_SB(0, 0), b2, voffB); PG8_STAGE(PG8_SB(0, 1), b2 + hstepB, voffB); PG8_STAGE(PG8_SA(0, 0), a2, voffA);
;             PG8_WAIT_V(8); PG8_WAIT_L(0); PG8_BAR; PG8_MMA(1, 0, At, B0); PG8_MMA(1, 1, At, B1); PG8_BAR; PG8_SCHED;
.LBB0_1780:
	ds_read_b128 v[128:131], v190
	ds_read_b128 v[132:135], v190 offset:1024
	ds_read_b128 v[136:139], v190 offset:2048
	ds_read_b128 v[140:143], v190 offset:3072
	ds_read_b128 v[144:147], v191
	ds_read_b128 v[148:151], v191 offset:1024
	ds_read_b128 v[172:175], v191 offset:2048
	ds_read_b128 v[176:179], v191 offset:3072
	s_add_u32 s34, s30, 0xfffc0080
	s_addc_u32 s35, s31, -1
	s_cmp_eq_u32 s70, 12
	s_cselect_b32 s37, s21, s35
	s_cselect_b32 s36, s27, s34
	s_cselect_b32 s35, s19, s69
	s_cselect_b32 s34, s29, s68
	s_add_i32 m0, s40, 0xc000
	ds_read_b128 v[180:183], v192
	ds_read_b128 v[184:187], v192 offset:1024
	ds_read_b128 v[194:197], v192 offset:2048
	ds_read_b128 v[198:201], v192 offset:3072
	ds_read_b128 v[202:205], v192 offset:4096
	ds_read_b128 v[206:209], v192 offset:5120
	ds_read_b128 v[210:213], v192 offset:6144
	ds_read_b128 v[214:217], v192 offset:7168
	global_load_lds_dwordx4 v164, s[30:31]
	s_add_i32 m0, s40, 0xe000
	s_nop 0
	global_load_lds_dwordx4 v166, s[30:31]
	s_waitcnt vmcnt(8) lgkmcnt(0)
	s_barrier
	s_setprio 1
	v_mfma_f32_16x16x32_bf16 v[124:127], v[128:131], v[180:183], v[124:127]
	v_mfma_f32_16x16x32_bf16 v[120:123], v[136:139], v[180:183], v[120:123]
	v_mfma_f32_16x16x32_bf16 v[108:111], v[128:131], v[194:197], v[108:111]
	v_mfma_f32_16x16x32_bf16 v[104:107], v[136:139], v[194:197], v[104:107]
	v_mfma_f32_16x16x32_bf16 v[92:95], v[128:131], v[202:205], v[92:95]
	v_mfma_f32_16x16x32_bf16 v[88:91], v[136:139], v[202:205], v[88:91]
	v_mfma_f32_16x16x32_bf16 v[76:79], v[128:131], v[210:213], v[76:79]
	v_mfma_f32_16x16x32_bf16 v[72:75], v[136:139], v[210:213], v[72:75]
	v_mfma_f32_16x16x32_bf16 v[124:127], v[132:135], v[184:187], v[124:127]
	v_mfma_f32_16x16x32_bf16 v[120:123], v[140:143], v[184:187], v[120:123]
	v_mfma_f32_16x16x32_bf16 v[108:111], v[132:135], v[198:201], v[108:111]
	v_mfma_f32_16x16x32_bf16 v[104:107], v[140:143], v[198:201], v[104:107]
	v_mfma_f32_16x16x32_bf16 v[92:95], v[132:135], v[206:209], v[92:95]
	v_mfma_f32_16x16x32_bf16 v[88:91], v[140:143], v[206:209], v[88:91]
	v_mfma_f32_16x16x32_bf16 v[76:79], v[132:135], v[214:217], v[76:79]
	v_mfma_f32_16x16x32_bf16 v[72:75], v[140:143], v[214:217], v[72:75]
	s_setprio 0
	s_setprio 1
	v_mfma_f32_16x16x32_bf16 v[116:119], v[144:147], v[180:183], v[116:119]
	v_mfma_f32_16x16x32_bf16 v[112:115], v[172:175], v[180:183], v[112:115]
	v_mfma_f32_16x16x32_bf16 v[100:103], v[144:147], v[194:197], v[100:103]
	v_mfma_f32_16x16x32_bf16 v[96:99], v[172:175], v[194:197], v[96:99]
	v_mfma_f32_16x16x32_bf16 v[84:87], v[144:147], v[202:205], v[84:87]
	v_mfma_f32_16x16x32_bf16 v[80:83], v[172:175], v[202:205], v[80:83]
	v_mfma_f32_16x16x32_bf16 v[68:71], v[144:147], v[210:213], v[68:71]
	v_mfma_f32_16x16x32_bf16 v[64:67], v[172:175], v[210:213], v[64:67]
	v_mfma_f32_16x16x32_bf16 v[116:119], v[148:151], v[184:187], v[116:119]
	v_mfma_f32_16x16x32_bf16 v[112:115], v[176:179], v[184:187], v[112:115]
	v_mfma_f32_16x16x32_bf16 v[100:103], v[148:151], v[198:201], v[100:103]
	v_mfma_f32_16x16x32_bf16 v[96:99], v[176:179], v[198:201], v[96:99]
	v_mfma_f32_16x16x32_bf16 v[84:87], v[148:151], v[206:209], v[84:87]
	v_mfma_f32_16x16x32_bf16 v[80:83], v[176:179], v[206:209], v[80:83]
	v_mfma_f32_16x16x32_bf16 v[68:71], v[148:151], v[214:217], v[68:71]
	v_mfma_f32_16x16x32_bf16 v[64:67], v[176:179], v[214:217], v[64:67]
	s_setprio 0
	s_barrier
	s_add_i32 s71, s65, s39
	v_lshl_add_u64 v[218:219], s[34:35], 0, v[154:155]
	s_mov_b32 m0, s71
	ds_read_b128 v[180:183], v192 offset:16384
	ds_read_b128 v[184:187], v192 offset:17408
	ds_read_b128 v[194:197], v192 offset:18432
	ds_read_b128 v[198:201], v192 offset:19456
	ds_read_b128 v[202:205], v192 offset:20480
	ds_read_b128 v[206:209], v192 offset:21504
	ds_read_b128 v[210:213], v192 offset:22528
	ds_read_b128 v[214:217], v192 offset:23552
	global_load_lds_dwordx4 v154, s[34:35]
	s_add_i32 m0, s71, 0x2000
	s_add_u32 s72, s34, 0x40000
	v_lshl_add_u64 v[220:221], s[34:35], 0, v[158:159]
	s_addc_u32 s73, s35, 0
	s_add_i32 s71, s66, s39
	global_load_lds_dwordx4 v158, s[34:35]
	s_mov_b32 m0, s71
	v_lshl_add_u64 v[224:225], s[36:37], 0, v[156:157]
	global_load_lds_dwordx4 v154, s[72:73]
	s_add_i32 m0, s71, 0x2000
	s_nop 0
	global_load_lds_dwordx4 v158, s[72:73]
	v_lshl_add_u64 v[222:223], s[36:37], 0, v[152:153]
	s_mov_b32 m0, s40
	s_nop 0
	global_load_lds_dwordx4 v152, s[36:37]
	s_mov_b32 m0, s41
	s_nop 0
	global_load_lds_dwordx4 v156, s[36:37]
	s_waitcnt vmcnt(8) lgkmcnt(0)
	s_barrier
	s_setprio 1
	v_mfma_f32_16x16x32_bf16 v[60:63], v[128:131], v[180:183], v[60:63]
	v_mfma_f32_16x16x32_bf16 v[56:59], v[136:139], v[180:183], v[56:59]
	v_mfma_f32_16x16x32_bf16 v[44:47], v[128:131], v[194:197], v[44:47]
	v_mfma_f32_16x16x32_bf16 v[40:43], v[136:139], v[194:197], v[40:43]
	v_mfma_f32_16x16x32_bf16 v[28:31], v[128:131], v[202:205], v[28:31]
	v_mfma_f32_16x16x32_bf16 v[24:27], v[136:139], v[202:205], v[24:27]
	v_mfma_f32_16x16x32_bf16 v[12:15], v[128:131], v[210:213], v[12:15]
	v_mfma_f32_16x16x32_bf16 v[8:11], v[136:139], v[210:213], v[8:11]
	v_mfma_f32_16x16x32_bf16 v[60:63], v[132:135], v[184:187], v[60:63]
	v_mfma_f32_16x16x32_bf16 v[56:59], v[140:143], v[184:187], v[56:59]
	v_mfma_f32_16x16x32_bf16 v[44:47], v[132:135], v[198:201], v[44:47]
	v_mfma_f32_16x16x32_bf16 v[40:43], v[140:143], v[198:201], v[40:43]
	v_mfma_f32_16x16x32_bf16 v[28:31], v[132:135], v[206:209], v[28:31]
	v_mfma_f32_16x16x32_bf16 v[24:27], v[140:143], v[206:209], v[24:27]
	v_mfma_f32_16x16x32_bf16 v[12:15], v[132:135], v[214:217], v[12:15]
	v_mfma_f32_16x16x32_bf16 v[8:11], v[140:143], v[214:217], v[8:11]
	s_setprio 0
	s_setprio 1
	v_mfma_f32_16x16x32_bf16 v[52:55], v[144:147], v[180:183], v[52:55]
	v_mfma_f32_16x16x32_bf16 v[48:51], v[172:175], v[180:183], v[48:51]
	v_mfma_f32_16x16x32_bf16 v[36:39], v[144:147], v[194:197], v[36:39]
	v_mfma_f32_16x16x32_bf16 v[32:35], v[172:175], v[194:197], v[32:35]
	v_mfma_f32_16x16x32_bf16 v[20:23], v[144:147], v[202:205], v[20:23]
	v_mfma_f32_16x16x32_bf16 v[16:19], v[172:175], v[202:205], v[16:19]
	v_mfma_f32_16x16x32_bf16 v[4:7], v[144:147], v[210:213], v[4:7]
	v_mfma_f32_16x16x32_bf16 v[0:3], v[172:175], v[210:213], v[0:3]
	v_mfma_f32_16x16x32_bf16 v[52:55], v[148:151], v[184:187], v[52:55]
	v_mfma_f32_16x16x32_bf16 v[48:51], v[176:179], v[184:187], v[48:51]
	v_mfma_f32_16x16x32_bf16 v[36:39], v[148:151], v[198:201], v[36:39]
	v_mfma_f32_16x16x32_bf16 v[32:35], v[176:179], v[198:201], v[32:35]
	v_mfma_f32_16x16x32_bf16 v[20:23], v[148:151], v[206:209], v[20:23]
	v_mfma_f32_16x16x32_bf16 v[16:19], v[176:179], v[206:209], v[16:19]
	v_mfma_f32_16x16x32_bf16 v[4:7], v[148:151], v[214:217], v[4:7]
	v_mfma_f32_16x16x32_bf16 v[0:3], v[176:179], v[214:217], v[0:3]
	s_setprio 0
	s_barrier
; #define PG8_STAGE(bufoff, gbase, voff) do { _Pragma("unroll") for (int _i = 0; _i < 2; ++_i) \
;         __builtin_amdgcn_global_load_lds((const unsigned*)((const char*)(gbase) + (voff)[_i]), (PG8_LAS unsigned*)(lds + (bufoff) + ldsw + _i * 8192), 16, 0, 0); } while (0)
; #define PG8_LDA(dst, b, h) do { _Pragma("unroll") for (int m = 0; m < 4; ++m) _Pragma("unroll") for (int k = 0; k < 2; ++k) dst[m][k] = *(const PG8_LAS bf16x8*)(lds + PG8_SA(b, h) + aoff + m * 2048 + k * 1024); } while (0)
; #define PG8_LDB(dst, b, h) do { _Pragma("unroll") for (int n = 0; n < 2; ++n) _Pragma("unroll") for (int k = 0; k < 2; ++k) dst[n][k] = *(const PG8_LAS bf16x8*)(lds + PG8_SB(b, h) + boff + n * 2048 + k * 1024); } while (0)
; #define PG8_MMA(ai, bj, At, Bt) do { __builtin_amdgcn_s_setprio(1); _Pragma("unroll") for (int m = 0; m < 4; ++m) _Pragma("unroll") for (int n = 0; n < 2; ++n) _Pragma("unroll") for (int k = 0; k < 2; ++k) \
;         acc[ai][bj][m][n] = __builtin_amdgcn_mfma_f32_16x16x32_bf16(Bt[n][k], At[m][k], acc[ai][bj][m][n], 0, 0, 0); __builtin_amdgcn_s_setprio(0); } while (0)
; #define PG8_WAIT_V(n) asm volatile("s_waitcnt vmcnt(" #n ")" ::: "memory")
; #define PG8_WAIT_L(n) asm volatile("s_waitcnt lgkmcnt(" #n ")" ::: "memory")
; #define PG8_BAR __builtin_amdgcn_s_barrier()
; #define PG8_SCHED __builtin_amdgcn_sched_barrier(0)
; template <class Epi, class Sched, bool ALIGN_EPI = false, bool SP2 = false>
; __device__ __forceinline__ void gemm_phase(PG8_LAS unsigned char* lds, const Gemm g, const Sched& S, const Epi& E, const int wid) {
;     ...
;         for (int t = 0; t < nt; t += 2) {
;             const bool last = (t == nt - 2);
;             const char* a1 = cA + (size_t)(t + 1) * kstep;
;             const char* a2 = last ? nA : cA + (size_t)(t + 2) * kstep; const char* b2 = last ? nB : cB + (size_t)(t + 2) * kstep;
;     ...
;             PG8_LDB(B0, 1, 0); PG8_LDB(B1, 1, 1); PG8_SCHED; PG8_LDA(At, 1, 0); PG8_STAGE(PG8_SA(0, 1), a2 + hstepA, voffA);
;             PG8_WAIT_V(8); PG8_WAIT_L(0); PG8_BAR; PG8_MMA(0, 0, At, B0); PG8_MMA(0, 1, At, B1); PG8_BAR; PG8_SCHED;
;             PG8_LDA(At, 1, 1); PG8_STAGE(PG8_SB(1, 0), b3, voffB); PG8_STAGE(PG8_SB(1, 1), b3 + hstepB, voffB); PG8_STAGE(PG8_SA(1, 0), a3, voffA);
;             PG8_WAIT_V(8); PG8_WAIT_L(0); PG8_BAR; PG8_MMA(1, 0, At, B0); PG8_MMA(1, 1, At, B1); PG8_BAR; PG8_SCHED;
	s_add_i32 s71, 0, 0x18000
	s_add_i32 s72, 0, 0x1c000
	v_add_u32_e32 v140, s71, v189
	v_add_u32_e32 v176, s72, v189
	ds_read_b128 v[128:131], v140
	ds_read_b128 v[132:135], v140 offset:1024
	ds_read_b128 v[136:139], v140 offset:2048
	ds_read_b128 v[140:143], v140 offset:3072
	ds_read_b128 v[144:147], v176
	ds_read_b128 v[148:151], v176 offset:1024
	ds_read_b128 v[172:175], v176 offset:2048
	ds_read_b128 v[176:179], v176 offset:3072
	s_add_u32 s36, s36, 0x40000
	s_addc_u32 s37, s37, 0
	s_mov_b32 m0, s44
	ds_read_b128 v[180:183], v192 offset:32768
	ds_read_b128 v[184:187], v192 offset:33792
	ds_read_b128 v[194:197], v192 offset:34816
	ds_read_b128 v[198:201], v192 offset:35840
	ds_read_b128 v[202:205], v192 offset:36864
	ds_read_b128 v[206:209], v192 offset:37888
	ds_read_b128 v[210:213], v192 offset:38912
	ds_read_b128 v[214:217], v192 offset:39936
	global_load_lds_dwordx4 v152, s[36:37]
	s_mov_b32 m0, s45
	s_nop 0
	global_load_lds_dwordx4 v156, s[36:37]
	s_waitcnt vmcnt(8) lgkmcnt(0)
	s_barrier
	s_setprio 1
	v_mfma_f32_16x16x32_bf16 v[124:127], v[128:131], v[180:183], v[124:127]
	v_mfma_f32_16x16x32_bf16 v[120:123], v[136:139], v[180:183], v[120:123]
	v_mfma_f32_16x16x32_bf16 v[108:111], v[128:131], v[194:197], v[108:111]
	v_mfma_f32_16x16x32_bf16 v[104:107], v[136:139], v[194:197], v[104:107]
	v_mfma_f32_16x16x32_bf16 v[92:95], v[128:131], v[202:205], v[92:95]
	v_mfma_f32_16x16x32_bf16 v[88:91], v[136:139], v[202:205], v[88:91]
	v_mfma_f32_16x16x32_bf16 v[76:79], v[128:131], v[210:213], v[76:79]
	v_mfma_f32_16x16x32_bf16 v[72:75], v[136:139], v[210:213], v[72:75]
	v_mfma_f32_16x16x32_bf16 v[124:127], v[132:135], v[184:187], v[124:127]
	v_mfma_f32_16x16x32_bf16 v[120:123], v[140:143], v[184:187], v[120:123]
	v_mfma_f32_16x16x32_bf16 v[108:111], v[132:135], v[198:201], v[108:111]
	v_mfma_f32_16x16x32_bf16 v[104:107], v[140:143], v[198:201], v[104:107]
	v_mfma_f32_16x16x32_bf16 v[92:95], v[132:135], v[206:209], v[92:95]
	v_mfma_f32_16x16x32_bf16 v[88:91], v[140:143], v[206:209], v[88:91]
	v_mfma_f32_16x16x32_bf16 v[76:79], v[132:135], v[214:217], v[76:79]
	v_mfma_f32_16x16x32_bf16 v[72:75], v[140:143], v[214:217], v[72:75]
	s_setprio 0
	s_setprio 1
	v_mfma_f32_16x16x32_bf16 v[116:119], v[144:147], v[180:183], v[116:119]
	v_mfma_f32_16x16x32_bf16 v[112:115], v[172:175], v[180:183], v[112:115]
	v_mfma_f32_16x16x32_bf16 v[100:103], v[144:147], v[194:197], v[100:103]
	v_mfma_f32_16x16x32_bf16 v[96:99], v[172:175], v[194:197], v[96:99]
	v_mfma_f32_16x16x32_bf16 v[84:87], v[144:147], v[202:205], v[84:87]
	v_mfma_f32_16x16x32_bf16 v[80:83], v[172:175], v[202:205], v[80:83]
	v_mfma_f32_16x16x32_bf16 v[68:71], v[144:147], v[210:213], v[68:71]
	v_mfma_f32_16x16x32_bf16 v[64:67], v[172:175], v[210:213], v[64:67]
	v_mfma_f32_16x16x32_bf16 v[116:119], v[148:151], v[184:187], v[116:119]
	v_mfma_f32_16x16x32_bf16 v[112:115], v[176:179], v[184:187], v[112:115]
	v_mfma_f32_16x16x32_bf16 v[100:103], v[148:151], v[198:201], v[100:103]
	v_mfma_f32_16x16x32_bf16 v[96:99], v[176:179], v[198:201], v[96:99]
	v_mfma_f32_16x16x32_bf16 v[84:87], v[148:151], v[206:209], v[84:87]
	v_mfma_f32_16x16x32_bf16 v[80:83], v[176:179], v[206:209], v[80:83]
	v_mfma_f32_16x16x32_bf16 v[68:71], v[148:151], v[214:217], v[68:71]
	v_mfma_f32_16x16x32_bf16 v[64:67], v[176:179], v[214:217], v[64:67]
	s_setprio 0
	s_barrier
	s_add_i32 s36, s71, s39
	v_lshl_add_u64 v[218:219], v[218:219], 0, s[14:15]
	s_mov_b32 m0, s36
	ds_read_b128 v[180:183], v192 offset:49152
	ds_read_b128 v[184:187], v192 offset:50176
	ds_read_b128 v[194:197], v192 offset:51200
	ds_read_b128 v[198:201], v192 offset:52224
	ds_read_b128 v[202:205], v192 offset:53248
	ds_read_b128 v[206:209], v192 offset:54272
	ds_read_b128 v[210:213], v192 offset:55296
	ds_read_b128 v[214:217], v192 offset:56320
	global_load_lds_dwordx4 v[218:219], off
	s_add_i32 m0, s36, 0x2000
	s_add_u32 s34, s34, 0x40080
	v_lshl_add_u64 v[218:219], v[220:221], 0, s[14:15]
	s_addc_u32 s35, s35, 0
	s_add_i32 s36, s72, s39
	global_load_lds_dwordx4 v[218:219], off
	s_mov_b32 m0, s36
	s_nop 0
	global_load_lds_dwordx4 v154, s[34:35]
	v_lshl_add_u64 v[218:219], s[34:35], 0, v[158:159]
	s_add_i32 m0, s36, 0x2000
	s_nop 0
	global_load_lds_dwordx4 v158, s[34:35]
	v_lshl_add_u64 v[218:219], v[222:223], 0, s[14:15]
	s_mov_b32 m0, s47
	s_nop 0
	global_load_lds_dwordx4 v[218:219], off
	v_lshl_add_u64 v[218:219], v[224:225], 0, s[14:15]
	s_mov_b32 m0, s48
	s_nop 0
	global_load_lds_dwordx4 v[218:219], off
	s_waitcnt vmcnt(8) lgkmcnt(0)
	s_barrier
	s_setprio 1
	v_mfma_f32_16x16x32_bf16 v[60:63], v[128:131], v[180:183], v[60:63]
	v_mfma_f32_16x16x32_bf16 v[56:59], v[136:139], v[180:183], v[56:59]
	v_mfma_f32_16x16x32_bf16 v[44:47], v[128:131], v[194:197], v[44:47]
	v_mfma_f32_16x16x32_bf16 v[40:43], v[136:139], v[194:197], v[40:43]
	v_mfma_f32_16x16x32_bf16 v[28:31], v[128:131], v[202:205], v[28:31]
	v_mfma_f32_16x16x32_bf16 v[24:27], v[136:139], v[202:205], v[24:27]
	v_mfma_f32_16x16x32_bf16 v[12:15], v[128:131], v[210:213], v[12:15]
	v_mfma_f32_16x16x32_bf16 v[8:11], v[136:139], v[210:213], v[8:11]
	v_mfma_f32_16x16x32_bf16 v[60:63], v[132:135], v[184:187], v[60:63]
	v_mfma_f32_16x16x32_bf16 v[56:59], v[140:143], v[184:187], v[56:59]
	v_mfma_f32_16x16x32_bf16 v[44:47], v[132:135], v[198:201], v[44:47]
	v_mfma_f32_16x16x32_bf16 v[40:43], v[140:143], v[198:201], v[40:43]
	v_mfma_f32_16x16x32_bf16 v[28:31], v[132:135], v[206:209], v[28:31]
	v_mfma_f32_16x16x32_bf16 v[24:27], v[140:143], v[206:209], v[24:27]
	v_mfma_f32_16x16x32_bf16 v[12:15], v[132:135], v[214:217], v[12:15]
	v_mfma_f32_16x16x32_bf16 v[8:11], v[140:143], v[214:217], v[8:11]
	s_setprio 0
	s_setprio 1
	v_mfma_f32_16x16x32_bf16 v[52:55], v[144:147], v[180:183], v[52:55]
	v_mfma_f32_16x16x32_bf16 v[48:51], v[172:175], v[180:183], v[48:51]
	v_mfma_f32_16x16x32_bf16 v[36:39], v[144:147], v[194:197], v[36:39]
	v_mfma_f32_16x16x32_bf16 v[32:35], v[172:175], v[194:197], v[32:35]
	v_mfma_f32_16x16x32_bf16 v[20:23], v[144:147], v[202:205], v[20:23]
	v_mfma_f32_16x16x32_bf16 v[16:19], v[172:175], v[202:205], v[16:19]
	v_mfma_f32_16x16x32_bf16 v[4:7], v[144:147], v[210:213], v[4:7]
	v_mfma_f32_16x16x32_bf16 v[0:3], v[172:175], v[210:213], v[0:3]
	v_mfma_f32_16x16x32_bf16 v[52:55], v[148:151], v[184:187], v[52:55]
	v_mfma_f32_16x16x32_bf16 v[48:51], v[176:179], v[184:187], v[48:51]
	v_mfma_f32_16x16x32_bf16 v[36:39], v[148:151], v[198:201], v[36:39]
	v_mfma_f32_16x16x32_bf16 v[32:35], v[176:179], v[198:201], v[32:35]
	v_mfma_f32_16x16x32_bf16 v[20:23], v[148:151], v[206:209], v[20:23]
	v_mfma_f32_16x16x32_bf16 v[16:19], v[176:179], v[206:209], v[16:19]
	v_mfma_f32_16x16x32_bf16 v[4:7], v[148:151], v[214:217], v[4:7]
	v_mfma_f32_16x16x32_bf16 v[0:3], v[176:179], v[214:217], v[0:3]
	s_setprio 0
	s_barrier
	s_add_i32 s70, s70, 2
	s_add_u32 s30, s30, 0x100
	s_addc_u32 s31, s31, 0
	s_add_u32 s68, s68, 0x100
	s_addc_u32 s69, s69, 0
	s_cmp_gt_u32 s70, 13
	s_cbranch_scc0 .LBB0_1780
	s_and_b64 vcc, exec, s[16:17]
	s_cbranch_vccz .LBB0_1783
	s_barrier

; #define PG8_STAGE(bufoff, gbase, voff) do { _Pragma("unroll") for (int _i = 0; _i < 2; ++_i) \
;         __builtin_amdgcn_global_load_lds((const unsigned*)((const char*)(gbase) + (voff)[_i]), (PG8_LAS unsigned*)(lds + (bufoff) + ldsw + _i * 8192), 16, 0, 0); } while (0)
; #define PG8_LDA(dst, b, h) do { _Pragma("unroll") for (int m = 0; m < 4; ++m) _Pragma("unroll") for (int k = 0; k < 2; ++k) dst[m][k] = *(const PG8_LAS bf16x8*)(lds + PG8_SA(b, h) + aoff + m * 2048 + k * 1024); } while (0)
; #define PG8_LDB(dst, b, h) do { _Pragma("unroll") for (int n = 0; n < 2; ++n) _Pragma("unroll") for (int k = 0; k < 2; ++k) dst[n][k] = *(const PG8_LAS bf16x8*)(lds + PG8_SB(b, h) + boff + n * 2048 + k * 1024); } while (0)
; #define PG8_MMA(ai, bj, At, Bt) do { __builtin_amdgcn_s_setprio(1); _Pragma("unroll") for (int m = 0; m < 4; ++m) _Pragma("unroll") for (int n = 0; n < 2; ++n) _Pragma("unroll") for (int k = 0; k < 2; ++k) \
;         acc[ai][bj][m][n] = __builtin_amdgcn_mfma_f32_16x16x32_bf16(Bt[n][k], At[m][k], acc[ai][bj][m][n], 0, 0, 0); __builtin_amdgcn_s_setprio(0); } while (0)
; #define PG8_WAIT_V(n) asm volatile("s_waitcnt vmcnt(" #n ")" ::: "memory")
; #define PG8_BAR __builtin_amdgcn_s_barrier()
; template <class Epi, class Sched, bool ALIGN_EPI = false, bool SP2 = false>
; __device__ __forceinline__ void gemm_phase(PG8_LAS unsigned char* lds, const Gemm g, const Sched& S, const Epi& E, const int wid) {
;     ...
;         for (int t = 0; t < nt; t += 2) {
;             const bool last = (t == nt - 2);
;             const char* a1 = cA + (size_t)(t + 1) * kstep;
;             const char* a2 = last ? nA : cA + (size_t)(t + 2) * kstep; const char* b2 = last ? nB : cB + (size_t)(t + 2) * kstep;
;             const char* a3 = a2 + kstep; const char* b3 = b2 + kstep;
;             if (last && has_next) S.a_ready(nxt);
;             if constexpr (SP2) {
;             PG8_LDB(B0, 0, 0); PG8_LDB(B1, 0, 1); PG8_SCHED; PG8_LDA(At, 0, 0); PG8_STAGE(PG8_SA(1, 1), a1 + hstepA, voffA);
;             PG8_WAIT_V(8); PG8_WAIT_L(0); PG8_BAR; PG8_MMA(0, 0, At, B0); PG8_MMA(0, 1, At, B1); PG8_BAR; PG8_SCHED;
;             PG8_LDA(At, 0, 1); PG8_STAGE(PG8_SB(0, 0), b2, voffB); PG8_STAGE(PG8_SB(0, 1), b2 + hstepB, voffB); PG8_STAGE(PG8_SA(0, 0), a2, voffA);
;             PG8_WAIT_V(8); PG8_WAIT_L(0); PG8_BAR; PG8_MMA(1, 0, At, B0); PG8_MMA(1, 1, At, B1); PG8_BAR; PG8_SCHED;
.LBB0_1867:
	ds_read_b128 v[148:151], v166
	ds_read_b128 v[152:155], v166 offset:1024
	ds_read_b128 v[156:159], v166 offset:2048
	ds_read_b128 v[160:163], v166 offset:3072
	ds_read_b128 v[172:175], v167
	ds_read_b128 v[176:179], v167 offset:1024
	ds_read_b128 v[180:183], v167 offset:2048
	ds_read_b128 v[184:187], v167 offset:3072
	s_add_u32 s26, s24, 0xfffc0080
	s_addc_u32 s27, s25, -1
	s_cmp_eq_u32 s67, 12
	s_cselect_b32 s29, s17, s27
	s_cselect_b32 s28, s49, s26
	s_cselect_b32 s27, s15, s66
	s_cselect_b32 s26, s64, s65
	s_add_i32 m0, s36, 0xc000
	ds_read_b128 v[188:191], v168
	ds_read_b128 v[192:195], v168 offset:1024
	ds_read_b128 v[196:199], v168 offset:2048
	ds_read_b128 v[200:203], v168 offset:3072
	ds_read_b128 v[204:207], v168 offset:4096
	ds_read_b128 v[208:211], v168 offset:5120
	ds_read_b128 v[212:215], v168 offset:6144
	ds_read_b128 v[216:219], v168 offset:7168
	global_load_lds_dwordx4 v140, s[24:25]
	s_add_i32 m0, s36, 0xe000
	s_nop 0
	global_load_lds_dwordx4 v142, s[24:25]
	s_waitcnt vmcnt(8) lgkmcnt(0)
	s_barrier
	s_setprio 1
	v_mfma_f32_16x16x32_bf16 v[124:127], v[148:151], v[188:191], v[124:127]
	v_mfma_f32_16x16x32_bf16 v[116:119], v[156:159], v[188:191], v[116:119]
	v_mfma_f32_16x16x32_bf16 v[108:111], v[148:151], v[196:199], v[108:111]
	v_mfma_f32_16x16x32_bf16 v[100:103], v[156:159], v[196:199], v[100:103]
	v_mfma_f32_16x16x32_bf16 v[92:95], v[148:151], v[204:207], v[92:95]
	v_mfma_f32_16x16x32_bf16 v[84:87], v[156:159], v[204:207], v[84:87]
	v_mfma_f32_16x16x32_bf16 v[76:79], v[148:151], v[212:215], v[76:79]
	v_mfma_f32_16x16x32_bf16 v[68:71], v[156:159], v[212:215], v[68:71]
	v_mfma_f32_16x16x32_bf16 v[124:127], v[152:155], v[192:195], v[124:127]
	v_mfma_f32_16x16x32_bf16 v[116:119], v[160:163], v[192:195], v[116:119]
	v_mfma_f32_16x16x32_bf16 v[108:111], v[152:155], v[200:203], v[108:111]
	v_mfma_f32_16x16x32_bf16 v[100:103], v[160:163], v[200:203], v[100:103]
	v_mfma_f32_16x16x32_bf16 v[92:95], v[152:155], v[208:211], v[92:95]
	v_mfma_f32_16x16x32_bf16 v[84:87], v[160:163], v[208:211], v[84:87]
	v_mfma_f32_16x16x32_bf16 v[76:79], v[152:155], v[216:219], v[76:79]
	v_mfma_f32_16x16x32_bf16 v[68:71], v[160:163], v[216:219], v[68:71]
	s_setprio 0
	s_setprio 1
	v_mfma_f32_16x16x32_bf16 v[120:123], v[172:175], v[188:191], v[120:123]
	v_mfma_f32_16x16x32_bf16 v[112:115], v[180:183], v[188:191], v[112:115]
	v_mfma_f32_16x16x32_bf16 v[104:107], v[172:175], v[196:199], v[104:107]
	v_mfma_f32_16x16x32_bf16 v[96:99], v[180:183], v[196:199], v[96:99]
	v_mfma_f32_16x16x32_bf16 v[88:91], v[172:175], v[204:207], v[88:91]
	v_mfma_f32_16x16x32_bf16 v[80:83], v[180:183], v[204:207], v[80:83]
	v_mfma_f32_16x16x32_bf16 v[72:75], v[172:175], v[212:215], v[72:75]
	v_mfma_f32_16x16x32_bf16 v[64:67], v[180:183], v[212:215], v[64:67]
	v_mfma_f32_16x16x32_bf16 v[120:123], v[176:179], v[192:195], v[120:123]
	v_mfma_f32_16x16x32_bf16 v[112:115], v[184:187], v[192:195], v[112:115]
	v_mfma_f32_16x16x32_bf16 v[104:107], v[176:179], v[200:203], v[104:107]
	v_mfma_f32_16x16x32_bf16 v[96:99], v[184:187], v[200:203], v[96:99]
	v_mfma_f32_16x16x32_bf16 v[88:91], v[176:179], v[208:211], v[88:91]
	v_mfma_f32_16x16x32_bf16 v[80:83], v[184:187], v[208:211], v[80:83]
	v_mfma_f32_16x16x32_bf16 v[72:75], v[176:179], v[216:219], v[72:75]
	v_mfma_f32_16x16x32_bf16 v[64:67], v[184:187], v[216:219], v[64:67]
	s_setprio 0
	s_barrier
	s_add_i32 s68, s45, s33
	v_lshl_add_u64 v[220:221], s[26:27], 0, v[132:133]
	s_mov_b32 m0, s68
	ds_read_b128 v[188:191], v168 offset:16384
	ds_read_b128 v[192:195], v168 offset:17408
	ds_read_b128 v[196:199], v168 offset:18432
	ds_read_b128 v[200:203], v168 offset:19456
	ds_read_b128 v[204:207], v168 offset:20480
	ds_read_b128 v[208:211], v168 offset:21504
	ds_read_b128 v[212:215], v168 offset:22528
	ds_read_b128 v[216:219], v168 offset:23552
	global_load_lds_dwordx4 v132, s[26:27]
	s_add_i32 m0, s68, 0x2000
	s_add_u32 s68, s26, 0x40000
	v_lshl_add_u64 v[222:223], s[26:27], 0, v[128:129]
	s_addc_u32 s69, s27, 0
	s_add_i32 s70, s46, s33
	global_load_lds_dwordx4 v128, s[26:27]
	s_mov_b32 m0, s70
	v_lshl_add_u64 v[226:227], s[28:29], 0, v[130:131]
	global_load_lds_dwordx4 v132, s[68:69]
	s_add_i32 m0, s70, 0x2000
	s_nop 0
	global_load_lds_dwordx4 v128, s[68:69]
	v_lshl_add_u64 v[224:225], s[28:29], 0, v[134:135]
	s_mov_b32 m0, s36
	s_nop 0
	global_load_lds_dwordx4 v134, s[28:29]
	s_mov_b32 m0, s37
	s_nop 0
	global_load_lds_dwordx4 v130, s[28:29]
	s_waitcnt vmcnt(8) lgkmcnt(0)
	s_barrier
	s_setprio 1
	v_mfma_f32_16x16x32_bf16 v[60:63], v[148:151], v[188:191], v[60:63]
	v_mfma_f32_16x16x32_bf16 v[52:55], v[156:159], v[188:191], v[52:55]
	v_mfma_f32_16x16x32_bf16 v[44:47], v[148:151], v[196:199], v[44:47]
	v_mfma_f32_16x16x32_bf16 v[36:39], v[156:159], v[196:199], v[36:39]
	v_mfma_f32_16x16x32_bf16 v[28:31], v[148:151], v[204:207], v[28:31]
	v_mfma_f32_16x16x32_bf16 v[20:23], v[156:159], v[204:207], v[20:23]
	v_mfma_f32_16x16x32_bf16 v[12:15], v[148:151], v[212:215], v[12:15]
	v_mfma_f32_16x16x32_bf16 v[4:7], v[156:159], v[212:215], v[4:7]
	v_mfma_f32_16x16x32_bf16 v[60:63], v[152:155], v[192:195], v[60:63]
	v_mfma_f32_16x16x32_bf16 v[52:55], v[160:163], v[192:195], v[52:55]
	v_mfma_f32_16x16x32_bf16 v[44:47], v[152:155], v[200:203], v[44:47]
	v_mfma_f32_16x16x32_bf16 v[36:39], v[160:163], v[200:203], v[36:39]
	v_mfma_f32_16x16x32_bf16 v[28:31], v[152:155], v[208:211], v[28:31]
	v_mfma_f32_16x16x32_bf16 v[20:23], v[160:163], v[208:211], v[20:23]
	v_mfma_f32_16x16x32_bf16 v[12:15], v[152:155], v[216:219], v[12:15]
	v_mfma_f32_16x16x32_bf16 v[4:7], v[160:163], v[216:219], v[4:7]
	s_setprio 0
	s_setprio 1
	v_mfma_f32_16x16x32_bf16 v[56:59], v[172:175], v[188:191], v[56:59]
	v_mfma_f32_16x16x32_bf16 v[48:51], v[180:183], v[188:191], v[48:51]
	v_mfma_f32_16x16x32_bf16 v[40:43], v[172:175], v[196:199], v[40:43]
	v_mfma_f32_16x16x32_bf16 v[32:35], v[180:183], v[196:199], v[32:35]
	v_mfma_f32_16x16x32_bf16 v[24:27], v[172:175], v[204:207], v[24:27]
	v_mfma_f32_16x16x32_bf16 v[16:19], v[180:183], v[204:207], v[16:19]
	v_mfma_f32_16x16x32_bf16 v[8:11], v[172:175], v[212:215], v[8:11]
	v_mfma_f32_16x16x32_bf16 v[0:3], v[180:183], v[212:215], v[0:3]
	v_mfma_f32_16x16x32_bf16 v[56:59], v[176:179], v[192:195], v[56:59]
	v_mfma_f32_16x16x32_bf16 v[48:51], v[184:187], v[192:195], v[48:51]
	v_mfma_f32_16x16x32_bf16 v[40:43], v[176:179], v[200:203], v[40:43]
	v_mfma_f32_16x16x32_bf16 v[32:35], v[184:187], v[200:203], v[32:35]
	v_mfma_f32_16x16x32_bf16 v[24:27], v[176:179], v[208:211], v[24:27]
	v_mfma_f32_16x16x32_bf16 v[16:19], v[184:187], v[208:211], v[16:19]
	v_mfma_f32_16x16x32_bf16 v[8:11], v[176:179], v[216:219], v[8:11]
	v_mfma_f32_16x16x32_bf16 v[0:3], v[184:187], v[216:219], v[0:3]
	s_setprio 0
	s_barrier
; #define PG8_STAGE(bufoff, gbase, voff) do { _Pragma("unroll") for (int _i = 0; _i < 2; ++_i) \
;         __builtin_amdgcn_global_load_lds((const unsigned*)((const char*)(gbase) + (voff)[_i]), (PG8_LAS unsigned*)(lds + (bufoff) + ldsw + _i * 8192), 16, 0, 0); } while (0)
; #define PG8_LDA(dst, b, h) do { _Pragma("unroll") for (int m = 0; m < 4; ++m) _Pragma("unroll") for (int k = 0; k < 2; ++k) dst[m][k] = *(const PG8_LAS bf16x8*)(lds + PG8_SA(b, h) + aoff + m * 2048 + k * 1024); } while (0)
; #define PG8_LDB(dst, b, h) do { _Pragma("unroll") for (int n = 0; n < 2; ++n) _Pragma("unroll") for (int k = 0; k < 2; ++k) dst[n][k] = *(const PG8_LAS bf16x8*)(lds + PG8_SB(b, h) + boff + n * 2048 + k * 1024); } while (0)
; #define PG8_MMA(ai, bj, At, Bt) do { __builtin_amdgcn_s_setprio(1); _Pragma("unroll") for (int m = 0; m < 4; ++m) _Pragma("unroll") for (int n = 0; n < 2; ++n) _Pragma("unroll") for (int k = 0; k < 2; ++k) \
;         acc[ai][bj][m][n] = __builtin_amdgcn_mfma_f32_16x16x32_bf16(Bt[n][k], At[m][k], acc[ai][bj][m][n], 0, 0, 0); __builtin_amdgcn_s_setprio(0); } while (0)
; #define PG8_WAIT_V(n) asm volatile("s_waitcnt vmcnt(" #n ")" ::: "memory")
; #define PG8_WAIT_L(n) asm volatile("s_waitcnt lgkmcnt(" #n ")" ::: "memory")
; #define PG8_BAR __builtin_amdgcn_s_barrier()
; #define PG8_SCHED __builtin_amdgcn_sched_barrier(0)
; template <class Epi, class Sched, bool ALIGN_EPI = false, bool SP2 = false>
; __device__ __forceinline__ void gemm_phase(PG8_LAS unsigned char* lds, const Gemm g, const Sched& S, const Epi& E, const int wid) {
;     ...
;         for (int t = 0; t < nt; t += 2) {
;             const bool last = (t == nt - 2);
;             const char* a1 = cA + (size_t)(t + 1) * kstep;
;             const char* a2 = last ? nA : cA + (size_t)(t + 2) * kstep; const char* b2 = last ? nB : cB + (size_t)(t + 2) * kstep;
;     ...
;             PG8_LDB(B0, 1, 0); PG8_LDB(B1, 1, 1); PG8_SCHED; PG8_LDA(At, 1, 0); PG8_STAGE(PG8_SA(0, 1), a2 + hstepA, voffA);
;             PG8_WAIT_V(8); PG8_WAIT_L(0); PG8_BAR; PG8_MMA(0, 0, At, B0); PG8_MMA(0, 1, At, B1); PG8_BAR; PG8_SCHED;
;             PG8_LDA(At, 1, 1); PG8_STAGE(PG8_SB(1, 0), b3, voffB); PG8_STAGE(PG8_SB(1, 1), b3 + hstepB, voffB); PG8_STAGE(PG8_SA(1, 0), a3, voffA);
;             PG8_WAIT_V(8); PG8_WAIT_L(0); PG8_BAR; PG8_MMA(1, 0, At, B0); PG8_MMA(1, 1, At, B1); PG8_BAR; PG8_SCHED;
	s_add_i32 s68, 0, 0x18000
	s_add_i32 s69, 0, 0x1c000
	v_add_u32_e32 v160, s68, v165
	v_add_u32_e32 v171, s69, v165
	ds_read_b128 v[148:151], v160
	ds_read_b128 v[152:155], v160 offset:1024
	ds_read_b128 v[156:159], v160 offset:2048
	ds_read_b128 v[160:163], v160 offset:3072
	ds_read_b128 v[172:175], v171
	ds_read_b128 v[176:179], v171 offset:1024
	ds_read_b128 v[180:183], v171 offset:2048
	ds_read_b128 v[184:187], v171 offset:3072
	s_add_u32 s28, s28, 0x40000
	s_addc_u32 s29, s29, 0
	s_mov_b32 m0, s38
	ds_read_b128 v[188:191], v168 offset:32768
	ds_read_b128 v[192:195], v168 offset:33792
	ds_read_b128 v[196:199], v168 offset:34816
	ds_read_b128 v[200:203], v168 offset:35840
	ds_read_b128 v[204:207], v168 offset:36864
	ds_read_b128 v[208:211], v168 offset:37888
	ds_read_b128 v[212:215], v168 offset:38912
	ds_read_b128 v[216:219], v168 offset:39936
	global_load_lds_dwordx4 v134, s[28:29]
	s_mov_b32 m0, s39
	s_nop 0
	global_load_lds_dwordx4 v130, s[28:29]
	s_waitcnt vmcnt(8) lgkmcnt(0)
	s_barrier
	s_setprio 1
	v_mfma_f32_16x16x32_bf16 v[124:127], v[148:151], v[188:191], v[124:127]
	v_mfma_f32_16x16x32_bf16 v[116:119], v[156:159], v[188:191], v[116:119]
	v_mfma_f32_16x16x32_bf16 v[108:111], v[148:151], v[196:199], v[108:111]
	v_mfma_f32_16x16x32_bf16 v[100:103], v[156:159], v[196:199], v[100:103]
	v_mfma_f32_16x16x32_bf16 v[92:95], v[148:151], v[204:207], v[92:95]
	v_mfma_f32_16x16x32_bf16 v[84:87], v[156:159], v[204:207], v[84:87]
	v_mfma_f32_16x16x32_bf16 v[76:79], v[148:151], v[212:215], v[76:79]
	v_mfma_f32_16x16x32_bf16 v[68:71], v[156:159], v[212:215], v[68:71]
	v_mfma_f32_16x16x32_bf16 v[124:127], v[152:155], v[192:195], v[124:127]
	v_mfma_f32_16x16x32_bf16 v[116:119], v[160:163], v[192:195], v[116:119]
	v_mfma_f32_16x16x32_bf16 v[108:111], v[152:155], v[200:203], v[108:111]
	v_mfma_f32_16x16x32_bf16 v[100:103], v[160:163], v[200:203], v[100:103]
	v_mfma_f32_16x16x32_bf16 v[92:95], v[152:155], v[208:211], v[92:95]
	v_mfma_f32_16x16x32_bf16 v[84:87], v[160:163], v[208:211], v[84:87]
	v_mfma_f32_16x16x32_bf16 v[76:79], v[152:155], v[216:219], v[76:79]
	v_mfma_f32_16x16x32_bf16 v[68:71], v[160:163], v[216:219], v[68:71]
	s_setprio 0
	s_setprio 1
	v_mfma_f32_16x16x32_bf16 v[120:123], v[172:175], v[188:191], v[120:123]
	v_mfma_f32_16x16x32_bf16 v[112:115], v[180:183], v[188:191], v[112:115]
	v_mfma_f32_16x16x32_bf16 v[104:107], v[172:175], v[196:199], v[104:107]
	v_mfma_f32_16x16x32_bf16 v[96:99], v[180:183], v[196:199], v[96:99]
	v_mfma_f32_16x16x32_bf16 v[88:91], v[172:175], v[204:207], v[88:91]
	v_mfma_f32_16x16x32_bf16 v[80:83], v[180:183], v[204:207], v[80:83]
	v_mfma_f32_16x16x32_bf16 v[72:75], v[172:175], v[212:215], v[72:75]
	v_mfma_f32_16x16x32_bf16 v[64:67], v[180:183], v[212:215], v[64:67]
	v_mfma_f32_16x16x32_bf16 v[120:123], v[176:179], v[192:195], v[120:123]
	v_mfma_f32_16x16x32_bf16 v[112:115], v[184:187], v[192:195], v[112:115]
	v_mfma_f32_16x16x32_bf16 v[104:107], v[176:179], v[200:203], v[104:107]
	v_mfma_f32_16x16x32_bf16 v[96:99], v[184:187], v[200:203], v[96:99]
	v_mfma_f32_16x16x32_bf16 v[88:91], v[176:179], v[208:211], v[88:91]
	v_mfma_f32_16x16x32_bf16 v[80:83], v[184:187], v[208:211], v[80:83]
	v_mfma_f32_16x16x32_bf16 v[72:75], v[176:179], v[216:219], v[72:75]
	v_mfma_f32_16x16x32_bf16 v[64:67], v[184:187], v[216:219], v[64:67]
	s_setprio 0
	s_barrier
	s_add_i32 s28, s68, s33
	v_lshl_add_u64 v[220:221], v[220:221], 0, s[10:11]
	s_mov_b32 m0, s28
	ds_read_b128 v[188:191], v168 offset:49152
	ds_read_b128 v[192:195], v168 offset:50176
	ds_read_b128 v[196:199], v168 offset:51200
	ds_read_b128 v[200:203], v168 offset:52224
	ds_read_b128 v[204:207], v168 offset:53248
	ds_read_b128 v[208:211], v168 offset:54272
	ds_read_b128 v[212:215], v168 offset:55296
	ds_read_b128 v[216:219], v168 offset:56320
	global_load_lds_dwordx4 v[220:221], off
	s_add_i32 m0, s28, 0x2000
	s_add_u32 s26, s26, 0x40080
	v_lshl_add_u64 v[220:221], v[222:223], 0, s[10:11]
	s_addc_u32 s27, s27, 0
	s_add_i32 s28, s69, s33
	global_load_lds_dwordx4 v[220:221], off
	s_mov_b32 m0, s28
	s_nop 0
	global_load_lds_dwordx4 v132, s[26:27]
	v_lshl_add_u64 v[220:221], s[26:27], 0, v[128:129]
	s_add_i32 m0, s28, 0x2000
	s_nop 0
	global_load_lds_dwordx4 v128, s[26:27]
	v_lshl_add_u64 v[220:221], v[224:225], 0, s[10:11]
	s_mov_b32 m0, s40
	s_nop 0
	global_load_lds_dwordx4 v[220:221], off
	v_lshl_add_u64 v[220:221], v[226:227], 0, s[10:11]
	s_mov_b32 m0, s41
	s_nop 0
	global_load_lds_dwordx4 v[220:221], off
	s_waitcnt vmcnt(8) lgkmcnt(0)
	s_barrier
	s_setprio 1
	v_mfma_f32_16x16x32_bf16 v[60:63], v[148:151], v[188:191], v[60:63]
	v_mfma_f32_16x16x32_bf16 v[52:55], v[156:159], v[188:191], v[52:55]
	v_mfma_f32_16x16x32_bf16 v[44:47], v[148:151], v[196:199], v[44:47]
	v_mfma_f32_16x16x32_bf16 v[36:39], v[156:159], v[196:199], v[36:39]
	v_mfma_f32_16x16x32_bf16 v[28:31], v[148:151], v[204:207], v[28:31]
	v_mfma_f32_16x16x32_bf16 v[20:23], v[156:159], v[204:207], v[20:23]
	v_mfma_f32_16x16x32_bf16 v[12:15], v[148:151], v[212:215], v[12:15]
	v_mfma_f32_16x16x32_bf16 v[4:7], v[156:159], v[212:215], v[4:7]
	v_mfma_f32_16x16x32_bf16 v[60:63], v[152:155], v[192:195], v[60:63]
	v_mfma_f32_16x16x32_bf16 v[52:55], v[160:163], v[192:195], v[52:55]
	v_mfma_f32_16x16x32_bf16 v[44:47], v[152:155], v[200:203], v[44:47]
	v_mfma_f32_16x16x32_bf16 v[36:39], v[160:163], v[200:203], v[36:39]
	v_mfma_f32_16x16x32_bf16 v[28:31], v[152:155], v[208:211], v[28:31]
	v_mfma_f32_16x16x32_bf16 v[20:23], v[160:163], v[208:211], v[20:23]
	v_mfma_f32_16x16x32_bf16 v[12:15], v[152:155], v[216:219], v[12:15]
	v_mfma_f32_16x16x32_bf16 v[4:7], v[160:163], v[216:219], v[4:7]
	s_setprio 0
	s_setprio 1
	v_mfma_f32_16x16x32_bf16 v[56:59], v[172:175], v[188:191], v[56:59]
	v_mfma_f32_16x16x32_bf16 v[48:51], v[180:183], v[188:191], v[48:51]
	v_mfma_f32_16x16x32_bf16 v[40:43], v[172:175], v[196:199], v[40:43]
	v_mfma_f32_16x16x32_bf16 v[32:35], v[180:183], v[196:199], v[32:35]
	v_mfma_f32_16x16x32_bf16 v[24:27], v[172:175], v[204:207], v[24:27]
	v_mfma_f32_16x16x32_bf16 v[16:19], v[180:183], v[204:207], v[16:19]
	v_mfma_f32_16x16x32_bf16 v[8:11], v[172:175], v[212:215], v[8:11]
	v_mfma_f32_16x16x32_bf16 v[0:3], v[180:183], v[212:215], v[0:3]
	v_mfma_f32_16x16x32_bf16 v[56:59], v[176:179], v[192:195], v[56:59]
	v_mfma_f32_16x16x32_bf16 v[48:51], v[184:187], v[192:195], v[48:51]
	v_mfma_f32_16x16x32_bf16 v[40:43], v[176:179], v[200:203], v[40:43]
	v_mfma_f32_16x16x32_bf16 v[32:35], v[184:187], v[200:203], v[32:35]
	v_mfma_f32_16x16x32_bf16 v[24:27], v[176:179], v[208:211], v[24:27]
	v_mfma_f32_16x16x32_bf16 v[16:19], v[184:187], v[208:211], v[16:19]
	v_mfma_f32_16x16x32_bf16 v[8:11], v[176:179], v[216:219], v[8:11]
	v_mfma_f32_16x16x32_bf16 v[0:3], v[184:187], v[216:219], v[0:3]
	s_setprio 0
	s_barrier
	s_add_i32 s67, s67, 2
	s_add_u32 s24, s24, 0x100
	s_addc_u32 s25, s25, 0
	s_add_u32 s65, s65, 0x100
	s_addc_u32 s66, s66, 0
	s_cmp_gt_u32 s67, 13
	s_cbranch_scc0 .LBB0_1867
	s_and_b64 vcc, exec, s[12:13]
	s_cbranch_vccz .LBB0_1870
	s_barrier

; #define PG8_STAGE(bufoff, gbase, voff) do { _Pragma("unroll") for (int _i = 0; _i < 2; ++_i) \
;         __builtin_amdgcn_global_load_lds((const unsigned*)((const char*)(gbase) + (voff)[_i]), (PG8_LAS unsigned*)(lds + (bufoff) + ldsw + _i * 8192), 16, 0, 0); } while (0)
; #define PG8_LDA(dst, b, h) do { _Pragma("unroll") for (int m = 0; m < 4; ++m) _Pragma("unroll") for (int k = 0; k < 2; ++k) dst[m][k] = *(const PG8_LAS bf16x8*)(lds + PG8_SA(b, h) + aoff + m * 2048 + k * 1024); } while (0)
; #define PG8_LDB(dst, b, h) do { _Pragma("unroll") for (int n = 0; n < 2; ++n) _Pragma("unroll") for (int k = 0; k < 2; ++k) dst[n][k] = *(const PG8_LAS bf16x8*)(lds + PG8_SB(b, h) + boff + n * 2048 + k * 1024); } while (0)
; #define PG8_MMA(ai, bj, At, Bt) do { __builtin_amdgcn_s_setprio(1); _Pragma("unroll") for (int m = 0; m < 4; ++m) _Pragma("unroll") for (int n = 0; n < 2; ++n) _Pragma("unroll") for (int k = 0; k < 2; ++k) \
;         acc[ai][bj][m][n] = __builtin_amdgcn_mfma_f32_16x16x32_bf16(Bt[n][k], At[m][k], acc[ai][bj][m][n], 0, 0, 0); __builtin_amdgcn_s_setprio(0); } while (0)
; #define PG8_WAIT_V(n) asm volatile("s_waitcnt vmcnt(" #n ")" ::: "memory")
; #define PG8_BAR __builtin_amdgcn_s_barrier()
; template <class Epi, class Sched, bool ALIGN_EPI = false, bool SP2 = false>
; __device__ __forceinline__ void gemm_phase(PG8_LAS unsigned char* lds, const Gemm g, const Sched& S, const Epi& E, const int wid) {
;     ...
;         for (int t = 0; t < nt; t += 2) {
;             const bool last = (t == nt - 2);
;             const char* a1 = cA + (size_t)(t + 1) * kstep;
;             const char* a2 = last ? nA : cA + (size_t)(t + 2) * kstep; const char* b2 = last ? nB : cB + (size_t)(t + 2) * kstep;
;             const char* a3 = a2 + kstep; const char* b3 = b2 + kstep;
;             if (last && has_next) S.a_ready(nxt);
;             if constexpr (SP2) {
;             PG8_LDB(B0, 0, 0); PG8_LDB(B1, 0, 1); PG8_SCHED; PG8_LDA(At, 0, 0); PG8_STAGE(PG8_SA(1, 1), a1 + hstepA, voffA);
;             PG8_WAIT_V(8); PG8_WAIT_L(0); PG8_BAR; PG8_MMA(0, 0, At, B0); PG8_MMA(0, 1, At, B1); PG8_BAR; PG8_SCHED;
;             PG8_LDA(At, 0, 1); PG8_STAGE(PG8_SB(0, 0), b2, voffB); PG8_STAGE(PG8_SB(0, 1), b2 + hstepB, voffB); PG8_STAGE(PG8_SA(0, 0), a2, voffA);
;             PG8_WAIT_V(8); PG8_WAIT_L(0); PG8_BAR; PG8_MMA(1, 0, At, B0); PG8_MMA(1, 1, At, B1); PG8_BAR; PG8_SCHED;
.LBB0_1952:
	ds_read_b128 v[128:131], v190
	ds_read_b128 v[132:135], v190 offset:1024
	ds_read_b128 v[136:139], v190 offset:2048
	ds_read_b128 v[140:143], v190 offset:3072
	ds_read_b128 v[144:147], v191
	ds_read_b128 v[148:151], v191 offset:1024
	ds_read_b128 v[172:175], v191 offset:2048
	ds_read_b128 v[176:179], v191 offset:3072
	s_add_u32 s24, s22, 0x100
	s_addc_u32 s25, s23, 0
	s_cmp_eq_u32 s68, 40
	s_cselect_b32 s29, s7, s25
	s_cselect_b32 s28, s6, s24
	s_cselect_b32 s27, s21, s67
	s_cselect_b32 s26, s20, s66
	s_add_i32 m0, s34, 0xc000
	ds_read_b128 v[180:183], v192
	ds_read_b128 v[184:187], v192 offset:1024
	ds_read_b128 v[194:197], v192 offset:2048
	ds_read_b128 v[198:201], v192 offset:3072
	ds_read_b128 v[202:205], v192 offset:4096
	ds_read_b128 v[206:209], v192 offset:5120
	ds_read_b128 v[210:213], v192 offset:6144
	ds_read_b128 v[214:217], v192 offset:7168
	global_load_lds_dwordx4 v164, s[22:23]
	s_add_i32 m0, s34, 0xe000
	s_nop 0
	global_load_lds_dwordx4 v166, s[22:23]
	s_waitcnt vmcnt(8) lgkmcnt(0)
	s_barrier
	s_setprio 1
	v_mfma_f32_16x16x32_bf16 v[124:127], v[128:131], v[180:183], v[124:127]
	v_mfma_f32_16x16x32_bf16 v[120:123], v[136:139], v[180:183], v[120:123]
	v_mfma_f32_16x16x32_bf16 v[108:111], v[128:131], v[194:197], v[108:111]
	v_mfma_f32_16x16x32_bf16 v[104:107], v[136:139], v[194:197], v[104:107]
	v_mfma_f32_16x16x32_bf16 v[92:95], v[128:131], v[202:205], v[92:95]
	v_mfma_f32_16x16x32_bf16 v[88:91], v[136:139], v[202:205], v[88:91]
	v_mfma_f32_16x16x32_bf16 v[76:79], v[128:131], v[210:213], v[76:79]
	v_mfma_f32_16x16x32_bf16 v[72:75], v[136:139], v[210:213], v[72:75]
	v_mfma_f32_16x16x32_bf16 v[124:127], v[132:135], v[184:187], v[124:127]
	v_mfma_f32_16x16x32_bf16 v[120:123], v[140:143], v[184:187], v[120:123]
	v_mfma_f32_16x16x32_bf16 v[108:111], v[132:135], v[198:201], v[108:111]
	v_mfma_f32_16x16x32_bf16 v[104:107], v[140:143], v[198:201], v[104:107]
	v_mfma_f32_16x16x32_bf16 v[92:95], v[132:135], v[206:209], v[92:95]
	v_mfma_f32_16x16x32_bf16 v[88:91], v[140:143], v[206:209], v[88:91]
	v_mfma_f32_16x16x32_bf16 v[76:79], v[132:135], v[214:217], v[76:79]
	v_mfma_f32_16x16x32_bf16 v[72:75], v[140:143], v[214:217], v[72:75]
	s_setprio 0
	s_setprio 1
	v_mfma_f32_16x16x32_bf16 v[116:119], v[144:147], v[180:183], v[116:119]
	v_mfma_f32_16x16x32_bf16 v[112:115], v[172:175], v[180:183], v[112:115]
	v_mfma_f32_16x16x32_bf16 v[100:103], v[144:147], v[194:197], v[100:103]
	v_mfma_f32_16x16x32_bf16 v[96:99], v[172:175], v[194:197], v[96:99]
	v_mfma_f32_16x16x32_bf16 v[84:87], v[144:147], v[202:205], v[84:87]
	v_mfma_f32_16x16x32_bf16 v[80:83], v[172:175], v[202:205], v[80:83]
	v_mfma_f32_16x16x32_bf16 v[68:71], v[144:147], v[210:213], v[68:71]
	v_mfma_f32_16x16x32_bf16 v[64:67], v[172:175], v[210:213], v[64:67]
	v_mfma_f32_16x16x32_bf16 v[116:119], v[148:151], v[184:187], v[116:119]
	v_mfma_f32_16x16x32_bf16 v[112:115], v[176:179], v[184:187], v[112:115]
	v_mfma_f32_16x16x32_bf16 v[100:103], v[148:151], v[198:201], v[100:103]
	v_mfma_f32_16x16x32_bf16 v[96:99], v[176:179], v[198:201], v[96:99]
	v_mfma_f32_16x16x32_bf16 v[84:87], v[148:151], v[206:209], v[84:87]
	v_mfma_f32_16x16x32_bf16 v[80:83], v[176:179], v[206:209], v[80:83]
	v_mfma_f32_16x16x32_bf16 v[68:71], v[148:151], v[214:217], v[68:71]
	v_mfma_f32_16x16x32_bf16 v[64:67], v[176:179], v[214:217], v[64:67]
	s_setprio 0
	s_barrier
	s_add_i32 s22, s45, s33
	v_lshl_add_u64 v[218:219], s[26:27], 0, v[154:155]
	s_mov_b32 m0, s22
	ds_read_b128 v[180:183], v192 offset:16384
	ds_read_b128 v[184:187], v192 offset:17408
	ds_read_b128 v[194:197], v192 offset:18432
	ds_read_b128 v[198:201], v192 offset:19456
	ds_read_b128 v[202:205], v192 offset:20480
	ds_read_b128 v[206:209], v192 offset:21504
	ds_read_b128 v[210:213], v192 offset:22528
	ds_read_b128 v[214:217], v192 offset:23552
	global_load_lds_dwordx4 v154, s[26:27]
	s_add_i32 m0, s22, 0x2000
	s_add_u32 s22, s26, 0xb0000
	v_lshl_add_u64 v[220:221], s[26:27], 0, v[158:159]
	s_addc_u32 s23, s27, 0
	s_add_i32 s69, s46, s33
	global_load_lds_dwordx4 v158, s[26:27]
	s_mov_b32 m0, s69
	v_lshl_add_u64 v[224:225], s[28:29], 0, v[156:157]
	global_load_lds_dwordx4 v154, s[22:23]
	s_add_i32 m0, s69, 0x2000
	s_nop 0
	global_load_lds_dwordx4 v158, s[22:23]
	v_lshl_add_u64 v[222:223], s[28:29], 0, v[152:153]
	s_mov_b32 m0, s34
	s_nop 0
	global_load_lds_dwordx4 v152, s[28:29]
	s_mov_b32 m0, s35
	s_nop 0
	global_load_lds_dwordx4 v156, s[28:29]
	s_waitcnt vmcnt(8) lgkmcnt(0)
	s_barrier
	s_setprio 1
	v_mfma_f32_16x16x32_bf16 v[60:63], v[128:131], v[180:183], v[60:63]
	v_mfma_f32_16x16x32_bf16 v[56:59], v[136:139], v[180:183], v[56:59]
	v_mfma_f32_16x16x32_bf16 v[44:47], v[128:131], v[194:197], v[44:47]
	v_mfma_f32_16x16x32_bf16 v[40:43], v[136:139], v[194:197], v[40:43]
	v_mfma_f32_16x16x32_bf16 v[28:31], v[128:131], v[202:205], v[28:31]
	v_mfma_f32_16x16x32_bf16 v[24:27], v[136:139], v[202:205], v[24:27]
	v_mfma_f32_16x16x32_bf16 v[12:15], v[128:131], v[210:213], v[12:15]
	v_mfma_f32_16x16x32_bf16 v[8:11], v[136:139], v[210:213], v[8:11]
	v_mfma_f32_16x16x32_bf16 v[60:63], v[132:135], v[184:187], v[60:63]
	v_mfma_f32_16x16x32_bf16 v[56:59], v[140:143], v[184:187], v[56:59]
	v_mfma_f32_16x16x32_bf16 v[44:47], v[132:135], v[198:201], v[44:47]
	v_mfma_f32_16x16x32_bf16 v[40:43], v[140:143], v[198:201], v[40:43]
	v_mfma_f32_16x16x32_bf16 v[28:31], v[132:135], v[206:209], v[28:31]
	v_mfma_f32_16x16x32_bf16 v[24:27], v[140:143], v[206:209], v[24:27]
	v_mfma_f32_16x16x32_bf16 v[12:15], v[132:135], v[214:217], v[12:15]
	v_mfma_f32_16x16x32_bf16 v[8:11], v[140:143], v[214:217], v[8:11]
	s_setprio 0
	s_setprio 1
	v_mfma_f32_16x16x32_bf16 v[52:55], v[144:147], v[180:183], v[52:55]
	v_mfma_f32_16x16x32_bf16 v[48:51], v[172:175], v[180:183], v[48:51]
	v_mfma_f32_16x16x32_bf16 v[36:39], v[144:147], v[194:197], v[36:39]
	v_mfma_f32_16x16x32_bf16 v[32:35], v[172:175], v[194:197], v[32:35]
	v_mfma_f32_16x16x32_bf16 v[20:23], v[144:147], v[202:205], v[20:23]
	v_mfma_f32_16x16x32_bf16 v[16:19], v[172:175], v[202:205], v[16:19]
	v_mfma_f32_16x16x32_bf16 v[4:7], v[144:147], v[210:213], v[4:7]
	v_mfma_f32_16x16x32_bf16 v[0:3], v[172:175], v[210:213], v[0:3]
	v_mfma_f32_16x16x32_bf16 v[52:55], v[148:151], v[184:187], v[52:55]
	v_mfma_f32_16x16x32_bf16 v[48:51], v[176:179], v[184:187], v[48:51]
	v_mfma_f32_16x16x32_bf16 v[36:39], v[148:151], v[198:201], v[36:39]
	v_mfma_f32_16x16x32_bf16 v[32:35], v[176:179], v[198:201], v[32:35]
	v_mfma_f32_16x16x32_bf16 v[20:23], v[148:151], v[206:209], v[20:23]
	v_mfma_f32_16x16x32_bf16 v[16:19], v[176:179], v[206:209], v[16:19]
	v_mfma_f32_16x16x32_bf16 v[4:7], v[148:151], v[214:217], v[4:7]
	v_mfma_f32_16x16x32_bf16 v[0:3], v[176:179], v[214:217], v[0:3]
	s_setprio 0
	s_barrier
; #define PG8_STAGE(bufoff, gbase, voff) do { _Pragma("unroll") for (int _i = 0; _i < 2; ++_i) \
;         __builtin_amdgcn_global_load_lds((const unsigned*)((const char*)(gbase) + (voff)[_i]), (PG8_LAS unsigned*)(lds + (bufoff) + ldsw + _i * 8192), 16, 0, 0); } while (0)
; #define PG8_LDA(dst, b, h) do { _Pragma("unroll") for (int m = 0; m < 4; ++m) _Pragma("unroll") for (int k = 0; k < 2; ++k) dst[m][k] = *(const PG8_LAS bf16x8*)(lds + PG8_SA(b, h) + aoff + m * 2048 + k * 1024); } while (0)
; #define PG8_LDB(dst, b, h) do { _Pragma("unroll") for (int n = 0; n < 2; ++n) _Pragma("unroll") for (int k = 0; k < 2; ++k) dst[n][k] = *(const PG8_LAS bf16x8*)(lds + PG8_SB(b, h) + boff + n * 2048 + k * 1024); } while (0)
; #define PG8_MMA(ai, bj, At, Bt) do { __builtin_amdgcn_s_setprio(1); _Pragma("unroll") for (int m = 0; m < 4; ++m) _Pragma("unroll") for (int n = 0; n < 2; ++n) _Pragma("unroll") for (int k = 0; k < 2; ++k) \
;         acc[ai][bj][m][n] = __builtin_amdgcn_mfma_f32_16x16x32_bf16(Bt[n][k], At[m][k], acc[ai][bj][m][n], 0, 0, 0); __builtin_amdgcn_s_setprio(0); } while (0)
; #define PG8_WAIT_V(n) asm volatile("s_waitcnt vmcnt(" #n ")" ::: "memory")
; #define PG8_WAIT_L(n) asm volatile("s_waitcnt lgkmcnt(" #n ")" ::: "memory")
; #define PG8_BAR __builtin_amdgcn_s_barrier()
; #define PG8_SCHED __builtin_amdgcn_sched_barrier(0)
; template <class Epi, class Sched, bool ALIGN_EPI = false, bool SP2 = false>
; __device__ __forceinline__ void gemm_phase(PG8_LAS unsigned char* lds, const Gemm g, const Sched& S, const Epi& E, const int wid) {
;     ...
;         for (int t = 0; t < nt; t += 2) {
;             const bool last = (t == nt - 2);
;             const char* a1 = cA + (size_t)(t + 1) * kstep;
;             const char* a2 = last ? nA : cA + (size_t)(t + 2) * kstep; const char* b2 = last ? nB : cB + (size_t)(t + 2) * kstep;
;     ...
;             PG8_LDB(B0, 1, 0); PG8_LDB(B1, 1, 1); PG8_SCHED; PG8_LDA(At, 1, 0); PG8_STAGE(PG8_SA(0, 1), a2 + hstepA, voffA);
;             PG8_WAIT_V(8); PG8_WAIT_L(0); PG8_BAR; PG8_MMA(0, 0, At, B0); PG8_MMA(0, 1, At, B1); PG8_BAR; PG8_SCHED;
;             PG8_LDA(At, 1, 1); PG8_STAGE(PG8_SB(1, 0), b3, voffB); PG8_STAGE(PG8_SB(1, 1), b3 + hstepB, voffB); PG8_STAGE(PG8_SA(1, 0), a3, voffA);
;             PG8_WAIT_V(8); PG8_WAIT_L(0); PG8_BAR; PG8_MMA(1, 0, At, B0); PG8_MMA(1, 1, At, B1); PG8_BAR; PG8_SCHED;
	s_add_i32 s69, 0, 0x18000
	s_add_i32 s70, 0, 0x1c000
	v_add_u32_e32 v140, s69, v189
	v_add_u32_e32 v176, s70, v189
	ds_read_b128 v[128:131], v140
	ds_read_b128 v[132:135], v140 offset:1024
	ds_read_b128 v[136:139], v140 offset:2048
	ds_read_b128 v[140:143], v140 offset:3072
	ds_read_b128 v[144:147], v176
	ds_read_b128 v[148:151], v176 offset:1024
	ds_read_b128 v[172:175], v176 offset:2048
	ds_read_b128 v[176:179], v176 offset:3072
	s_add_u32 s22, s28, 0xb0000
	s_addc_u32 s23, s29, 0
	s_mov_b32 m0, s36
	ds_read_b128 v[180:183], v192 offset:32768
	ds_read_b128 v[184:187], v192 offset:33792
	ds_read_b128 v[194:197], v192 offset:34816
	ds_read_b128 v[198:201], v192 offset:35840
	ds_read_b128 v[202:205], v192 offset:36864
	ds_read_b128 v[206:209], v192 offset:37888
	ds_read_b128 v[210:213], v192 offset:38912
	ds_read_b128 v[214:217], v192 offset:39936
	global_load_lds_dwordx4 v152, s[22:23]
	s_mov_b32 m0, s37
	s_nop 0
	global_load_lds_dwordx4 v156, s[22:23]
	s_waitcnt vmcnt(8) lgkmcnt(0)
	s_barrier
	s_setprio 1
	v_mfma_f32_16x16x32_bf16 v[124:127], v[128:131], v[180:183], v[124:127]
	v_mfma_f32_16x16x32_bf16 v[120:123], v[136:139], v[180:183], v[120:123]
	v_mfma_f32_16x16x32_bf16 v[108:111], v[128:131], v[194:197], v[108:111]
	v_mfma_f32_16x16x32_bf16 v[104:107], v[136:139], v[194:197], v[104:107]
	v_mfma_f32_16x16x32_bf16 v[92:95], v[128:131], v[202:205], v[92:95]
	v_mfma_f32_16x16x32_bf16 v[88:91], v[136:139], v[202:205], v[88:91]
	v_mfma_f32_16x16x32_bf16 v[76:79], v[128:131], v[210:213], v[76:79]
	v_mfma_f32_16x16x32_bf16 v[72:75], v[136:139], v[210:213], v[72:75]
	v_mfma_f32_16x16x32_bf16 v[124:127], v[132:135], v[184:187], v[124:127]
	v_mfma_f32_16x16x32_bf16 v[120:123], v[140:143], v[184:187], v[120:123]
	v_mfma_f32_16x16x32_bf16 v[108:111], v[132:135], v[198:201], v[108:111]
	v_mfma_f32_16x16x32_bf16 v[104:107], v[140:143], v[198:201], v[104:107]
	v_mfma_f32_16x16x32_bf16 v[92:95], v[132:135], v[206:209], v[92:95]
	v_mfma_f32_16x16x32_bf16 v[88:91], v[140:143], v[206:209], v[88:91]
	v_mfma_f32_16x16x32_bf16 v[76:79], v[132:135], v[214:217], v[76:79]
	v_mfma_f32_16x16x32_bf16 v[72:75], v[140:143], v[214:217], v[72:75]
	s_setprio 0
	s_setprio 1
	v_mfma_f32_16x16x32_bf16 v[116:119], v[144:147], v[180:183], v[116:119]
	v_mfma_f32_16x16x32_bf16 v[112:115], v[172:175], v[180:183], v[112:115]
	v_mfma_f32_16x16x32_bf16 v[100:103], v[144:147], v[194:197], v[100:103]
	v_mfma_f32_16x16x32_bf16 v[96:99], v[172:175], v[194:197], v[96:99]
	v_mfma_f32_16x16x32_bf16 v[84:87], v[144:147], v[202:205], v[84:87]
	v_mfma_f32_16x16x32_bf16 v[80:83], v[172:175], v[202:205], v[80:83]
	v_mfma_f32_16x16x32_bf16 v[68:71], v[144:147], v[210:213], v[68:71]
	v_mfma_f32_16x16x32_bf16 v[64:67], v[172:175], v[210:213], v[64:67]
	v_mfma_f32_16x16x32_bf16 v[116:119], v[148:151], v[184:187], v[116:119]
	v_mfma_f32_16x16x32_bf16 v[112:115], v[176:179], v[184:187], v[112:115]
	v_mfma_f32_16x16x32_bf16 v[100:103], v[148:151], v[198:201], v[100:103]
	v_mfma_f32_16x16x32_bf16 v[96:99], v[176:179], v[198:201], v[96:99]
	v_mfma_f32_16x16x32_bf16 v[84:87], v[148:151], v[206:209], v[84:87]
	v_mfma_f32_16x16x32_bf16 v[80:83], v[176:179], v[206:209], v[80:83]
	v_mfma_f32_16x16x32_bf16 v[68:71], v[148:151], v[214:217], v[68:71]
	v_mfma_f32_16x16x32_bf16 v[64:67], v[176:179], v[214:217], v[64:67]
	s_setprio 0
	s_barrier
	s_add_i32 s22, s69, s33
	v_lshl_add_u64 v[218:219], v[218:219], 0, s[16:17]
	s_mov_b32 m0, s22
	ds_read_b128 v[180:183], v192 offset:49152
	ds_read_b128 v[184:187], v192 offset:50176
	ds_read_b128 v[194:197], v192 offset:51200
	ds_read_b128 v[198:201], v192 offset:52224
	ds_read_b128 v[202:205], v192 offset:53248
	ds_read_b128 v[206:209], v192 offset:54272
	ds_read_b128 v[210:213], v192 offset:55296
	ds_read_b128 v[214:217], v192 offset:56320
	global_load_lds_dwordx4 v[218:219], off
	s_add_i32 m0, s22, 0x2000
	s_add_u32 s22, s26, 0xb0080
	v_lshl_add_u64 v[218:219], v[220:221], 0, s[16:17]
	s_addc_u32 s23, s27, 0
	s_add_i32 s26, s70, s33
	global_load_lds_dwordx4 v[218:219], off
	s_mov_b32 m0, s26
	s_nop 0
	global_load_lds_dwordx4 v154, s[22:23]
	v_lshl_add_u64 v[218:219], s[22:23], 0, v[158:159]
	s_add_i32 m0, s26, 0x2000
	s_nop 0
	global_load_lds_dwordx4 v158, s[22:23]
	v_lshl_add_u64 v[218:219], v[222:223], 0, s[16:17]
	s_mov_b32 m0, s39
	s_nop 0
	global_load_lds_dwordx4 v[218:219], off
	v_lshl_add_u64 v[218:219], v[224:225], 0, s[16:17]
	s_mov_b32 m0, s40
	s_nop 0
	global_load_lds_dwordx4 v[218:219], off
	s_waitcnt vmcnt(8) lgkmcnt(0)
	s_barrier
	s_setprio 1
	v_mfma_f32_16x16x32_bf16 v[60:63], v[128:131], v[180:183], v[60:63]
	v_mfma_f32_16x16x32_bf16 v[56:59], v[136:139], v[180:183], v[56:59]
	v_mfma_f32_16x16x32_bf16 v[44:47], v[128:131], v[194:197], v[44:47]
	v_mfma_f32_16x16x32_bf16 v[40:43], v[136:139], v[194:197], v[40:43]
	v_mfma_f32_16x16x32_bf16 v[28:31], v[128:131], v[202:205], v[28:31]
	v_mfma_f32_16x16x32_bf16 v[24:27], v[136:139], v[202:205], v[24:27]
	v_mfma_f32_16x16x32_bf16 v[12:15], v[128:131], v[210:213], v[12:15]
	v_mfma_f32_16x16x32_bf16 v[8:11], v[136:139], v[210:213], v[8:11]
	v_mfma_f32_16x16x32_bf16 v[60:63], v[132:135], v[184:187], v[60:63]
	v_mfma_f32_16x16x32_bf16 v[56:59], v[140:143], v[184:187], v[56:59]
	v_mfma_f32_16x16x32_bf16 v[44:47], v[132:135], v[198:201], v[44:47]
	v_mfma_f32_16x16x32_bf16 v[40:43], v[140:143], v[198:201], v[40:43]
	v_mfma_f32_16x16x32_bf16 v[28:31], v[132:135], v[206:209], v[28:31]
	v_mfma_f32_16x16x32_bf16 v[24:27], v[140:143], v[206:209], v[24:27]
	v_mfma_f32_16x16x32_bf16 v[12:15], v[132:135], v[214:217], v[12:15]
	v_mfma_f32_16x16x32_bf16 v[8:11], v[140:143], v[214:217], v[8:11]
	s_setprio 0
	s_setprio 1
	v_mfma_f32_16x16x32_bf16 v[52:55], v[144:147], v[180:183], v[52:55]
	v_mfma_f32_16x16x32_bf16 v[48:51], v[172:175], v[180:183], v[48:51]
	v_mfma_f32_16x16x32_bf16 v[36:39], v[144:147], v[194:197], v[36:39]
	v_mfma_f32_16x16x32_bf16 v[32:35], v[172:175], v[194:197], v[32:35]
	v_mfma_f32_16x16x32_bf16 v[20:23], v[144:147], v[202:205], v[20:23]
	v_mfma_f32_16x16x32_bf16 v[16:19], v[172:175], v[202:205], v[16:19]
	v_mfma_f32_16x16x32_bf16 v[4:7], v[144:147], v[210:213], v[4:7]
	v_mfma_f32_16x16x32_bf16 v[0:3], v[172:175], v[210:213], v[0:3]
	v_mfma_f32_16x16x32_bf16 v[52:55], v[148:151], v[184:187], v[52:55]
	v_mfma_f32_16x16x32_bf16 v[48:51], v[176:179], v[184:187], v[48:51]
	v_mfma_f32_16x16x32_bf16 v[36:39], v[148:151], v[198:201], v[36:39]
	v_mfma_f32_16x16x32_bf16 v[32:35], v[176:179], v[198:201], v[32:35]
	v_mfma_f32_16x16x32_bf16 v[20:23], v[148:151], v[206:209], v[20:23]
	v_mfma_f32_16x16x32_bf16 v[16:19], v[176:179], v[206:209], v[16:19]
	v_mfma_f32_16x16x32_bf16 v[4:7], v[148:151], v[214:217], v[4:7]
	v_mfma_f32_16x16x32_bf16 v[0:3], v[176:179], v[214:217], v[0:3]
	s_setprio 0
	s_barrier
	s_add_i32 s68, s68, 2
	s_add_u32 s66, s66, 0x100
	s_addc_u32 s67, s67, 0
	s_cmp_gt_u32 s68, 41
	s_mov_b64 s[22:23], s[24:25]
	s_cbranch_scc0 .LBB0_1952
	s_and_b64 vcc, exec, s[18:19]
	s_cbranch_vccz .LBB0_1955
	s_barrier

; #define PG8_STAGE(bufoff, gbase, voff) do { _Pragma("unroll") for (int _i = 0; _i < 2; ++_i) \
;         __builtin_amdgcn_global_load_lds((const unsigned*)((const char*)(gbase) + (voff)[_i]), (PG8_LAS unsigned*)(lds + (bufoff) + ldsw + _i * 8192), 16, 0, 0); } while (0)
; #define PG8_LDA(dst, b, h) do { _Pragma("unroll") for (int m = 0; m < 4; ++m) _Pragma("unroll") for (int k = 0; k < 2; ++k) dst[m][k] = *(const PG8_LAS bf16x8*)(lds + PG8_SA(b, h) + aoff + m * 2048 + k * 1024); } while (0)
; #define PG8_LDB(dst, b, h) do { _Pragma("unroll") for (int n = 0; n < 2; ++n) _Pragma("unroll") for (int k = 0; k < 2; ++k) dst[n][k] = *(const PG8_LAS bf16x8*)(lds + PG8_SB(b, h) + boff + n * 2048 + k * 1024); } while (0)
; #define PG8_MMA(ai, bj, At, Bt) do { __builtin_amdgcn_s_setprio(1); _Pragma("unroll") for (int m = 0; m < 4; ++m) _Pragma("unroll") for (int n = 0; n < 2; ++n) _Pragma("unroll") for (int k = 0; k < 2; ++k) \
;         acc[ai][bj][m][n] = __builtin_amdgcn_mfma_f32_16x16x32_bf16(Bt[n][k], At[m][k], acc[ai][bj][m][n], 0, 0, 0); __builtin_amdgcn_s_setprio(0); } while (0)
; #define PG8_WAIT_V(n) asm volatile("s_waitcnt vmcnt(" #n ")" ::: "memory")
; #define PG8_BAR __builtin_amdgcn_s_barrier()
; template <class Epi, class Sched, bool ALIGN_EPI = false, bool SP2 = false>
; __device__ __forceinline__ void gemm_phase(PG8_LAS unsigned char* lds, const Gemm g, const Sched& S, const Epi& E, const int wid) {
;     ...
;         for (int t = 0; t < nt; t += 2) {
;             const bool last = (t == nt - 2);
;             const char* a1 = cA + (size_t)(t + 1) * kstep;
;             const char* a2 = last ? nA : cA + (size_t)(t + 2) * kstep; const char* b2 = last ? nB : cB + (size_t)(t + 2) * kstep;
;             const char* a3 = a2 + kstep; const char* b3 = b2 + kstep;
;             if (last && has_next) S.a_ready(nxt);
;             if constexpr (SP2) {
;             PG8_LDB(B0, 0, 0); PG8_LDB(B1, 0, 1); PG8_SCHED; PG8_LDA(At, 0, 0); PG8_STAGE(PG8_SA(1, 1), a1 + hstepA, voffA);
;             PG8_WAIT_V(8); PG8_WAIT_L(0); PG8_BAR; PG8_MMA(0, 0, At, B0); PG8_MMA(0, 1, At, B1); PG8_BAR; PG8_SCHED;
;             PG8_LDA(At, 0, 1); PG8_STAGE(PG8_SB(0, 0), b2, voffB); PG8_STAGE(PG8_SB(0, 1), b2 + hstepB, voffB); PG8_STAGE(PG8_SA(0, 0), a2, voffA);
;             PG8_WAIT_V(8); PG8_WAIT_L(0); PG8_BAR; PG8_MMA(1, 0, At, B0); PG8_MMA(1, 1, At, B1); PG8_BAR; PG8_SCHED;
.LBB0_2049:
	ds_read_b128 v[146:149], v179
	ds_read_b128 v[150:153], v179 offset:1024
	ds_read_b128 v[154:157], v179 offset:2048
	ds_read_b128 v[158:161], v179 offset:3072
	ds_read_b128 v[162:165], v180
	ds_read_b128 v[166:169], v180 offset:1024
	ds_read_b128 v[184:187], v180 offset:2048
	ds_read_b128 v[188:191], v180 offset:3072
	s_add_u32 s12, s8, 0xfffc0080
	s_addc_u32 s13, s9, -1
	s_cmp_eq_u32 s71, 12
	s_cselect_b32 s39, s7, s13
	s_cselect_b32 s38, s11, s12
	s_cselect_b32 s13, s29, s41
	s_cselect_b32 s12, s31, s40
	s_add_i32 m0, s46, 0xc000
	ds_read_b128 v[192:195], v181
	ds_read_b128 v[196:199], v181 offset:1024
	ds_read_b128 v[200:203], v181 offset:2048
	ds_read_b128 v[204:207], v181 offset:3072
	ds_read_b128 v[208:211], v181 offset:4096
	ds_read_b128 v[212:215], v181 offset:5120
	ds_read_b128 v[216:219], v181 offset:6144
	ds_read_b128 v[220:223], v181 offset:7168
	global_load_lds_dwordx4 v138, s[8:9]
	s_add_i32 m0, s46, 0xe000
	s_nop 0
	global_load_lds_dwordx4 v140, s[8:9]
	s_waitcnt vmcnt(8) lgkmcnt(0)
	s_barrier
	s_setprio 1
	v_mfma_f32_16x16x32_bf16 v[124:127], v[146:149], v[192:195], v[124:127]
	v_mfma_f32_16x16x32_bf16 v[120:123], v[154:157], v[192:195], v[120:123]
	v_mfma_f32_16x16x32_bf16 v[108:111], v[146:149], v[200:203], v[108:111]
	v_mfma_f32_16x16x32_bf16 v[104:107], v[154:157], v[200:203], v[104:107]
	v_mfma_f32_16x16x32_bf16 v[92:95], v[146:149], v[208:211], v[92:95]
	v_mfma_f32_16x16x32_bf16 v[88:91], v[154:157], v[208:211], v[88:91]
	v_mfma_f32_16x16x32_bf16 v[76:79], v[146:149], v[216:219], v[76:79]
	v_mfma_f32_16x16x32_bf16 v[72:75], v[154:157], v[216:219], v[72:75]
	v_mfma_f32_16x16x32_bf16 v[124:127], v[150:153], v[196:199], v[124:127]
	v_mfma_f32_16x16x32_bf16 v[120:123], v[158:161], v[196:199], v[120:123]
	v_mfma_f32_16x16x32_bf16 v[108:111], v[150:153], v[204:207], v[108:111]
	v_mfma_f32_16x16x32_bf16 v[104:107], v[158:161], v[204:207], v[104:107]
	v_mfma_f32_16x16x32_bf16 v[92:95], v[150:153], v[212:215], v[92:95]
	v_mfma_f32_16x16x32_bf16 v[88:91], v[158:161], v[212:215], v[88:91]
	v_mfma_f32_16x16x32_bf16 v[76:79], v[150:153], v[220:223], v[76:79]
	v_mfma_f32_16x16x32_bf16 v[72:75], v[158:161], v[220:223], v[72:75]
	s_setprio 0
	s_setprio 1
	v_mfma_f32_16x16x32_bf16 v[116:119], v[162:165], v[192:195], v[116:119]
	v_mfma_f32_16x16x32_bf16 v[112:115], v[184:187], v[192:195], v[112:115]
	v_mfma_f32_16x16x32_bf16 v[100:103], v[162:165], v[200:203], v[100:103]
	v_mfma_f32_16x16x32_bf16 v[96:99], v[184:187], v[200:203], v[96:99]
	v_mfma_f32_16x16x32_bf16 v[84:87], v[162:165], v[208:211], v[84:87]
	v_mfma_f32_16x16x32_bf16 v[80:83], v[184:187], v[208:211], v[80:83]
	v_mfma_f32_16x16x32_bf16 v[68:71], v[162:165], v[216:219], v[68:71]
	v_mfma_f32_16x16x32_bf16 v[64:67], v[184:187], v[216:219], v[64:67]
	v_mfma_f32_16x16x32_bf16 v[116:119], v[166:169], v[196:199], v[116:119]
	v_mfma_f32_16x16x32_bf16 v[112:115], v[188:191], v[196:199], v[112:115]
	v_mfma_f32_16x16x32_bf16 v[100:103], v[166:169], v[204:207], v[100:103]
	v_mfma_f32_16x16x32_bf16 v[96:99], v[188:191], v[204:207], v[96:99]
	v_mfma_f32_16x16x32_bf16 v[84:87], v[166:169], v[212:215], v[84:87]
	v_mfma_f32_16x16x32_bf16 v[80:83], v[188:191], v[212:215], v[80:83]
	v_mfma_f32_16x16x32_bf16 v[68:71], v[166:169], v[220:223], v[68:71]
	v_mfma_f32_16x16x32_bf16 v[64:67], v[188:191], v[220:223], v[64:67]
	s_setprio 0
	s_barrier
	s_add_i32 s72, s69, s45
	v_lshl_add_u64 v[170:171], s[12:13], 0, v[130:131]
	s_mov_b32 m0, s72
	ds_read_b128 v[192:195], v181 offset:16384
	ds_read_b128 v[196:199], v181 offset:17408
	ds_read_b128 v[200:203], v181 offset:18432
	ds_read_b128 v[204:207], v181 offset:19456
	ds_read_b128 v[208:211], v181 offset:20480
	ds_read_b128 v[212:215], v181 offset:21504
	ds_read_b128 v[216:219], v181 offset:22528
	ds_read_b128 v[220:223], v181 offset:23552
	global_load_lds_dwordx4 v130, s[12:13]
	s_add_i32 m0, s72, 0x2000
	s_add_u32 s72, s12, 0x40000
	v_lshl_add_u64 v[224:225], s[12:13], 0, v[134:135]
	s_addc_u32 s73, s13, 0
	s_add_i32 s74, s70, s45
	global_load_lds_dwordx4 v134, s[12:13]
	s_mov_b32 m0, s74
	v_lshl_add_u64 v[228:229], s[38:39], 0, v[132:133]
	global_load_lds_dwordx4 v130, s[72:73]
	s_add_i32 m0, s74, 0x2000
	s_nop 0
	global_load_lds_dwordx4 v134, s[72:73]
	v_lshl_add_u64 v[226:227], s[38:39], 0, v[128:129]
	s_mov_b32 m0, s46
	s_nop 0
	global_load_lds_dwordx4 v128, s[38:39]
	s_mov_b32 m0, s47
	s_nop 0
	global_load_lds_dwordx4 v132, s[38:39]
	s_waitcnt vmcnt(8) lgkmcnt(0)
	s_barrier
	s_setprio 1
	v_mfma_f32_16x16x32_bf16 v[60:63], v[146:149], v[192:195], v[60:63]
	v_mfma_f32_16x16x32_bf16 v[56:59], v[154:157], v[192:195], v[56:59]
	v_mfma_f32_16x16x32_bf16 v[44:47], v[146:149], v[200:203], v[44:47]
	v_mfma_f32_16x16x32_bf16 v[40:43], v[154:157], v[200:203], v[40:43]
	v_mfma_f32_16x16x32_bf16 v[28:31], v[146:149], v[208:211], v[28:31]
	v_mfma_f32_16x16x32_bf16 v[24:27], v[154:157], v[208:211], v[24:27]
	v_mfma_f32_16x16x32_bf16 v[12:15], v[146:149], v[216:219], v[12:15]
	v_mfma_f32_16x16x32_bf16 v[8:11], v[154:157], v[216:219], v[8:11]
	v_mfma_f32_16x16x32_bf16 v[60:63], v[150:153], v[196:199], v[60:63]
	v_mfma_f32_16x16x32_bf16 v[56:59], v[158:161], v[196:199], v[56:59]
	v_mfma_f32_16x16x32_bf16 v[44:47], v[150:153], v[204:207], v[44:47]
	v_mfma_f32_16x16x32_bf16 v[40:43], v[158:161], v[204:207], v[40:43]
	v_mfma_f32_16x16x32_bf16 v[28:31], v[150:153], v[212:215], v[28:31]
	v_mfma_f32_16x16x32_bf16 v[24:27], v[158:161], v[212:215], v[24:27]
	v_mfma_f32_16x16x32_bf16 v[12:15], v[150:153], v[220:223], v[12:15]
	v_mfma_f32_16x16x32_bf16 v[8:11], v[158:161], v[220:223], v[8:11]
	s_setprio 0
	s_setprio 1
	v_mfma_f32_16x16x32_bf16 v[52:55], v[162:165], v[192:195], v[52:55]
	v_mfma_f32_16x16x32_bf16 v[48:51], v[184:187], v[192:195], v[48:51]
	v_mfma_f32_16x16x32_bf16 v[36:39], v[162:165], v[200:203], v[36:39]
	v_mfma_f32_16x16x32_bf16 v[32:35], v[184:187], v[200:203], v[32:35]
	v_mfma_f32_16x16x32_bf16 v[20:23], v[162:165], v[208:211], v[20:23]
	v_mfma_f32_16x16x32_bf16 v[16:19], v[184:187], v[208:211], v[16:19]
	v_mfma_f32_16x16x32_bf16 v[4:7], v[162:165], v[216:219], v[4:7]
	v_mfma_f32_16x16x32_bf16 v[0:3], v[184:187], v[216:219], v[0:3]
	v_mfma_f32_16x16x32_bf16 v[52:55], v[166:169], v[196:199], v[52:55]
	v_mfma_f32_16x16x32_bf16 v[48:51], v[188:191], v[196:199], v[48:51]
	v_mfma_f32_16x16x32_bf16 v[36:39], v[166:169], v[204:207], v[36:39]
	v_mfma_f32_16x16x32_bf16 v[32:35], v[188:191], v[204:207], v[32:35]
	v_mfma_f32_16x16x32_bf16 v[20:23], v[166:169], v[212:215], v[20:23]
	v_mfma_f32_16x16x32_bf16 v[16:19], v[188:191], v[212:215], v[16:19]
	v_mfma_f32_16x16x32_bf16 v[4:7], v[166:169], v[220:223], v[4:7]
	v_mfma_f32_16x16x32_bf16 v[0:3], v[188:191], v[220:223], v[0:3]
	s_setprio 0
	s_barrier
; #define PG8_STAGE(bufoff, gbase, voff) do { _Pragma("unroll") for (int _i = 0; _i < 2; ++_i) \
;         __builtin_amdgcn_global_load_lds((const unsigned*)((const char*)(gbase) + (voff)[_i]), (PG8_LAS unsigned*)(lds + (bufoff) + ldsw + _i * 8192), 16, 0, 0); } while (0)
; #define PG8_LDA(dst, b, h) do { _Pragma("unroll") for (int m = 0; m < 4; ++m) _Pragma("unroll") for (int k = 0; k < 2; ++k) dst[m][k] = *(const PG8_LAS bf16x8*)(lds + PG8_SA(b, h) + aoff + m * 2048 + k * 1024); } while (0)
; #define PG8_LDB(dst, b, h) do { _Pragma("unroll") for (int n = 0; n < 2; ++n) _Pragma("unroll") for (int k = 0; k < 2; ++k) dst[n][k] = *(const PG8_LAS bf16x8*)(lds + PG8_SB(b, h) + boff + n * 2048 + k * 1024); } while (0)
; #define PG8_MMA(ai, bj, At, Bt) do { __builtin_amdgcn_s_setprio(1); _Pragma("unroll") for (int m = 0; m < 4; ++m) _Pragma("unroll") for (int n = 0; n < 2; ++n) _Pragma("unroll") for (int k = 0; k < 2; ++k) \
;         acc[ai][bj][m][n] = __builtin_amdgcn_mfma_f32_16x16x32_bf16(Bt[n][k], At[m][k], acc[ai][bj][m][n], 0, 0, 0); __builtin_amdgcn_s_setprio(0); } while (0)
; #define PG8_WAIT_V(n) asm volatile("s_waitcnt vmcnt(" #n ")" ::: "memory")
; #define PG8_WAIT_L(n) asm volatile("s_waitcnt lgkmcnt(" #n ")" ::: "memory")
; #define PG8_BAR __builtin_amdgcn_s_barrier()
; #define PG8_SCHED __builtin_amdgcn_sched_barrier(0)
; template <class Epi, class Sched, bool ALIGN_EPI = false, bool SP2 = false>
; __device__ __forceinline__ void gemm_phase(PG8_LAS unsigned char* lds, const Gemm g, const Sched& S, const Epi& E, const int wid) {
;     ...
;         for (int t = 0; t < nt; t += 2) {
;             const bool last = (t == nt - 2);
;             const char* a1 = cA + (size_t)(t + 1) * kstep;
;             const char* a2 = last ? nA : cA + (size_t)(t + 2) * kstep; const char* b2 = last ? nB : cB + (size_t)(t + 2) * kstep;
;     ...
;             PG8_LDB(B0, 1, 0); PG8_LDB(B1, 1, 1); PG8_SCHED; PG8_LDA(At, 1, 0); PG8_STAGE(PG8_SA(0, 1), a2 + hstepA, voffA);
;             PG8_WAIT_V(8); PG8_WAIT_L(0); PG8_BAR; PG8_MMA(0, 0, At, B0); PG8_MMA(0, 1, At, B1); PG8_BAR; PG8_SCHED;
;             PG8_LDA(At, 1, 1); PG8_STAGE(PG8_SB(1, 0), b3, voffB); PG8_STAGE(PG8_SB(1, 1), b3 + hstepB, voffB); PG8_STAGE(PG8_SA(1, 0), a3, voffA);
;             PG8_WAIT_V(8); PG8_WAIT_L(0); PG8_BAR; PG8_MMA(1, 0, At, B0); PG8_MMA(1, 1, At, B1); PG8_BAR; PG8_SCHED;
	s_add_i32 s72, 0, 0x18000
	s_add_i32 s73, 0, 0x1c000
	v_add_u32_e32 v158, s72, v174
	v_add_u32_e32 v188, s73, v174
	ds_read_b128 v[146:149], v158
	ds_read_b128 v[150:153], v158 offset:1024
	ds_read_b128 v[154:157], v158 offset:2048
	ds_read_b128 v[158:161], v158 offset:3072
	ds_read_b128 v[162:165], v188
	ds_read_b128 v[166:169], v188 offset:1024
	ds_read_b128 v[184:187], v188 offset:2048
	ds_read_b128 v[188:191], v188 offset:3072
	s_add_u32 s38, s38, 0x40000
	s_addc_u32 s39, s39, 0
	s_mov_b32 m0, s48
	ds_read_b128 v[192:195], v181 offset:32768
	ds_read_b128 v[196:199], v181 offset:33792
	ds_read_b128 v[200:203], v181 offset:34816
	ds_read_b128 v[204:207], v181 offset:35840
	ds_read_b128 v[208:211], v181 offset:36864
	ds_read_b128 v[212:215], v181 offset:37888
	ds_read_b128 v[216:219], v181 offset:38912
	ds_read_b128 v[220:223], v181 offset:39936
	global_load_lds_dwordx4 v128, s[38:39]
	s_mov_b32 m0, s49
	s_nop 0
	global_load_lds_dwordx4 v132, s[38:39]
	s_waitcnt vmcnt(8) lgkmcnt(0)
	s_barrier
	s_setprio 1
	v_mfma_f32_16x16x32_bf16 v[124:127], v[146:149], v[192:195], v[124:127]
	v_mfma_f32_16x16x32_bf16 v[120:123], v[154:157], v[192:195], v[120:123]
	v_mfma_f32_16x16x32_bf16 v[108:111], v[146:149], v[200:203], v[108:111]
	v_mfma_f32_16x16x32_bf16 v[104:107], v[154:157], v[200:203], v[104:107]
	v_mfma_f32_16x16x32_bf16 v[92:95], v[146:149], v[208:211], v[92:95]
	v_mfma_f32_16x16x32_bf16 v[88:91], v[154:157], v[208:211], v[88:91]
	v_mfma_f32_16x16x32_bf16 v[76:79], v[146:149], v[216:219], v[76:79]
	v_mfma_f32_16x16x32_bf16 v[72:75], v[154:157], v[216:219], v[72:75]
	v_mfma_f32_16x16x32_bf16 v[124:127], v[150:153], v[196:199], v[124:127]
	v_mfma_f32_16x16x32_bf16 v[120:123], v[158:161], v[196:199], v[120:123]
	v_mfma_f32_16x16x32_bf16 v[108:111], v[150:153], v[204:207], v[108:111]
	v_mfma_f32_16x16x32_bf16 v[104:107], v[158:161], v[204:207], v[104:107]
	v_mfma_f32_16x16x32_bf16 v[92:95], v[150:153], v[212:215], v[92:95]
	v_mfma_f32_16x16x32_bf16 v[88:91], v[158:161], v[212:215], v[88:91]
	v_mfma_f32_16x16x32_bf16 v[76:79], v[150:153], v[220:223], v[76:79]
	v_mfma_f32_16x16x32_bf16 v[72:75], v[158:161], v[220:223], v[72:75]
	s_setprio 0
	s_setprio 1
	v_mfma_f32_16x16x32_bf16 v[116:119], v[162:165], v[192:195], v[116:119]
	v_mfma_f32_16x16x32_bf16 v[112:115], v[184:187], v[192:195], v[112:115]
	v_mfma_f32_16x16x32_bf16 v[100:103], v[162:165], v[200:203], v[100:103]
	v_mfma_f32_16x16x32_bf16 v[96:99], v[184:187], v[200:203], v[96:99]
	v_mfma_f32_16x16x32_bf16 v[84:87], v[162:165], v[208:211], v[84:87]
	v_mfma_f32_16x16x32_bf16 v[80:83], v[184:187], v[208:211], v[80:83]
	v_mfma_f32_16x16x32_bf16 v[68:71], v[162:165], v[216:219], v[68:71]
	v_mfma_f32_16x16x32_bf16 v[64:67], v[184:187], v[216:219], v[64:67]
	v_mfma_f32_16x16x32_bf16 v[116:119], v[166:169], v[196:199], v[116:119]
	v_mfma_f32_16x16x32_bf16 v[112:115], v[188:191], v[196:199], v[112:115]
	v_mfma_f32_16x16x32_bf16 v[100:103], v[166:169], v[204:207], v[100:103]
	v_mfma_f32_16x16x32_bf16 v[96:99], v[188:191], v[204:207], v[96:99]
	v_mfma_f32_16x16x32_bf16 v[84:87], v[166:169], v[212:215], v[84:87]
	v_mfma_f32_16x16x32_bf16 v[80:83], v[188:191], v[212:215], v[80:83]
	v_mfma_f32_16x16x32_bf16 v[68:71], v[166:169], v[220:223], v[68:71]
	v_mfma_f32_16x16x32_bf16 v[64:67], v[188:191], v[220:223], v[64:67]
	s_setprio 0
	s_barrier
	s_add_i32 s38, s72, s45
	v_lshl_add_u64 v[170:171], v[170:171], 0, s[18:19]
	s_mov_b32 m0, s38
	ds_read_b128 v[192:195], v181 offset:49152
	ds_read_b128 v[196:199], v181 offset:50176
	ds_read_b128 v[200:203], v181 offset:51200
	ds_read_b128 v[204:207], v181 offset:52224
	ds_read_b128 v[208:211], v181 offset:53248
	ds_read_b128 v[212:215], v181 offset:54272
	ds_read_b128 v[216:219], v181 offset:55296
	ds_read_b128 v[220:223], v181 offset:56320
	global_load_lds_dwordx4 v[170:171], off
	s_add_i32 m0, s38, 0x2000
	s_add_u32 s12, s12, 0x40080
	v_lshl_add_u64 v[170:171], v[224:225], 0, s[18:19]
	s_addc_u32 s13, s13, 0
	s_add_i32 s38, s73, s45
	global_load_lds_dwordx4 v[170:171], off
	s_mov_b32 m0, s38
	s_nop 0
	global_load_lds_dwordx4 v130, s[12:13]
	v_lshl_add_u64 v[170:171], s[12:13], 0, v[134:135]
	s_add_i32 m0, s38, 0x2000
	s_nop 0
	global_load_lds_dwordx4 v134, s[12:13]
	v_lshl_add_u64 v[170:171], v[226:227], 0, s[18:19]
	s_mov_b32 m0, s65
	s_nop 0
	global_load_lds_dwordx4 v[170:171], off
	v_lshl_add_u64 v[170:171], v[228:229], 0, s[18:19]
	s_mov_b32 m0, s66
	s_nop 0
	global_load_lds_dwordx4 v[170:171], off
	s_waitcnt vmcnt(8) lgkmcnt(0)
	s_barrier
	s_setprio 1
	v_mfma_f32_16x16x32_bf16 v[60:63], v[146:149], v[192:195], v[60:63]
	v_mfma_f32_16x16x32_bf16 v[56:59], v[154:157], v[192:195], v[56:59]
	v_mfma_f32_16x16x32_bf16 v[44:47], v[146:149], v[200:203], v[44:47]
	v_mfma_f32_16x16x32_bf16 v[40:43], v[154:157], v[200:203], v[40:43]
	v_mfma_f32_16x16x32_bf16 v[28:31], v[146:149], v[208:211], v[28:31]
	v_mfma_f32_16x16x32_bf16 v[24:27], v[154:157], v[208:211], v[24:27]
	v_mfma_f32_16x16x32_bf16 v[12:15], v[146:149], v[216:219], v[12:15]
	v_mfma_f32_16x16x32_bf16 v[8:11], v[154:157], v[216:219], v[8:11]
	v_mfma_f32_16x16x32_bf16 v[60:63], v[150:153], v[196:199], v[60:63]
	v_mfma_f32_16x16x32_bf16 v[56:59], v[158:161], v[196:199], v[56:59]
	v_mfma_f32_16x16x32_bf16 v[44:47], v[150:153], v[204:207], v[44:47]
	v_mfma_f32_16x16x32_bf16 v[40:43], v[158:161], v[204:207], v[40:43]
	v_mfma_f32_16x16x32_bf16 v[28:31], v[150:153], v[212:215], v[28:31]
	v_mfma_f32_16x16x32_bf16 v[24:27], v[158:161], v[212:215], v[24:27]
	v_mfma_f32_16x16x32_bf16 v[12:15], v[150:153], v[220:223], v[12:15]
	v_mfma_f32_16x16x32_bf16 v[8:11], v[158:161], v[220:223], v[8:11]
	s_setprio 0
	s_setprio 1
	v_mfma_f32_16x16x32_bf16 v[52:55], v[162:165], v[192:195], v[52:55]
	v_mfma_f32_16x16x32_bf16 v[48:51], v[184:187], v[192:195], v[48:51]
	v_mfma_f32_16x16x32_bf16 v[36:39], v[162:165], v[200:203], v[36:39]
	v_mfma_f32_16x16x32_bf16 v[32:35], v[184:187], v[200:203], v[32:35]
	v_mfma_f32_16x16x32_bf16 v[20:23], v[162:165], v[208:211], v[20:23]
	v_mfma_f32_16x16x32_bf16 v[16:19], v[184:187], v[208:211], v[16:19]
	v_mfma_f32_16x16x32_bf16 v[4:7], v[162:165], v[216:219], v[4:7]
	v_mfma_f32_16x16x32_bf16 v[0:3], v[184:187], v[216:219], v[0:3]
	v_mfma_f32_16x16x32_bf16 v[52:55], v[166:169], v[196:199], v[52:55]
	v_mfma_f32_16x16x32_bf16 v[48:51], v[188:191], v[196:199], v[48:51]
	v_mfma_f32_16x16x32_bf16 v[36:39], v[166:169], v[204:207], v[36:39]
	v_mfma_f32_16x16x32_bf16 v[32:35], v[188:191], v[204:207], v[32:35]
	v_mfma_f32_16x16x32_bf16 v[20:23], v[166:169], v[212:215], v[20:23]
	v_mfma_f32_16x16x32_bf16 v[16:19], v[188:191], v[212:215], v[16:19]
	v_mfma_f32_16x16x32_bf16 v[4:7], v[166:169], v[220:223], v[4:7]
	v_mfma_f32_16x16x32_bf16 v[0:3], v[188:191], v[220:223], v[0:3]
	s_setprio 0
	s_barrier
	s_add_i32 s71, s71, 2
	s_add_u32 s8, s8, 0x100
	s_addc_u32 s9, s9, 0
	s_add_u32 s40, s40, 0x100
	s_addc_u32 s41, s41, 0
	s_cmp_gt_u32 s71, 13
	s_cbranch_scc0 .LBB0_2049
	s_and_b64 vcc, exec, s[20:21]
	s_cbranch_vccz .LBB0_2052
	s_barrier

; #define PG8_STAGE(bufoff, gbase, voff) do { _Pragma("unroll") for (int _i = 0; _i < 2; ++_i) \
;         __builtin_amdgcn_global_load_lds((const unsigned*)((const char*)(gbase) + (voff)[_i]), (PG8_LAS unsigned*)(lds + (bufoff) + ldsw + _i * 8192), 16, 0, 0); } while (0)
; #define PG8_LDA(dst, b, h) do { _Pragma("unroll") for (int m = 0; m < 4; ++m) _Pragma("unroll") for (int k = 0; k < 2; ++k) dst[m][k] = *(const PG8_LAS bf16x8*)(lds + PG8_SA(b, h) + aoff + m * 2048 + k * 1024); } while (0)
; #define PG8_LDB(dst, b, h) do { _Pragma("unroll") for (int n = 0; n < 2; ++n) _Pragma("unroll") for (int k = 0; k < 2; ++k) dst[n][k] = *(const PG8_LAS bf16x8*)(lds + PG8_SB(b, h) + boff + n * 2048 + k * 1024); } while (0)
; #define PG8_WAIT_V(n) asm volatile("s_waitcnt vmcnt(" #n ")" ::: "memory")
; #define PG8_WAIT_L(n) asm volatile("s_waitcnt lgkmcnt(" #n ")" ::: "memory")
; #define PG8_BAR __builtin_amdgcn_s_barrier()
; #define PG8_SCHED __builtin_amdgcn_sched_barrier(0)
; template <class Epi, class Sched, bool ALIGN_EPI = false, bool SP2 = false>
; __device__ __forceinline__ void gemm_phase(PG8_LAS unsigned char* lds, const Gemm g, const Sched& S, const Epi& E, const int wid) {
;     ...
;         const bool has_next = S.next(ui + 1, nxt);
;         const char* nA = has_next ? (const char*)g.A + (size_t)nxt.pm * tstepA : cA; const char* nB = has_next ? (const char*)g.Bt + (size_t)nxt.pn * tstepB : cB;
;         for (int t = 0; t < nt; t += 2) {
;             const bool last = (t == nt - 2);
;             const char* a1 = cA + (size_t)(t + 1) * kstep;
;             const char* a2 = last ? nA : cA + (size_t)(t + 2) * kstep; const char* b2 = last ? nB : cB + (size_t)(t + 2) * kstep;
;             const char* a3 = a2 + kstep; const char* b3 = b2 + kstep;
;             if (last && has_next) S.a_ready(nxt);
;             if constexpr (SP2) {
;             PG8_LDB(B0, 0, 0); PG8_LDB(B1, 0, 1); PG8_SCHED; PG8_LDA(At, 0, 0); PG8_STAGE(PG8_SA(1, 1), a1 + hstepA, voffA);
;             PG8_WAIT_V(8); PG8_WAIT_L(0); PG8_BAR; PG8_MMA(0, 0, At, B0); PG8_MMA(0, 1, At, B1); PG8_BAR; PG8_SCHED;
;             PG8_LDA(At, 0, 1); PG8_STAGE(PG8_SB(0, 0), b2, voffB); PG8_STAGE(PG8_SB(0, 1), b2 + hstepB, voffB); PG8_STAGE(PG8_SA(0, 0), a2, voffA);
;             PG8_WAIT_V(8); PG8_WAIT_L(0); PG8_BAR; PG8_MMA(1, 0, At, B0); PG8_MMA(1, 1, At, B1); PG8_BAR; PG8_SCHED;
.LBB0_2280:
	s_add_u32 s37, s28, s36
	s_addc_u32 s44, s29, 0
	s_add_u32 s40, s37, 0x100
	s_addc_u32 s41, s44, 0
	s_and_b64 s[38:39], s[34:35], exec
	s_cselect_b32 s39, s19, s41
	s_cselect_b32 s38, s81, s40
	s_add_u32 s36, s26, s36
	s_addc_u32 s40, s27, 0
	s_add_u32 s36, s36, 0x100
	s_addc_u32 s40, s40, 0
	s_and_b64 s[34:35], s[34:35], exec
	s_cselect_b32 s41, s17, s40
	s_cselect_b32 s40, s82, s36
	s_add_u32 s46, s37, 0x80080
	ds_read_b128 v[142:145], v157
	ds_read_b128 v[146:149], v157 offset:1024
	ds_read_b128 v[150:153], v157 offset:2048
	ds_read_b128 v[162:165], v157 offset:3072
	ds_read_b128 v[166:169], v158
	ds_read_b128 v[170:173], v158 offset:1024
	ds_read_b128 v[174:177], v158 offset:2048
	ds_read_b128 v[178:181], v158 offset:3072
	s_addc_u32 s47, s44, 0
	s_add_i32 s93, s77, s0
	s_add_i32 m0, s70, 0xc000
	s_add_i32 s94, s70, 0xe000
	s_add_i32 s89, s93, 0x2000
	s_add_u32 s44, s40, 0x10000
	s_addc_u32 s45, s41, 0
	s_add_i32 s92, s78, s0
	s_add_i32 s91, s92, 0x2000
	s_add_i32 s88, 0, 0x18000
	s_add_i32 s87, 0, 0x1c000
	s_add_u32 s36, s38, 0x80000
	s_addc_u32 s37, s39, 0
	s_add_i32 s86, s88, s0
	s_add_i32 s84, s86, 0x2000
	s_add_u32 s34, s40, 0x10080
	s_addc_u32 s35, s41, 0
	s_add_i32 s85, s87, s0
	s_add_i32 s83, s85, 0x2000
	ds_read_b128 v[182:185], v159
	ds_read_b128 v[186:189], v159 offset:1024
	ds_read_b128 v[190:193], v159 offset:2048
	ds_read_b128 v[194:197], v159 offset:3072
	ds_read_b128 v[198:201], v159 offset:4096
	ds_read_b128 v[202:205], v159 offset:5120
	ds_read_b128 v[206:209], v159 offset:6144
	ds_read_b128 v[210:213], v159 offset:7168
	global_load_lds_dwordx4 v134, s[46:47]
	s_mov_b32 m0, s94
	s_nop 0
	global_load_lds_dwordx4 v130, s[46:47]
	s_waitcnt vmcnt(8) lgkmcnt(0)
	s_barrier
	s_setprio 1
	v_mfma_f32_16x16x32_bf16 v[124:127], v[142:145], v[182:185], v[124:127]
	v_mfma_f32_16x16x32_bf16 v[120:123], v[150:153], v[182:185], v[120:123]
	v_mfma_f32_16x16x32_bf16 v[116:119], v[142:145], v[190:193], v[116:119]
	v_mfma_f32_16x16x32_bf16 v[112:115], v[150:153], v[190:193], v[112:115]
	v_mfma_f32_16x16x32_bf16 v[100:103], v[142:145], v[198:201], v[100:103]
	v_mfma_f32_16x16x32_bf16 v[96:99], v[150:153], v[198:201], v[96:99]
	v_mfma_f32_16x16x32_bf16 v[84:87], v[142:145], v[206:209], v[84:87]
	v_mfma_f32_16x16x32_bf16 v[80:83], v[150:153], v[206:209], v[80:83]
	v_mfma_f32_16x16x32_bf16 v[124:127], v[146:149], v[186:189], v[124:127]
	v_mfma_f32_16x16x32_bf16 v[120:123], v[162:165], v[186:189], v[120:123]
	v_mfma_f32_16x16x32_bf16 v[116:119], v[146:149], v[194:197], v[116:119]
	v_mfma_f32_16x16x32_bf16 v[112:115], v[162:165], v[194:197], v[112:115]
	v_mfma_f32_16x16x32_bf16 v[100:103], v[146:149], v[202:205], v[100:103]
	v_mfma_f32_16x16x32_bf16 v[96:99], v[162:165], v[202:205], v[96:99]
	v_mfma_f32_16x16x32_bf16 v[84:87], v[146:149], v[210:213], v[84:87]
	v_mfma_f32_16x16x32_bf16 v[80:83], v[162:165], v[210:213], v[80:83]
	s_setprio 0
	s_setprio 1
	v_mfma_f32_16x16x32_bf16 v[108:111], v[166:169], v[182:185], v[108:111]
	v_mfma_f32_16x16x32_bf16 v[104:107], v[174:177], v[182:185], v[104:107]
	v_mfma_f32_16x16x32_bf16 v[92:95], v[166:169], v[190:193], v[92:95]
	v_mfma_f32_16x16x32_bf16 v[88:91], v[174:177], v[190:193], v[88:91]
	v_mfma_f32_16x16x32_bf16 v[76:79], v[166:169], v[198:201], v[76:79]
	v_mfma_f32_16x16x32_bf16 v[72:75], v[174:177], v[198:201], v[72:75]
	v_mfma_f32_16x16x32_bf16 v[68:71], v[166:169], v[206:209], v[68:71]
	v_mfma_f32_16x16x32_bf16 v[64:67], v[174:177], v[206:209], v[64:67]
	v_mfma_f32_16x16x32_bf16 v[108:111], v[170:173], v[186:189], v[108:111]
	v_mfma_f32_16x16x32_bf16 v[104:107], v[178:181], v[186:189], v[104:107]
	v_mfma_f32_16x16x32_bf16 v[92:95], v[170:173], v[194:197], v[92:95]
	v_mfma_f32_16x16x32_bf16 v[88:91], v[178:181], v[194:197], v[88:91]
	v_mfma_f32_16x16x32_bf16 v[76:79], v[170:173], v[202:205], v[76:79]
	v_mfma_f32_16x16x32_bf16 v[72:75], v[178:181], v[202:205], v[72:75]
	v_mfma_f32_16x16x32_bf16 v[68:71], v[170:173], v[210:213], v[68:71]
	v_mfma_f32_16x16x32_bf16 v[64:67], v[178:181], v[210:213], v[64:67]
	s_setprio 0
	s_barrier
	s_mov_b32 m0, s93
	v_lshl_add_u64 v[214:215], s[40:41], 0, v[132:133]
	ds_read_b128 v[182:185], v159 offset:16384
	ds_read_b128 v[186:189], v159 offset:17408
	ds_read_b128 v[190:193], v159 offset:18432
	ds_read_b128 v[194:197], v159 offset:19456
	ds_read_b128 v[198:201], v159 offset:20480
	ds_read_b128 v[202:205], v159 offset:21504
	ds_read_b128 v[206:209], v159 offset:22528
	ds_read_b128 v[210:213], v159 offset:23552
	global_load_lds_dwordx4 v132, s[40:41]
	v_lshl_add_u64 v[216:217], s[40:41], 0, v[128:129]
	s_mov_b32 m0, s89
	s_nop 0
	global_load_lds_dwordx4 v128, s[40:41]
	s_mov_b32 m0, s92
	v_lshl_add_u64 v[220:221], s[38:39], 0, v[130:131]
	global_load_lds_dwordx4 v132, s[44:45]
	s_mov_b32 m0, s91
	s_nop 0
	global_load_lds_dwordx4 v128, s[44:45]
	v_lshl_add_u64 v[218:219], s[38:39], 0, v[134:135]
	s_mov_b32 m0, s70
	s_nop 0
	global_load_lds_dwordx4 v134, s[38:39]
	s_mov_b32 m0, s71
	s_nop 0
	global_load_lds_dwordx4 v130, s[38:39]
	s_waitcnt vmcnt(8) lgkmcnt(0)
	s_barrier
; #define PG8_STAGE(bufoff, gbase, voff) do { _Pragma("unroll") for (int _i = 0; _i < 2; ++_i) \
;         __builtin_amdgcn_global_load_lds((const unsigned*)((const char*)(gbase) + (voff)[_i]), (PG8_LAS unsigned*)(lds + (bufoff) + ldsw + _i * 8192), 16, 0, 0); } while (0)
; #define PG8_LDA(dst, b, h) do { _Pragma("unroll") for (int m = 0; m < 4; ++m) _Pragma("unroll") for (int k = 0; k < 2; ++k) dst[m][k] = *(const PG8_LAS bf16x8*)(lds + PG8_SA(b, h) + aoff + m * 2048 + k * 1024); } while (0)
; #define PG8_LDB(dst, b, h) do { _Pragma("unroll") for (int n = 0; n < 2; ++n) _Pragma("unroll") for (int k = 0; k < 2; ++k) dst[n][k] = *(const PG8_LAS bf16x8*)(lds + PG8_SB(b, h) + boff + n * 2048 + k * 1024); } while (0)
; #define PG8_MMA(ai, bj, At, Bt) do { __builtin_amdgcn_s_setprio(1); _Pragma("unroll") for (int m = 0; m < 4; ++m) _Pragma("unroll") for (int n = 0; n < 2; ++n) _Pragma("unroll") for (int k = 0; k < 2; ++k) \
;         acc[ai][bj][m][n] = __builtin_amdgcn_mfma_f32_16x16x32_bf16(Bt[n][k], At[m][k], acc[ai][bj][m][n], 0, 0, 0); __builtin_amdgcn_s_setprio(0); } while (0)
; #define PG8_WAIT_V(n) asm volatile("s_waitcnt vmcnt(" #n ")" ::: "memory")
; #define PG8_WAIT_L(n) asm volatile("s_waitcnt lgkmcnt(" #n ")" ::: "memory")
; #define PG8_BAR __builtin_amdgcn_s_barrier()
; #define PG8_SCHED __builtin_amdgcn_sched_barrier(0)
; template <class Epi, class Sched, bool ALIGN_EPI = false, bool SP2 = false>
; __device__ __forceinline__ void gemm_phase(PG8_LAS unsigned char* lds, const Gemm g, const Sched& S, const Epi& E, const int wid) {
;     ...
;             PG8_WAIT_V(8); PG8_WAIT_L(0); PG8_BAR; PG8_MMA(1, 0, At, B0); PG8_MMA(1, 1, At, B1); PG8_BAR; PG8_SCHED;
;             PG8_LDB(B0, 1, 0); PG8_LDB(B1, 1, 1); PG8_SCHED; PG8_LDA(At, 1, 0); PG8_STAGE(PG8_SA(0, 1), a2 + hstepA, voffA);
;             PG8_WAIT_V(8); PG8_WAIT_L(0); PG8_BAR; PG8_MMA(0, 0, At, B0); PG8_MMA(0, 1, At, B1); PG8_BAR; PG8_SCHED;
	s_setprio 1
	v_mfma_f32_16x16x32_bf16 v[60:63], v[142:145], v[182:185], v[60:63]
	v_mfma_f32_16x16x32_bf16 v[56:59], v[150:153], v[182:185], v[56:59]
	v_mfma_f32_16x16x32_bf16 v[52:55], v[142:145], v[190:193], v[52:55]
	v_mfma_f32_16x16x32_bf16 v[48:51], v[150:153], v[190:193], v[48:51]
	v_mfma_f32_16x16x32_bf16 v[36:39], v[142:145], v[198:201], v[36:39]
	v_mfma_f32_16x16x32_bf16 v[32:35], v[150:153], v[198:201], v[32:35]
	v_mfma_f32_16x16x32_bf16 v[20:23], v[142:145], v[206:209], v[20:23]
	v_mfma_f32_16x16x32_bf16 v[16:19], v[150:153], v[206:209], v[16:19]
	v_mfma_f32_16x16x32_bf16 v[60:63], v[146:149], v[186:189], v[60:63]
	v_mfma_f32_16x16x32_bf16 v[56:59], v[162:165], v[186:189], v[56:59]
	v_mfma_f32_16x16x32_bf16 v[52:55], v[146:149], v[194:197], v[52:55]
	v_mfma_f32_16x16x32_bf16 v[48:51], v[162:165], v[194:197], v[48:51]
	v_mfma_f32_16x16x32_bf16 v[36:39], v[146:149], v[202:205], v[36:39]
	v_mfma_f32_16x16x32_bf16 v[32:35], v[162:165], v[202:205], v[32:35]
	v_mfma_f32_16x16x32_bf16 v[20:23], v[146:149], v[210:213], v[20:23]
	v_mfma_f32_16x16x32_bf16 v[16:19], v[162:165], v[210:213], v[16:19]
	s_setprio 0
	s_setprio 1
	v_mfma_f32_16x16x32_bf16 v[44:47], v[166:169], v[182:185], v[44:47]
	v_mfma_f32_16x16x32_bf16 v[40:43], v[174:177], v[182:185], v[40:43]
	v_mfma_f32_16x16x32_bf16 v[28:31], v[166:169], v[190:193], v[28:31]
	v_mfma_f32_16x16x32_bf16 v[24:27], v[174:177], v[190:193], v[24:27]
	v_mfma_f32_16x16x32_bf16 v[12:15], v[166:169], v[198:201], v[12:15]
	v_mfma_f32_16x16x32_bf16 v[8:11], v[174:177], v[198:201], v[8:11]
	v_mfma_f32_16x16x32_bf16 v[4:7], v[166:169], v[206:209], v[4:7]
	v_mfma_f32_16x16x32_bf16 v[0:3], v[174:177], v[206:209], v[0:3]
	v_mfma_f32_16x16x32_bf16 v[44:47], v[170:173], v[186:189], v[44:47]
	v_mfma_f32_16x16x32_bf16 v[40:43], v[178:181], v[186:189], v[40:43]
	v_mfma_f32_16x16x32_bf16 v[28:31], v[170:173], v[194:197], v[28:31]
	v_mfma_f32_16x16x32_bf16 v[24:27], v[178:181], v[194:197], v[24:27]
	v_mfma_f32_16x16x32_bf16 v[12:15], v[170:173], v[202:205], v[12:15]
	v_mfma_f32_16x16x32_bf16 v[8:11], v[178:181], v[202:205], v[8:11]
	v_mfma_f32_16x16x32_bf16 v[4:7], v[170:173], v[210:213], v[4:7]
	v_mfma_f32_16x16x32_bf16 v[0:3], v[178:181], v[210:213], v[0:3]
	s_setprio 0
	s_barrier
	v_add_u32_e32 v161, s88, v156
	ds_read_b128 v[142:145], v161
	ds_read_b128 v[146:149], v161 offset:1024
	ds_read_b128 v[150:153], v161 offset:2048
	ds_read_b128 v[162:165], v161 offset:3072
	v_add_u32_e32 v161, s87, v156
	ds_read_b128 v[166:169], v161
	ds_read_b128 v[170:173], v161 offset:1024
	ds_read_b128 v[174:177], v161 offset:2048
	ds_read_b128 v[178:181], v161 offset:3072
	s_mov_b32 m0, s72
	ds_read_b128 v[182:185], v159 offset:32768
	ds_read_b128 v[186:189], v159 offset:33792
	ds_read_b128 v[190:193], v159 offset:34816
	ds_read_b128 v[194:197], v159 offset:35840
	ds_read_b128 v[198:201], v159 offset:36864
	ds_read_b128 v[202:205], v159 offset:37888
	ds_read_b128 v[206:209], v159 offset:38912
	ds_read_b128 v[210:213], v159 offset:39936
	global_load_lds_dwordx4 v134, s[36:37]
	s_mov_b32 m0, s73
	s_nop 0
	global_load_lds_dwordx4 v130, s[36:37]
	s_waitcnt vmcnt(8) lgkmcnt(0)
	s_barrier
	s_setprio 1
	v_mfma_f32_16x16x32_bf16 v[124:127], v[142:145], v[182:185], v[124:127]
	v_mfma_f32_16x16x32_bf16 v[120:123], v[150:153], v[182:185], v[120:123]
	v_mfma_f32_16x16x32_bf16 v[116:119], v[142:145], v[190:193], v[116:119]
	v_mfma_f32_16x16x32_bf16 v[112:115], v[150:153], v[190:193], v[112:115]
	v_mfma_f32_16x16x32_bf16 v[100:103], v[142:145], v[198:201], v[100:103]
	v_mfma_f32_16x16x32_bf16 v[96:99], v[150:153], v[198:201], v[96:99]
	v_mfma_f32_16x16x32_bf16 v[84:87], v[142:145], v[206:209], v[84:87]
	v_mfma_f32_16x16x32_bf16 v[80:83], v[150:153], v[206:209], v[80:83]
	v_mfma_f32_16x16x32_bf16 v[124:127], v[146:149], v[186:189], v[124:127]
	v_mfma_f32_16x16x32_bf16 v[120:123], v[162:165], v[186:189], v[120:123]
	v_mfma_f32_16x16x32_bf16 v[116:119], v[146:149], v[194:197], v[116:119]
	v_mfma_f32_16x16x32_bf16 v[112:115], v[162:165], v[194:197], v[112:115]
	v_mfma_f32_16x16x32_bf16 v[100:103], v[146:149], v[202:205], v[100:103]
	v_mfma_f32_16x16x32_bf16 v[96:99], v[162:165], v[202:205], v[96:99]
	v_mfma_f32_16x16x32_bf16 v[84:87], v[146:149], v[210:213], v[84:87]
	v_mfma_f32_16x16x32_bf16 v[80:83], v[162:165], v[210:213], v[80:83]
	s_setprio 0
	s_setprio 1
	v_mfma_f32_16x16x32_bf16 v[108:111], v[166:169], v[182:185], v[108:111]
	v_mfma_f32_16x16x32_bf16 v[104:107], v[174:177], v[182:185], v[104:107]
	v_mfma_f32_16x16x32_bf16 v[92:95], v[166:169], v[190:193], v[92:95]
	v_mfma_f32_16x16x32_bf16 v[88:91], v[174:177], v[190:193], v[88:91]
	v_mfma_f32_16x16x32_bf16 v[76:79], v[166:169], v[198:201], v[76:79]
	v_mfma_f32_16x16x32_bf16 v[72:75], v[174:177], v[198:201], v[72:75]
	v_mfma_f32_16x16x32_bf16 v[68:71], v[166:169], v[206:209], v[68:71]
	v_mfma_f32_16x16x32_bf16 v[64:67], v[174:177], v[206:209], v[64:67]
	v_mfma_f32_16x16x32_bf16 v[108:111], v[170:173], v[186:189], v[108:111]
	v_mfma_f32_16x16x32_bf16 v[104:107], v[178:181], v[186:189], v[104:107]
	v_mfma_f32_16x16x32_bf16 v[92:95], v[170:173], v[194:197], v[92:95]
	v_mfma_f32_16x16x32_bf16 v[88:91], v[178:181], v[194:197], v[88:91]
	v_mfma_f32_16x16x32_bf16 v[76:79], v[170:173], v[202:205], v[76:79]
	v_mfma_f32_16x16x32_bf16 v[72:75], v[178:181], v[202:205], v[72:75]
	v_mfma_f32_16x16x32_bf16 v[68:71], v[170:173], v[210:213], v[68:71]
	v_mfma_f32_16x16x32_bf16 v[64:67], v[178:181], v[210:213], v[64:67]
	s_setprio 0
	s_barrier
; #define PG8_STAGE(bufoff, gbase, voff) do { _Pragma("unroll") for (int _i = 0; _i < 2; ++_i) \
;         __builtin_amdgcn_global_load_lds((const unsigned*)((const char*)(gbase) + (voff)[_i]), (PG8_LAS unsigned*)(lds + (bufoff) + ldsw + _i * 8192), 16, 0, 0); } while (0)
; #define PG8_LDA(dst, b, h) do { _Pragma("unroll") for (int m = 0; m < 4; ++m) _Pragma("unroll") for (int k = 0; k < 2; ++k) dst[m][k] = *(const PG8_LAS bf16x8*)(lds + PG8_SA(b, h) + aoff + m * 2048 + k * 1024); } while (0)
; #define PG8_MMA(ai, bj, At, Bt) do { __builtin_amdgcn_s_setprio(1); _Pragma("unroll") for (int m = 0; m < 4; ++m) _Pragma("unroll") for (int n = 0; n < 2; ++n) _Pragma("unroll") for (int k = 0; k < 2; ++k) \
;         acc[ai][bj][m][n] = __builtin_amdgcn_mfma_f32_16x16x32_bf16(Bt[n][k], At[m][k], acc[ai][bj][m][n], 0, 0, 0); __builtin_amdgcn_s_setprio(0); } while (0)
; #define PG8_WAIT_V(n) asm volatile("s_waitcnt vmcnt(" #n ")" ::: "memory")
; #define PG8_WAIT_L(n) asm volatile("s_waitcnt lgkmcnt(" #n ")" ::: "memory")
; #define PG8_BAR __builtin_amdgcn_s_barrier()
; #define PG8_SCHED __builtin_amdgcn_sched_barrier(0)
; template <class Epi, class Sched, bool ALIGN_EPI = false, bool SP2 = false>
; __device__ __forceinline__ void gemm_phase(PG8_LAS unsigned char* lds, const Gemm g, const Sched& S, const Epi& E, const int wid) {
;     ...
;             PG8_LDA(At, 1, 1); PG8_STAGE(PG8_SB(1, 0), b3, voffB); PG8_STAGE(PG8_SB(1, 1), b3 + hstepB, voffB); PG8_STAGE(PG8_SA(1, 0), a3, voffA);
;             PG8_WAIT_V(8); PG8_WAIT_L(0); PG8_BAR; PG8_MMA(1, 0, At, B0); PG8_MMA(1, 1, At, B1); PG8_BAR; PG8_SCHED;
	s_mov_b32 m0, s86
	v_lshl_add_u64 v[214:215], v[214:215], 0, s[12:13]
	ds_read_b128 v[182:185], v159 offset:49152
	ds_read_b128 v[186:189], v159 offset:50176
	ds_read_b128 v[190:193], v159 offset:51200
	ds_read_b128 v[194:197], v159 offset:52224
	ds_read_b128 v[198:201], v159 offset:53248
	ds_read_b128 v[202:205], v159 offset:54272
	ds_read_b128 v[206:209], v159 offset:55296
	ds_read_b128 v[210:213], v159 offset:56320
	global_load_lds_dwordx4 v[214:215], off
	v_lshl_add_u64 v[214:215], v[216:217], 0, s[12:13]
	s_mov_b32 m0, s84
	s_nop 0
	global_load_lds_dwordx4 v[214:215], off
	s_mov_b32 m0, s85
	s_nop 0
	global_load_lds_dwordx4 v132, s[34:35]
	v_lshl_add_u64 v[214:215], s[34:35], 0, v[128:129]
	s_mov_b32 m0, s83
	s_nop 0
	global_load_lds_dwordx4 v128, s[34:35]
	v_lshl_add_u64 v[214:215], v[218:219], 0, s[12:13]
	s_mov_b32 m0, s74
	s_nop 0
	global_load_lds_dwordx4 v[214:215], off
	v_lshl_add_u64 v[214:215], v[220:221], 0, s[12:13]
	s_mov_b32 m0, s75
	s_nop 0
	global_load_lds_dwordx4 v[214:215], off
	s_waitcnt vmcnt(8) lgkmcnt(0)
	s_barrier
	s_setprio 1
	v_mfma_f32_16x16x32_bf16 v[60:63], v[142:145], v[182:185], v[60:63]
	v_mfma_f32_16x16x32_bf16 v[56:59], v[150:153], v[182:185], v[56:59]
	v_mfma_f32_16x16x32_bf16 v[52:55], v[142:145], v[190:193], v[52:55]
	v_mfma_f32_16x16x32_bf16 v[48:51], v[150:153], v[190:193], v[48:51]
	v_mfma_f32_16x16x32_bf16 v[36:39], v[142:145], v[198:201], v[36:39]
	v_mfma_f32_16x16x32_bf16 v[32:35], v[150:153], v[198:201], v[32:35]
	v_mfma_f32_16x16x32_bf16 v[20:23], v[142:145], v[206:209], v[20:23]
	v_mfma_f32_16x16x32_bf16 v[16:19], v[150:153], v[206:209], v[16:19]
	v_mfma_f32_16x16x32_bf16 v[60:63], v[146:149], v[186:189], v[60:63]
	v_mfma_f32_16x16x32_bf16 v[56:59], v[162:165], v[186:189], v[56:59]
	v_mfma_f32_16x16x32_bf16 v[52:55], v[146:149], v[194:197], v[52:55]
	v_mfma_f32_16x16x32_bf16 v[48:51], v[162:165], v[194:197], v[48:51]
	v_mfma_f32_16x16x32_bf16 v[36:39], v[146:149], v[202:205], v[36:39]
	v_mfma_f32_16x16x32_bf16 v[32:35], v[162:165], v[202:205], v[32:35]
	v_mfma_f32_16x16x32_bf16 v[20:23], v[146:149], v[210:213], v[20:23]
	v_mfma_f32_16x16x32_bf16 v[16:19], v[162:165], v[210:213], v[16:19]
	s_setprio 0
	s_setprio 1
	v_mfma_f32_16x16x32_bf16 v[44:47], v[166:169], v[182:185], v[44:47]
	v_mfma_f32_16x16x32_bf16 v[40:43], v[174:177], v[182:185], v[40:43]
	v_mfma_f32_16x16x32_bf16 v[28:31], v[166:169], v[190:193], v[28:31]
	v_mfma_f32_16x16x32_bf16 v[24:27], v[174:177], v[190:193], v[24:27]
	v_mfma_f32_16x16x32_bf16 v[12:15], v[166:169], v[198:201], v[12:15]
	v_mfma_f32_16x16x32_bf16 v[8:11], v[174:177], v[198:201], v[8:11]
	v_mfma_f32_16x16x32_bf16 v[4:7], v[166:169], v[206:209], v[4:7]
	v_mfma_f32_16x16x32_bf16 v[0:3], v[174:177], v[206:209], v[0:3]
	v_mfma_f32_16x16x32_bf16 v[44:47], v[170:173], v[186:189], v[44:47]
	v_mfma_f32_16x16x32_bf16 v[40:43], v[178:181], v[186:189], v[40:43]
	v_mfma_f32_16x16x32_bf16 v[28:31], v[170:173], v[194:197], v[28:31]
	v_mfma_f32_16x16x32_bf16 v[24:27], v[178:181], v[194:197], v[24:27]
	v_mfma_f32_16x16x32_bf16 v[12:15], v[170:173], v[202:205], v[12:15]
	v_mfma_f32_16x16x32_bf16 v[8:11], v[178:181], v[202:205], v[8:11]
	v_mfma_f32_16x16x32_bf16 v[4:7], v[170:173], v[210:213], v[4:7]
	v_mfma_f32_16x16x32_bf16 v[0:3], v[178:181], v[210:213], v[0:3]
	s_setprio 0
	s_barrier
	s_movk_i32 s36, 0x100
	s_andn2_b64 vcc, exec, s[30:31]
	s_mov_b64 s[34:35], -1
	s_mov_b64 s[30:31], 0
	s_cbranch_vccz .LBB0_2280
	s_and_b64 vcc, exec, s[14:15]
	s_cbranch_vccz .LBB0_2283
	s_barrier

; #define LAS __attribute__((address_space(3)))
; __device__ __forceinline__ unsigned cvt_pk_bf16(float lo, float hi) { unsigned r; asm volatile("v_cvt_pk_bf16_f32 %0, %1, %2" : "=v"(r) : "v"(lo), "v"(hi)); return r; }
; template <int MODE, int DQK, int DV>
; __device__ __forceinline__ void attn_pass(LAS unsigned char* lds, const Tens& T, size_t rowbase, int q0, f32x16 (&o)[DV / 32], float& l_out, const int wave, QPre* qp = nullptr) {
;     ...
;             l += psum;
;             bf16x8 pf[4];
; #pragma unroll
;             for (int kb = 0; kb < 2; ++kb)
; #pragma unroll
;                 for (int s = 0; s < 2; ++s) {
;                     u32x4 w;
;                     w.x = pg8::cvt_pk_bf16(p[kb][8 * s + 0], p[kb][8 * s + 1]); w.y = pg8::cvt_pk_bf16(p[kb][8 * s + 2], p[kb][8 * s + 3]);
;                     w.z = pg8::cvt_pk_bf16(p[kb][8 * s + 4], p[kb][8 * s + 5]); w.w = pg8::cvt_pk_bf16(p[kb][8 * s + 6], p[kb][8 * s + 7]);
;                     pf[2 * kb + s] = __builtin_bit_cast(bf16x8, w);
;                 }
; #pragma unroll
;             for (int db = 0; db < NDB; ++db) {
; #pragma unroll
;                 for (int ks = 0; ks < 4; ++ks) {
;                     const LAS unsigned char* vp = vfa[db] + sl * VSL + sub * VB_T + (16 * ks) * VROW;
;                     const s16x4 lo = __builtin_bit_cast(s16x4, __builtin_amdgcn_ds_read_tr16_b64_v4i16((LAS s16x4*)(vp)));
;                     const s16x4 hi = __builtin_bit_cast(s16x4, __builtin_amdgcn_ds_read_tr16_b64_v4i16((LAS s16x4*)(vp + 8 * VROW)));
;                     const bf16x8 a = {lo[0], lo[1], lo[2], lo[3], hi[0], hi[1], hi[2], hi[3]};
;                     o[db] = __builtin_amdgcn_mfma_f32_32x32x16_bf16(a, pf[ks], o[db], 0, 0, 0);
;                 }
;             }
.LBB0_2439:
	v_cvt_pk_bf16_f32 v116, v13, v15
	v_cvt_pk_bf16_f32 v117, v97, v99
	v_cvt_pk_bf16_f32 v118, v112, v113
	v_cvt_pk_bf16_f32 v119, v114, v115
	v_cvt_pk_bf16_f32 v104, v103, v104
	v_cvt_pk_bf16_f32 v105, v105, v106
	v_cvt_pk_bf16_f32 v106, v107, v108
	v_cvt_pk_bf16_f32 v107, v109, v110
	v_cvt_pk_bf16_f32 v4, v3, v4
	v_cvt_pk_bf16_f32 v5, v5, v6
	v_cvt_pk_bf16_f32 v6, v7, v8
	v_cvt_pk_bf16_f32 v7, v9, v11
	v_cvt_pk_bf16_f32 v8, v10, v12
	v_cvt_pk_bf16_f32 v9, v14, v96
	v_cvt_pk_bf16_f32 v10, v98, v100
	v_cvt_pk_bf16_f32 v11, v101, v102
	s_waitcnt lgkmcnt(0)
	ds_read_b64_tr_b16 v[220:221], v161 offset:49152
	ds_read_b64_tr_b16 v[222:223], v161 offset:51200
	ds_read_b64_tr_b16 v[224:225], v161 offset:53248
	ds_read_b64_tr_b16 v[226:227], v161 offset:55296
	ds_read_b64_tr_b16 v[228:229], v161 offset:57344
	ds_read_b64_tr_b16 v[230:231], v161 offset:59392
	ds_read_b64_tr_b16 v[232:233], v161 offset:61440
	ds_read_b64_tr_b16 v[234:235], v161 offset:63488
	ds_read_b64_tr_b16 v[236:237], v162 offset:49152
	ds_read_b64_tr_b16 v[238:239], v162 offset:51200
	ds_read_b64_tr_b16 v[240:241], v162 offset:53248
	ds_read_b64_tr_b16 v[242:243], v162 offset:55296
	ds_read_b64_tr_b16 v[244:245], v162 offset:57344
	ds_read_b64_tr_b16 v[246:247], v162 offset:59392
	ds_read_b64_tr_b16 v[248:249], v162 offset:61440
	ds_read_b64_tr_b16 v[250:251], v162 offset:63488
	v_mfma_f32_32x32x16_bf16 v[16:31], v[188:191], v[116:119], v[16:31]
	v_add_f32_e32 v165, v165, v2
	v_mfma_f32_32x32x16_bf16 v[16:31], v[192:195], v[104:107], v[16:31]
	v_mfma_f32_32x32x16_bf16 v[16:31], v[196:199], v[4:7], v[16:31]
	v_mfma_f32_32x32x16_bf16 v[16:31], v[200:203], v[8:11], v[16:31]
	v_mfma_f32_32x32x16_bf16 v[64:79], v[204:207], v[116:119], v[64:79]
	v_mfma_f32_32x32x16_bf16 v[64:79], v[208:211], v[104:107], v[64:79]
	v_mfma_f32_32x32x16_bf16 v[64:79], v[212:215], v[4:7], v[64:79]
	v_mfma_f32_32x32x16_bf16 v[64:79], v[216:219], v[8:11], v[64:79]
	s_waitcnt lgkmcnt(8)
	v_mfma_f32_32x32x16_bf16 v[48:63], v[220:223], v[116:119], v[48:63]
	v_mfma_f32_32x32x16_bf16 v[48:63], v[224:227], v[104:107], v[48:63]
	v_mfma_f32_32x32x16_bf16 v[48:63], v[228:231], v[4:7], v[48:63]
	v_mfma_f32_32x32x16_bf16 v[48:63], v[232:235], v[8:11], v[48:63]
	s_waitcnt lgkmcnt(0)
	v_mfma_f32_32x32x16_bf16 v[32:47], v[236:239], v[116:119], v[32:47]
	v_mfma_f32_32x32x16_bf16 v[32:47], v[240:243], v[104:107], v[32:47]
	v_mfma_f32_32x32x16_bf16 v[32:47], v[244:247], v[4:7], v[32:47]
	v_mfma_f32_32x32x16_bf16 v[32:47], v[248:251], v[8:11], v[32:47]

; #define LAS __attribute__((address_space(3)))
; template <int MODE, int DQK, int DV>
; __device__ __forceinline__ void attn_pass(LAS unsigned char* lds, const Tens& T, size_t rowbase, int q0, f32x16 (&o)[DV / 32], float& l_out, const int wave, QPre* qp = nullptr) {
;     ...
; #pragma unroll
;                 for (int s = 0; s < NSTEP; ++s) {
;                     bf16x8 a;
;                     if (s < 4) a = *(const LAS bf16x8*)(kfa[s] + sl * KSL + sub * KB_T + kb * 4096);
;                     else       a = *(const LAS bf16x8*)(kfa[s] + sl * KSL + sub * KB_T + kb * 2048);
;                     if ((MODE == AM_DIFF || MODE == AM_MLA) && s == 0)
;                         asm("v_mfma_f32_32x32x16_bf16 %0, %1, %2, %3" : "=&v"(p[kb]) : "v"(a), "v"(qf[0]), "v"(negm));
;                     else
;                         p[kb] = __builtin_amdgcn_mfma_f32_32x32x16_bf16(a, qf[s], p[kb], 0, 0, 0);
;                 }
;     ...
; #pragma unroll
;             for (int db = 0; db < NDB; ++db) {
; #pragma unroll
;                 for (int ks = 0; ks < 4; ++ks) {
;                     const LAS unsigned char* vp = vfa[db] + sl * VSL + sub * VB_T + (16 * ks) * VROW;
;                     const s16x4 lo = __builtin_bit_cast(s16x4, __builtin_amdgcn_ds_read_tr16_b64_v4i16((LAS s16x4*)(vp)));
;                     const s16x4 hi = __builtin_bit_cast(s16x4, __builtin_amdgcn_ds_read_tr16_b64_v4i16((LAS s16x4*)(vp + 8 * VROW)));
;                     const bf16x8 a = {lo[0], lo[1], lo[2], lo[3], hi[0], hi[1], hi[2], hi[3]};
;                     o[db] = __builtin_amdgcn_mfma_f32_32x32x16_bf16(a, pf[ks], o[db], 0, 0, 0);
;                 }
.LBB0_2447:
	ds_read_b128 v[2:5], v156
	ds_read_b128 v[6:9], v155
	ds_read_b128 v[10:13], v155 offset:4096
	ds_read_b128 v[168:171], v156 offset:4096
	s_andn2_b64 vcc, exec, s[70:71]
	s_waitcnt lgkmcnt(2)
	v_mfma_f32_32x32x16_bf16 v[96:111], v[6:9], v[128:131], v[80:95]
	s_waitcnt lgkmcnt(1)
	v_mfma_f32_32x32x16_bf16 v[112:127], v[10:13], v[128:131], v[80:95]
	v_mfma_f32_32x32x16_bf16 v[96:111], v[2:5], v[132:135], v[96:111]
	ds_read_b128 v[2:5], v157
	ds_read_b128 v[6:9], v157 offset:4096
	s_waitcnt lgkmcnt(2)
	v_mfma_f32_32x32x16_bf16 v[112:127], v[168:171], v[132:135], v[112:127]
	s_waitcnt lgkmcnt(1)
	v_mfma_f32_32x32x16_bf16 v[96:111], v[2:5], v[136:139], v[96:111]
	ds_read_b128 v[2:5], v158
	ds_read_b128 v[172:175], v158 offset:4096
	s_waitcnt lgkmcnt(2)
	v_mfma_f32_32x32x16_bf16 v[112:127], v[6:9], v[136:139], v[112:127]
	s_waitcnt lgkmcnt(1)
	v_mfma_f32_32x32x16_bf16 v[96:111], v[2:5], v[140:143], v[96:111]
	s_waitcnt lgkmcnt(0)
	v_mfma_f32_32x32x16_bf16 v[112:127], v[172:175], v[140:143], v[112:127]
	ds_read_b64_tr_b16 v[188:189], v159
	ds_read_b64_tr_b16 v[190:191], v159 offset:2048
	ds_read_b64_tr_b16 v[192:193], v159 offset:4096
	ds_read_b64_tr_b16 v[194:195], v159 offset:6144
	ds_read_b64_tr_b16 v[196:197], v159 offset:8192
	ds_read_b64_tr_b16 v[198:199], v159 offset:10240
	ds_read_b64_tr_b16 v[200:201], v159 offset:12288
	ds_read_b64_tr_b16 v[202:203], v159 offset:14336
	ds_read_b64_tr_b16 v[204:205], v160
	ds_read_b64_tr_b16 v[206:207], v160 offset:2048
	ds_read_b64_tr_b16 v[208:209], v160 offset:4096
	ds_read_b64_tr_b16 v[210:211], v160 offset:6144
	ds_read_b64_tr_b16 v[212:213], v160 offset:8192
	ds_read_b64_tr_b16 v[214:215], v160 offset:10240
	ds_read_b64_tr_b16 v[216:217], v160 offset:12288
	ds_read_b64_tr_b16 v[218:219], v160 offset:14336
	s_cbranch_vccz .LBB0_2453
	s_andn2_b64 vcc, exec, s[68:69]
	s_cbranch_vccz .LBB0_2454

; #define LAS __attribute__((address_space(3)))
; __device__ __forceinline__ unsigned cvt_pk_bf16(float lo, float hi) { unsigned r; asm volatile("v_cvt_pk_bf16_f32 %0, %1, %2" : "=v"(r) : "v"(lo), "v"(hi)); return r; }
; template <int MODE, int DQK, int DV>
; __device__ __forceinline__ void attn_pass(LAS unsigned char* lds, const Tens& T, size_t rowbase, int q0, f32x16 (&o)[DV / 32], float& l_out, const int wave, QPre* qp = nullptr) {
;     ...
;             l += psum;
;             bf16x8 pf[4];
; #pragma unroll
;             for (int kb = 0; kb < 2; ++kb)
; #pragma unroll
;                 for (int s = 0; s < 2; ++s) {
;                     u32x4 w;
;                     w.x = pg8::cvt_pk_bf16(p[kb][8 * s + 0], p[kb][8 * s + 1]); w.y = pg8::cvt_pk_bf16(p[kb][8 * s + 2], p[kb][8 * s + 3]);
;                     w.z = pg8::cvt_pk_bf16(p[kb][8 * s + 4], p[kb][8 * s + 5]); w.w = pg8::cvt_pk_bf16(p[kb][8 * s + 6], p[kb][8 * s + 7]);
;                     pf[2 * kb + s] = __builtin_bit_cast(bf16x8, w);
;                 }
; #pragma unroll
;             for (int db = 0; db < NDB; ++db) {
; #pragma unroll
;                 for (int ks = 0; ks < 4; ++ks) {
;                     const LAS unsigned char* vp = vfa[db] + sl * VSL + sub * VB_T + (16 * ks) * VROW;
;                     const s16x4 lo = __builtin_bit_cast(s16x4, __builtin_amdgcn_ds_read_tr16_b64_v4i16((LAS s16x4*)(vp)));
;                     const s16x4 hi = __builtin_bit_cast(s16x4, __builtin_amdgcn_ds_read_tr16_b64_v4i16((LAS s16x4*)(vp + 8 * VROW)));
;                     const bf16x8 a = {lo[0], lo[1], lo[2], lo[3], hi[0], hi[1], hi[2], hi[3]};
;                     o[db] = __builtin_amdgcn_mfma_f32_32x32x16_bf16(a, pf[ks], o[db], 0, 0, 0);
;                 }
;             }
.LBB0_2455:
	v_cvt_pk_bf16_f32 v116, v13, v15
	v_cvt_pk_bf16_f32 v117, v97, v99
	v_cvt_pk_bf16_f32 v118, v112, v113
	v_cvt_pk_bf16_f32 v119, v114, v115
	v_cvt_pk_bf16_f32 v104, v103, v104
	v_cvt_pk_bf16_f32 v105, v105, v106
	v_cvt_pk_bf16_f32 v106, v107, v108
	v_cvt_pk_bf16_f32 v107, v109, v110
	v_cvt_pk_bf16_f32 v4, v3, v4
	v_cvt_pk_bf16_f32 v5, v5, v6
	v_cvt_pk_bf16_f32 v6, v7, v8
	v_cvt_pk_bf16_f32 v7, v9, v11
	v_cvt_pk_bf16_f32 v8, v10, v12
	v_cvt_pk_bf16_f32 v9, v14, v96
	v_cvt_pk_bf16_f32 v10, v98, v100
	v_cvt_pk_bf16_f32 v11, v101, v102
	s_waitcnt lgkmcnt(0)
	ds_read_b64_tr_b16 v[220:221], v161
	ds_read_b64_tr_b16 v[222:223], v161 offset:2048
	ds_read_b64_tr_b16 v[224:225], v161 offset:4096
	ds_read_b64_tr_b16 v[226:227], v161 offset:6144
	ds_read_b64_tr_b16 v[228:229], v161 offset:8192
	ds_read_b64_tr_b16 v[230:231], v161 offset:10240
	ds_read_b64_tr_b16 v[232:233], v161 offset:12288
	ds_read_b64_tr_b16 v[234:235], v161 offset:14336
	ds_read_b64_tr_b16 v[236:237], v162
	ds_read_b64_tr_b16 v[238:239], v162 offset:2048
	ds_read_b64_tr_b16 v[240:241], v162 offset:4096
	ds_read_b64_tr_b16 v[242:243], v162 offset:6144
	ds_read_b64_tr_b16 v[244:245], v162 offset:8192
	ds_read_b64_tr_b16 v[246:247], v162 offset:10240
	ds_read_b64_tr_b16 v[248:249], v162 offset:12288
	ds_read_b64_tr_b16 v[250:251], v162 offset:14336
	v_mfma_f32_32x32x16_bf16 v[16:31], v[188:191], v[116:119], v[16:31]
	v_add_f32_e32 v165, v165, v2
	v_mfma_f32_32x32x16_bf16 v[16:31], v[192:195], v[104:107], v[16:31]
	v_mfma_f32_32x32x16_bf16 v[16:31], v[196:199], v[4:7], v[16:31]
	v_mfma_f32_32x32x16_bf16 v[16:31], v[200:203], v[8:11], v[16:31]
	v_mfma_f32_32x32x16_bf16 v[64:79], v[204:207], v[116:119], v[64:79]
	v_mfma_f32_32x32x16_bf16 v[64:79], v[208:211], v[104:107], v[64:79]
	v_mfma_f32_32x32x16_bf16 v[64:79], v[212:215], v[4:7], v[64:79]
	v_mfma_f32_32x32x16_bf16 v[64:79], v[216:219], v[8:11], v[64:79]
	s_waitcnt lgkmcnt(8)
	v_mfma_f32_32x32x16_bf16 v[48:63], v[220:223], v[116:119], v[48:63]
	v_mfma_f32_32x32x16_bf16 v[48:63], v[224:227], v[104:107], v[48:63]
	v_mfma_f32_32x32x16_bf16 v[48:63], v[228:231], v[4:7], v[48:63]
	v_mfma_f32_32x32x16_bf16 v[48:63], v[232:235], v[8:11], v[48:63]
	s_waitcnt lgkmcnt(0)
	v_mfma_f32_32x32x16_bf16 v[32:47], v[236:239], v[116:119], v[32:47]
	v_mfma_f32_32x32x16_bf16 v[32:47], v[240:243], v[104:107], v[32:47]
	v_mfma_f32_32x32x16_bf16 v[32:47], v[244:247], v[4:7], v[32:47]
	v_mfma_f32_32x32x16_bf16 v[32:47], v[248:251], v[8:11], v[32:47]
	s_cmp_ge_u32 s34, s83
	s_cbranch_scc1 .LBB0_2467

; #define LAS __attribute__((address_space(3)))
; template <int MODE, int DQK, int DV>
; __device__ __forceinline__ void attn_pass(LAS unsigned char* lds, const Tens& T, size_t rowbase, int q0, f32x16 (&o)[DV / 32], float& l_out, const int wave, QPre* qp = nullptr) {
;     ...
; #pragma unroll
;                 for (int s = 0; s < NSTEP; ++s) {
;                     bf16x8 a;
;                     if (s < 4) a = *(const LAS bf16x8*)(kfa[s] + sl * KSL + sub * KB_T + kb * 4096);
;                     else       a = *(const LAS bf16x8*)(kfa[s] + sl * KSL + sub * KB_T + kb * 2048);
;                     if ((MODE == AM_DIFF || MODE == AM_MLA) && s == 0)
;                         asm("v_mfma_f32_32x32x16_bf16 %0, %1, %2, %3" : "=&v"(p[kb]) : "v"(a), "v"(qf[0]), "v"(negm));
;                     else
;                         p[kb] = __builtin_amdgcn_mfma_f32_32x32x16_bf16(a, qf[s], p[kb], 0, 0, 0);
;                 }
;     ...
; #pragma unroll
;             for (int db = 0; db < NDB; ++db) {
; #pragma unroll
;                 for (int ks = 0; ks < 4; ++ks) {
;                     const LAS unsigned char* vp = vfa[db] + sl * VSL + sub * VB_T + (16 * ks) * VROW;
;                     const s16x4 lo = __builtin_bit_cast(s16x4, __builtin_amdgcn_ds_read_tr16_b64_v4i16((LAS s16x4*)(vp)));
;                     const s16x4 hi = __builtin_bit_cast(s16x4, __builtin_amdgcn_ds_read_tr16_b64_v4i16((LAS s16x4*)(vp + 8 * VROW)));
;                     const bf16x8 a = {lo[0], lo[1], lo[2], lo[3], hi[0], hi[1], hi[2], hi[3]};
;                     o[db] = __builtin_amdgcn_mfma_f32_32x32x16_bf16(a, pf[ks], o[db], 0, 0, 0);
;                 }
.LBB0_2458:
	ds_read_b128 v[2:5], v156 offset:8192
	ds_read_b128 v[6:9], v155 offset:8192
	ds_read_b128 v[10:13], v155 offset:12288
	ds_read_b128 v[168:171], v156 offset:12288
	s_andn2_b64 vcc, exec, s[70:71]
	s_waitcnt lgkmcnt(2)
	v_mfma_f32_32x32x16_bf16 v[96:111], v[6:9], v[128:131], v[80:95]
	s_waitcnt lgkmcnt(1)
	v_mfma_f32_32x32x16_bf16 v[112:127], v[10:13], v[128:131], v[80:95]
	v_mfma_f32_32x32x16_bf16 v[96:111], v[2:5], v[132:135], v[96:111]
	ds_read_b128 v[2:5], v157 offset:8192
	ds_read_b128 v[6:9], v157 offset:12288
	s_waitcnt lgkmcnt(2)
	v_mfma_f32_32x32x16_bf16 v[112:127], v[168:171], v[132:135], v[112:127]
	s_waitcnt lgkmcnt(1)
	v_mfma_f32_32x32x16_bf16 v[96:111], v[2:5], v[136:139], v[96:111]
	ds_read_b128 v[2:5], v158 offset:8192
	ds_read_b128 v[172:175], v158 offset:12288
	s_waitcnt lgkmcnt(2)
	v_mfma_f32_32x32x16_bf16 v[112:127], v[6:9], v[136:139], v[112:127]
	s_waitcnt lgkmcnt(1)
	v_mfma_f32_32x32x16_bf16 v[96:111], v[2:5], v[140:143], v[96:111]
	s_waitcnt lgkmcnt(0)
	v_mfma_f32_32x32x16_bf16 v[112:127], v[172:175], v[140:143], v[112:127]
	ds_read_b64_tr_b16 v[188:189], v159 offset:16384
	ds_read_b64_tr_b16 v[190:191], v159 offset:18432
	ds_read_b64_tr_b16 v[192:193], v159 offset:20480
	ds_read_b64_tr_b16 v[194:195], v159 offset:22528
	ds_read_b64_tr_b16 v[196:197], v159 offset:24576
	ds_read_b64_tr_b16 v[198:199], v159 offset:26624
	ds_read_b64_tr_b16 v[200:201], v159 offset:28672
	ds_read_b64_tr_b16 v[202:203], v159 offset:30720
	ds_read_b64_tr_b16 v[204:205], v160 offset:16384
	ds_read_b64_tr_b16 v[206:207], v160 offset:18432
	ds_read_b64_tr_b16 v[208:209], v160 offset:20480
	ds_read_b64_tr_b16 v[210:211], v160 offset:22528
	ds_read_b64_tr_b16 v[212:213], v160 offset:24576
	ds_read_b64_tr_b16 v[214:215], v160 offset:26624
	ds_read_b64_tr_b16 v[216:217], v160 offset:28672
	ds_read_b64_tr_b16 v[218:219], v160 offset:30720
	s_cbranch_vccz .LBB0_2464
	s_andn2_b64 vcc, exec, s[68:69]
	s_cbranch_vccz .LBB0_2465

; #define LAS __attribute__((address_space(3)))
; __device__ __forceinline__ unsigned cvt_pk_bf16(float lo, float hi) { unsigned r; asm volatile("v_cvt_pk_bf16_f32 %0, %1, %2" : "=v"(r) : "v"(lo), "v"(hi)); return r; }
; template <int MODE, int DQK, int DV>
; __device__ __forceinline__ void attn_pass(LAS unsigned char* lds, const Tens& T, size_t rowbase, int q0, f32x16 (&o)[DV / 32], float& l_out, const int wave, QPre* qp = nullptr) {
;     ...
;             l += psum;
;             bf16x8 pf[4];
; #pragma unroll
;             for (int kb = 0; kb < 2; ++kb)
; #pragma unroll
;                 for (int s = 0; s < 2; ++s) {
;                     u32x4 w;
;                     w.x = pg8::cvt_pk_bf16(p[kb][8 * s + 0], p[kb][8 * s + 1]); w.y = pg8::cvt_pk_bf16(p[kb][8 * s + 2], p[kb][8 * s + 3]);
;                     w.z = pg8::cvt_pk_bf16(p[kb][8 * s + 4], p[kb][8 * s + 5]); w.w = pg8::cvt_pk_bf16(p[kb][8 * s + 6], p[kb][8 * s + 7]);
;                     pf[2 * kb + s] = __builtin_bit_cast(bf16x8, w);
;                 }
; #pragma unroll
;             for (int db = 0; db < NDB; ++db) {
; #pragma unroll
;                 for (int ks = 0; ks < 4; ++ks) {
;                     const LAS unsigned char* vp = vfa[db] + sl * VSL + sub * VB_T + (16 * ks) * VROW;
;                     const s16x4 lo = __builtin_bit_cast(s16x4, __builtin_amdgcn_ds_read_tr16_b64_v4i16((LAS s16x4*)(vp)));
;                     const s16x4 hi = __builtin_bit_cast(s16x4, __builtin_amdgcn_ds_read_tr16_b64_v4i16((LAS s16x4*)(vp + 8 * VROW)));
;                     const bf16x8 a = {lo[0], lo[1], lo[2], lo[3], hi[0], hi[1], hi[2], hi[3]};
;                     o[db] = __builtin_amdgcn_mfma_f32_32x32x16_bf16(a, pf[ks], o[db], 0, 0, 0);
;                 }
;             }
.LBB0_2466:
	v_cvt_pk_bf16_f32 v116, v13, v15
	v_cvt_pk_bf16_f32 v117, v97, v99
	v_cvt_pk_bf16_f32 v118, v112, v113
	v_cvt_pk_bf16_f32 v119, v114, v115
	v_cvt_pk_bf16_f32 v104, v103, v104
	v_cvt_pk_bf16_f32 v105, v105, v106
	v_cvt_pk_bf16_f32 v106, v107, v108
	v_cvt_pk_bf16_f32 v107, v109, v110
	v_cvt_pk_bf16_f32 v4, v3, v4
	v_cvt_pk_bf16_f32 v5, v5, v6
	v_cvt_pk_bf16_f32 v6, v7, v8
	v_cvt_pk_bf16_f32 v7, v9, v11
	v_cvt_pk_bf16_f32 v8, v10, v12
	v_cvt_pk_bf16_f32 v9, v14, v96
	v_cvt_pk_bf16_f32 v10, v98, v100
	v_cvt_pk_bf16_f32 v11, v101, v102
	s_waitcnt lgkmcnt(0)
	ds_read_b64_tr_b16 v[220:221], v161 offset:16384
	ds_read_b64_tr_b16 v[222:223], v161 offset:18432
	ds_read_b64_tr_b16 v[224:225], v161 offset:20480
	ds_read_b64_tr_b16 v[226:227], v161 offset:22528
	ds_read_b64_tr_b16 v[228:229], v161 offset:24576
	ds_read_b64_tr_b16 v[230:231], v161 offset:26624
	ds_read_b64_tr_b16 v[232:233], v161 offset:28672
	ds_read_b64_tr_b16 v[234:235], v161 offset:30720
	ds_read_b64_tr_b16 v[236:237], v162 offset:16384
	ds_read_b64_tr_b16 v[238:239], v162 offset:18432
	ds_read_b64_tr_b16 v[240:241], v162 offset:20480
	ds_read_b64_tr_b16 v[242:243], v162 offset:22528
	ds_read_b64_tr_b16 v[244:245], v162 offset:24576
	ds_read_b64_tr_b16 v[246:247], v162 offset:26624
	ds_read_b64_tr_b16 v[248:249], v162 offset:28672
	ds_read_b64_tr_b16 v[250:251], v162 offset:30720
	v_mfma_f32_32x32x16_bf16 v[16:31], v[188:191], v[116:119], v[16:31]
	v_add_f32_e32 v165, v165, v2
	v_mfma_f32_32x32x16_bf16 v[16:31], v[192:195], v[104:107], v[16:31]
	v_mfma_f32_32x32x16_bf16 v[16:31], v[196:199], v[4:7], v[16:31]
	v_mfma_f32_32x32x16_bf16 v[16:31], v[200:203], v[8:11], v[16:31]
	v_mfma_f32_32x32x16_bf16 v[64:79], v[204:207], v[116:119], v[64:79]
	v_mfma_f32_32x32x16_bf16 v[64:79], v[208:211], v[104:107], v[64:79]
	v_mfma_f32_32x32x16_bf16 v[64:79], v[212:215], v[4:7], v[64:79]
	v_mfma_f32_32x32x16_bf16 v[64:79], v[216:219], v[8:11], v[64:79]
	s_waitcnt lgkmcnt(8)
	v_mfma_f32_32x32x16_bf16 v[48:63], v[220:223], v[116:119], v[48:63]
	v_mfma_f32_32x32x16_bf16 v[48:63], v[224:227], v[104:107], v[48:63]
	v_mfma_f32_32x32x16_bf16 v[48:63], v[228:231], v[4:7], v[48:63]
	v_mfma_f32_32x32x16_bf16 v[48:63], v[232:235], v[8:11], v[48:63]
	s_waitcnt lgkmcnt(0)
	v_mfma_f32_32x32x16_bf16 v[32:47], v[236:239], v[116:119], v[32:47]
	v_mfma_f32_32x32x16_bf16 v[32:47], v[240:243], v[104:107], v[32:47]
	v_mfma_f32_32x32x16_bf16 v[32:47], v[244:247], v[4:7], v[32:47]
	v_mfma_f32_32x32x16_bf16 v[32:47], v[248:251], v[8:11], v[32:47]

; #define LAS __attribute__((address_space(3)))
; template <int MODE, int DQK, int DV>
; __device__ __forceinline__ void attn_pass(LAS unsigned char* lds, const Tens& T, size_t rowbase, int q0, f32x16 (&o)[DV / 32], float& l_out, const int wave, QPre* qp = nullptr) {
;     ...
; #pragma unroll
;                 for (int s = 0; s < NSTEP; ++s) {
;                     bf16x8 a;
;                     if (s < 4) a = *(const LAS bf16x8*)(kfa[s] + sl * KSL + sub * KB_T + kb * 4096);
;                     else       a = *(const LAS bf16x8*)(kfa[s] + sl * KSL + sub * KB_T + kb * 2048);
;                     if ((MODE == AM_DIFF || MODE == AM_MLA) && s == 0)
;                         asm("v_mfma_f32_32x32x16_bf16 %0, %1, %2, %3" : "=&v"(p[kb]) : "v"(a), "v"(qf[0]), "v"(negm));
;                     else
;                         p[kb] = __builtin_amdgcn_mfma_f32_32x32x16_bf16(a, qf[s], p[kb], 0, 0, 0);
;                 }
;     ...
; #pragma unroll
;             for (int db = 0; db < NDB; ++db) {
; #pragma unroll
;                 for (int ks = 0; ks < 4; ++ks) {
;                     const LAS unsigned char* vp = vfa[db] + sl * VSL + sub * VB_T + (16 * ks) * VROW;
;                     const s16x4 lo = __builtin_bit_cast(s16x4, __builtin_amdgcn_ds_read_tr16_b64_v4i16((LAS s16x4*)(vp)));
;                     const s16x4 hi = __builtin_bit_cast(s16x4, __builtin_amdgcn_ds_read_tr16_b64_v4i16((LAS s16x4*)(vp + 8 * VROW)));
;                     const bf16x8 a = {lo[0], lo[1], lo[2], lo[3], hi[0], hi[1], hi[2], hi[3]};
;                     o[db] = __builtin_amdgcn_mfma_f32_32x32x16_bf16(a, pf[ks], o[db], 0, 0, 0);
;                 }
.LBB0_2475:
	ds_read_b128 v[2:5], v156 offset:16384
	ds_read_b128 v[6:9], v155 offset:16384
	ds_read_b128 v[10:13], v155 offset:20480
	ds_read_b128 v[168:171], v156 offset:20480
	s_andn2_b64 vcc, exec, s[70:71]
	s_waitcnt lgkmcnt(2)
	v_mfma_f32_32x32x16_bf16 v[96:111], v[6:9], v[128:131], v[80:95]
	s_waitcnt lgkmcnt(1)
	v_mfma_f32_32x32x16_bf16 v[112:127], v[10:13], v[128:131], v[80:95]
	v_mfma_f32_32x32x16_bf16 v[96:111], v[2:5], v[132:135], v[96:111]
	ds_read_b128 v[2:5], v157 offset:16384
	ds_read_b128 v[6:9], v157 offset:20480
	s_waitcnt lgkmcnt(2)
	v_mfma_f32_32x32x16_bf16 v[112:127], v[168:171], v[132:135], v[112:127]
	s_waitcnt lgkmcnt(1)
	v_mfma_f32_32x32x16_bf16 v[96:111], v[2:5], v[136:139], v[96:111]
	ds_read_b128 v[2:5], v158 offset:16384
	ds_read_b128 v[172:175], v158 offset:20480
	s_waitcnt lgkmcnt(2)
	v_mfma_f32_32x32x16_bf16 v[112:127], v[6:9], v[136:139], v[112:127]
	s_waitcnt lgkmcnt(1)
	v_mfma_f32_32x32x16_bf16 v[96:111], v[2:5], v[140:143], v[96:111]
	s_waitcnt lgkmcnt(0)
	v_mfma_f32_32x32x16_bf16 v[112:127], v[172:175], v[140:143], v[112:127]
	ds_read_b64_tr_b16 v[188:189], v159 offset:32768
	ds_read_b64_tr_b16 v[190:191], v159 offset:34816
	ds_read_b64_tr_b16 v[192:193], v159 offset:36864
	ds_read_b64_tr_b16 v[194:195], v159 offset:38912
	ds_read_b64_tr_b16 v[196:197], v159 offset:40960
	ds_read_b64_tr_b16 v[198:199], v159 offset:43008
	ds_read_b64_tr_b16 v[200:201], v159 offset:45056
	ds_read_b64_tr_b16 v[202:203], v159 offset:47104
	ds_read_b64_tr_b16 v[204:205], v160 offset:32768
	ds_read_b64_tr_b16 v[206:207], v160 offset:34816
	ds_read_b64_tr_b16 v[208:209], v160 offset:36864
	ds_read_b64_tr_b16 v[210:211], v160 offset:38912
	ds_read_b64_tr_b16 v[212:213], v160 offset:40960
	ds_read_b64_tr_b16 v[214:215], v160 offset:43008
	ds_read_b64_tr_b16 v[216:217], v160 offset:45056
	ds_read_b64_tr_b16 v[218:219], v160 offset:47104
	s_cbranch_vccz .LBB0_2481
	s_andn2_b64 vcc, exec, s[68:69]
	s_cbranch_vccz .LBB0_2482

; #define LAS __attribute__((address_space(3)))
; __device__ __forceinline__ unsigned cvt_pk_bf16(float lo, float hi) { unsigned r; asm volatile("v_cvt_pk_bf16_f32 %0, %1, %2" : "=v"(r) : "v"(lo), "v"(hi)); return r; }
; template <int MODE, int DQK, int DV>
; __device__ __forceinline__ void attn_pass(LAS unsigned char* lds, const Tens& T, size_t rowbase, int q0, f32x16 (&o)[DV / 32], float& l_out, const int wave, QPre* qp = nullptr) {
;     ...
;             l += psum;
;             bf16x8 pf[4];
; #pragma unroll
;             for (int kb = 0; kb < 2; ++kb)
; #pragma unroll
;                 for (int s = 0; s < 2; ++s) {
;                     u32x4 w;
;                     w.x = pg8::cvt_pk_bf16(p[kb][8 * s + 0], p[kb][8 * s + 1]); w.y = pg8::cvt_pk_bf16(p[kb][8 * s + 2], p[kb][8 * s + 3]);
;                     w.z = pg8::cvt_pk_bf16(p[kb][8 * s + 4], p[kb][8 * s + 5]); w.w = pg8::cvt_pk_bf16(p[kb][8 * s + 6], p[kb][8 * s + 7]);
;                     pf[2 * kb + s] = __builtin_bit_cast(bf16x8, w);
;                 }
; #pragma unroll
;             for (int db = 0; db < NDB; ++db) {
; #pragma unroll
;                 for (int ks = 0; ks < 4; ++ks) {
;                     const LAS unsigned char* vp = vfa[db] + sl * VSL + sub * VB_T + (16 * ks) * VROW;
;                     const s16x4 lo = __builtin_bit_cast(s16x4, __builtin_amdgcn_ds_read_tr16_b64_v4i16((LAS s16x4*)(vp)));
;                     const s16x4 hi = __builtin_bit_cast(s16x4, __builtin_amdgcn_ds_read_tr16_b64_v4i16((LAS s16x4*)(vp + 8 * VROW)));
;                     const bf16x8 a = {lo[0], lo[1], lo[2], lo[3], hi[0], hi[1], hi[2], hi[3]};
;                     o[db] = __builtin_amdgcn_mfma_f32_32x32x16_bf16(a, pf[ks], o[db], 0, 0, 0);
;                 }
;             }
.LBB0_2483:
	v_cvt_pk_bf16_f32 v116, v13, v15
	v_cvt_pk_bf16_f32 v117, v97, v99
	v_cvt_pk_bf16_f32 v118, v112, v113
	v_cvt_pk_bf16_f32 v119, v114, v115
	v_cvt_pk_bf16_f32 v104, v103, v104
	v_cvt_pk_bf16_f32 v105, v105, v106
	v_cvt_pk_bf16_f32 v106, v107, v108
	v_cvt_pk_bf16_f32 v107, v109, v110
	v_cvt_pk_bf16_f32 v4, v3, v4
	v_cvt_pk_bf16_f32 v5, v5, v6
	v_cvt_pk_bf16_f32 v6, v7, v8
	v_cvt_pk_bf16_f32 v7, v9, v11
	v_cvt_pk_bf16_f32 v8, v10, v12
	v_cvt_pk_bf16_f32 v9, v14, v96
	v_cvt_pk_bf16_f32 v10, v98, v100
	v_cvt_pk_bf16_f32 v11, v101, v102
	s_waitcnt lgkmcnt(0)
	ds_read_b64_tr_b16 v[220:221], v161 offset:32768
	ds_read_b64_tr_b16 v[222:223], v161 offset:34816
	ds_read_b64_tr_b16 v[224:225], v161 offset:36864
	ds_read_b64_tr_b16 v[226:227], v161 offset:38912
	ds_read_b64_tr_b16 v[228:229], v161 offset:40960
	ds_read_b64_tr_b16 v[230:231], v161 offset:43008
	ds_read_b64_tr_b16 v[232:233], v161 offset:45056
	ds_read_b64_tr_b16 v[234:235], v161 offset:47104
	ds_read_b64_tr_b16 v[236:237], v162 offset:32768
	ds_read_b64_tr_b16 v[238:239], v162 offset:34816
	ds_read_b64_tr_b16 v[240:241], v162 offset:36864
	ds_read_b64_tr_b16 v[242:243], v162 offset:38912
	ds_read_b64_tr_b16 v[244:245], v162 offset:40960
	ds_read_b64_tr_b16 v[246:247], v162 offset:43008
	ds_read_b64_tr_b16 v[248:249], v162 offset:45056
	ds_read_b64_tr_b16 v[250:251], v162 offset:47104
	v_mfma_f32_32x32x16_bf16 v[16:31], v[188:191], v[116:119], v[16:31]
	v_add_f32_e32 v165, v165, v2
	v_mfma_f32_32x32x16_bf16 v[16:31], v[192:195], v[104:107], v[16:31]
	v_mfma_f32_32x32x16_bf16 v[16:31], v[196:199], v[4:7], v[16:31]
	v_mfma_f32_32x32x16_bf16 v[16:31], v[200:203], v[8:11], v[16:31]
	v_mfma_f32_32x32x16_bf16 v[64:79], v[204:207], v[116:119], v[64:79]
	v_mfma_f32_32x32x16_bf16 v[64:79], v[208:211], v[104:107], v[64:79]
	v_mfma_f32_32x32x16_bf16 v[64:79], v[212:215], v[4:7], v[64:79]
	v_mfma_f32_32x32x16_bf16 v[64:79], v[216:219], v[8:11], v[64:79]
	s_waitcnt lgkmcnt(8)
	v_mfma_f32_32x32x16_bf16 v[48:63], v[220:223], v[116:119], v[48:63]
	v_mfma_f32_32x32x16_bf16 v[48:63], v[224:227], v[104:107], v[48:63]
	v_mfma_f32_32x32x16_bf16 v[48:63], v[228:231], v[4:7], v[48:63]
	v_mfma_f32_32x32x16_bf16 v[48:63], v[232:235], v[8:11], v[48:63]
	s_waitcnt lgkmcnt(0)
	v_mfma_f32_32x32x16_bf16 v[32:47], v[236:239], v[116:119], v[32:47]
	v_mfma_f32_32x32x16_bf16 v[32:47], v[240:243], v[104:107], v[32:47]
	v_mfma_f32_32x32x16_bf16 v[32:47], v[244:247], v[4:7], v[32:47]
	v_mfma_f32_32x32x16_bf16 v[32:47], v[248:251], v[8:11], v[32:47]
	s_cmp_ge_u32 s34, s83
	s_cbranch_scc1 .LBB0_2440

; #define LAS __attribute__((address_space(3)))
; template <int MODE, int DQK, int DV>
; __device__ __forceinline__ void attn_pass(LAS unsigned char* lds, const Tens& T, size_t rowbase, int q0, f32x16 (&o)[DV / 32], float& l_out, const int wave, QPre* qp = nullptr) {
;     ...
; #pragma unroll
;                 for (int s = 0; s < NSTEP; ++s) {
;                     bf16x8 a;
;                     if (s < 4) a = *(const LAS bf16x8*)(kfa[s] + sl * KSL + sub * KB_T + kb * 4096);
;                     else       a = *(const LAS bf16x8*)(kfa[s] + sl * KSL + sub * KB_T + kb * 2048);
;                     if ((MODE == AM_DIFF || MODE == AM_MLA) && s == 0)
;                         asm("v_mfma_f32_32x32x16_bf16 %0, %1, %2, %3" : "=&v"(p[kb]) : "v"(a), "v"(qf[0]), "v"(negm));
;                     else
;                         p[kb] = __builtin_amdgcn_mfma_f32_32x32x16_bf16(a, qf[s], p[kb], 0, 0, 0);
;                 }
;     ...
; #pragma unroll
;             for (int db = 0; db < NDB; ++db) {
; #pragma unroll
;                 for (int ks = 0; ks < 4; ++ks) {
;                     const LAS unsigned char* vp = vfa[db] + sl * VSL + sub * VB_T + (16 * ks) * VROW;
;                     const s16x4 lo = __builtin_bit_cast(s16x4, __builtin_amdgcn_ds_read_tr16_b64_v4i16((LAS s16x4*)(vp)));
;                     const s16x4 hi = __builtin_bit_cast(s16x4, __builtin_amdgcn_ds_read_tr16_b64_v4i16((LAS s16x4*)(vp + 8 * VROW)));
;                     const bf16x8 a = {lo[0], lo[1], lo[2], lo[3], hi[0], hi[1], hi[2], hi[3]};
;                     o[db] = __builtin_amdgcn_mfma_f32_32x32x16_bf16(a, pf[ks], o[db], 0, 0, 0);
;                 }
.LBB0_2486:
	ds_read_b128 v[2:5], v156 offset:24576
	ds_read_b128 v[6:9], v155 offset:24576
	ds_read_b128 v[10:13], v155 offset:28672
	ds_read_b128 v[168:171], v156 offset:28672
	s_andn2_b64 vcc, exec, s[70:71]
	s_waitcnt lgkmcnt(2)
	v_mfma_f32_32x32x16_bf16 v[96:111], v[6:9], v[128:131], v[80:95]
	s_waitcnt lgkmcnt(1)
	v_mfma_f32_32x32x16_bf16 v[112:127], v[10:13], v[128:131], v[80:95]
	v_mfma_f32_32x32x16_bf16 v[96:111], v[2:5], v[132:135], v[96:111]
	ds_read_b128 v[2:5], v157 offset:24576
	ds_read_b128 v[6:9], v157 offset:28672
	s_waitcnt lgkmcnt(2)
	v_mfma_f32_32x32x16_bf16 v[112:127], v[168:171], v[132:135], v[112:127]
	s_waitcnt lgkmcnt(1)
	v_mfma_f32_32x32x16_bf16 v[96:111], v[2:5], v[136:139], v[96:111]
	ds_read_b128 v[2:5], v158 offset:24576
	ds_read_b128 v[172:175], v158 offset:28672
	s_waitcnt lgkmcnt(2)
	v_mfma_f32_32x32x16_bf16 v[112:127], v[6:9], v[136:139], v[112:127]
	s_waitcnt lgkmcnt(1)
	v_mfma_f32_32x32x16_bf16 v[96:111], v[2:5], v[140:143], v[96:111]
	s_waitcnt lgkmcnt(0)
	v_mfma_f32_32x32x16_bf16 v[112:127], v[172:175], v[140:143], v[112:127]
	ds_read_b64_tr_b16 v[188:189], v159 offset:49152
	ds_read_b64_tr_b16 v[190:191], v159 offset:51200
	ds_read_b64_tr_b16 v[192:193], v159 offset:53248
	ds_read_b64_tr_b16 v[194:195], v159 offset:55296
	ds_read_b64_tr_b16 v[196:197], v159 offset:57344
	ds_read_b64_tr_b16 v[198:199], v159 offset:59392
	ds_read_b64_tr_b16 v[200:201], v159 offset:61440
	ds_read_b64_tr_b16 v[202:203], v159 offset:63488
	ds_read_b64_tr_b16 v[204:205], v160 offset:49152
	ds_read_b64_tr_b16 v[206:207], v160 offset:51200
	ds_read_b64_tr_b16 v[208:209], v160 offset:53248
	ds_read_b64_tr_b16 v[210:211], v160 offset:55296
	ds_read_b64_tr_b16 v[212:213], v160 offset:57344
	ds_read_b64_tr_b16 v[214:215], v160 offset:59392
	ds_read_b64_tr_b16 v[216:217], v160 offset:61440
	ds_read_b64_tr_b16 v[218:219], v160 offset:63488
	s_cbranch_vccz .LBB0_2492
	s_andn2_b64 vcc, exec, s[68:69]
	s_cbranch_vccz .LBB0_2493

; #define LAS __attribute__((address_space(3)))
; __device__ __forceinline__ unsigned cvt_pk_bf16(float lo, float hi) { unsigned r; asm volatile("v_cvt_pk_bf16_f32 %0, %1, %2" : "=v"(r) : "v"(lo), "v"(hi)); return r; }
; template <int MODE, int DQK, int DV>
; __device__ __forceinline__ void attn_pass(LAS unsigned char* lds, const Tens& T, size_t rowbase, int q0, f32x16 (&o)[DV / 32], float& l_out, const int wave, QPre* qp = nullptr) {
;     ...
; #pragma unroll
;                 for (int s = 0; s < NSTEP; ++s) {
;                     bf16x8 a;
;                     if (s < 4) a = *(const LAS bf16x8*)(kfa[s] + sl * KSL + sub * KB_T + kb * 4096);
;                     else       a = *(const LAS bf16x8*)(kfa[s] + sl * KSL + sub * KB_T + kb * 2048);
;                     if ((MODE == AM_DIFF || MODE == AM_MLA) && s == 0)
;                         asm("v_mfma_f32_32x32x16_bf16 %0, %1, %2, %3" : "=&v"(p[kb]) : "v"(a), "v"(qf[0]), "v"(negm));
;                     else
;                         p[kb] = __builtin_amdgcn_mfma_f32_32x32x16_bf16(a, qf[s], p[kb], 0, 0, 0);
;                 }
;     ...
;             psum = 0.f;
; #pragma unroll
;             for (int rg = 0; rg < 16; ++rg) { const float e0 = __builtin_amdgcn_exp2f(p[0][rg]), e1 = __builtin_amdgcn_exp2f(p[1][rg]); p[0][rg] = e0; p[1][rg] = e1; psum += e0; psum += e1; }
;             if (!POSTHOC || redo) break;
;             if (__builtin_expect(!__any(!(psum <= BIG)), 1)) break;
;             redo = true;
;             }
;             l += psum;
;             bf16x8 pf[4];
; #pragma unroll
;             for (int kb = 0; kb < 2; ++kb)
; #pragma unroll
;                 for (int s = 0; s < 2; ++s) {
;                     u32x4 w;
;                     w.x = pg8::cvt_pk_bf16(p[kb][8 * s + 0], p[kb][8 * s + 1]); w.y = pg8::cvt_pk_bf16(p[kb][8 * s + 2], p[kb][8 * s + 3]);
;                     w.z = pg8::cvt_pk_bf16(p[kb][8 * s + 4], p[kb][8 * s + 5]); w.w = pg8::cvt_pk_bf16(p[kb][8 * s + 6], p[kb][8 * s + 7]);
;                     pf[2 * kb + s] = __builtin_bit_cast(bf16x8, w);
;                 }
.Lmla_fast0:
	v_mov_b32_e32 v14, v144
	v_mov_b32_e32 v15, v145
	v_mov_b32_e32 v17, v146
	v_mov_b32_e32 v30, v147
	v_mov_b32_e32 v31, v148
	v_mov_b32_e32 v252, v149
	v_mov_b32_e32 v253, v151
	v_mov_b32_e32 v163, v152
	ds_read_b128 v[200:203], v14
	ds_read_b128 v[204:207], v14 offset:4096
	ds_read_b128 v[208:211], v15
	ds_read_b128 v[212:215], v15 offset:4096
	ds_read_b128 v[216:219], v17
	ds_read_b128 v[220:223], v17 offset:4096
	ds_read_b128 v[224:227], v30
	ds_read_b128 v[228:231], v30 offset:4096
	s_waitcnt lgkmcnt(4)
	v_mfma_f32_32x32x16_bf16 v[80:95], v[200:203], v[112:115], v[64:79]
	ds_read_b128 v[200:203], v31
	v_mfma_f32_32x32x16_bf16 v[96:111], v[204:207], v[112:115], v[64:79]
	ds_read_b128 v[204:207], v31 offset:2048
	v_mfma_f32_32x32x16_bf16 v[80:95], v[208:211], v[116:119], v[80:95]
	ds_read_b128 v[208:211], v252
	v_mfma_f32_32x32x16_bf16 v[96:111], v[212:215], v[116:119], v[96:111]
	ds_read_b128 v[212:215], v252 offset:2048
	s_waitcnt lgkmcnt(4)
	v_mfma_f32_32x32x16_bf16 v[80:95], v[216:219], v[120:123], v[80:95]
	ds_read_b128 v[216:219], v14 offset:12288
	v_mfma_f32_32x32x16_bf16 v[96:111], v[220:223], v[120:123], v[96:111]
	ds_read_b128 v[220:223], v14 offset:16384
	v_mfma_f32_32x32x16_bf16 v[80:95], v[224:227], v[124:127], v[80:95]
	ds_read_b128 v[224:227], v15 offset:12288
	v_mfma_f32_32x32x16_bf16 v[96:111], v[228:231], v[124:127], v[96:111]
	ds_read_b128 v[228:231], v15 offset:16384
	s_waitcnt lgkmcnt(4)
	v_mfma_f32_32x32x16_bf16 v[80:95], v[200:203], v[128:131], v[80:95]
	ds_read_b128 v[200:203], v17 offset:12288
	v_mfma_f32_32x32x16_bf16 v[96:111], v[204:207], v[128:131], v[96:111]
	ds_read_b128 v[204:207], v17 offset:16384
	v_mfma_f32_32x32x16_bf16 v[80:95], v[208:211], v[132:135], v[80:95]
	ds_read_b128 v[208:211], v30 offset:12288
	v_mfma_f32_32x32x16_bf16 v[96:111], v[212:215], v[132:135], v[96:111]
	ds_read_b128 v[212:215], v30 offset:16384
	s_waitcnt lgkmcnt(4)
	v_mfma_f32_32x32x16_bf16 v[168:183], v[216:219], v[112:115], v[64:79]
	ds_read_b128 v[216:219], v31 offset:12288
	v_mfma_f32_32x32x16_bf16 v[184:199], v[220:223], v[112:115], v[64:79]
	ds_read_b128 v[220:223], v31 offset:14336
	v_mfma_f32_32x32x16_bf16 v[168:183], v[224:227], v[116:119], v[168:183]
	ds_read_b128 v[224:227], v252 offset:12288
	v_mfma_f32_32x32x16_bf16 v[184:199], v[228:231], v[116:119], v[184:199]
	ds_read_b128 v[228:231], v252 offset:14336
	v_exp_f32_e32 v80, v80
	v_exp_f32_e32 v81, v81
	v_exp_f32_e32 v82, v82
	v_add_f32_e32 v0, v80, v81
	v_exp_f32_e32 v83, v83
	v_add_f32_e32 v0, v0, v82
	v_exp_f32_e32 v84, v84
	v_add_f32_e32 v0, v0, v83
	v_exp_f32_e32 v85, v85
	s_waitcnt lgkmcnt(4)
	v_mfma_f32_32x32x16_bf16 v[168:183], v[200:203], v[120:123], v[168:183]
	ds_read_b64_tr_b16 v[2:3], v253
	ds_read_b64_tr_b16 v[4:5], v253 offset:1024
	v_add_f32_e32 v0, v0, v84
	v_exp_f32_e32 v86, v86
	v_add_f32_e32 v0, v0, v85
	v_exp_f32_e32 v87, v87
	v_add_f32_e32 v0, v0, v86
	v_exp_f32_e32 v88, v88
	v_add_f32_e32 v0, v0, v87
	v_exp_f32_e32 v89, v89
	v_add_f32_e32 v0, v0, v88
	v_mfma_f32_32x32x16_bf16 v[184:199], v[204:207], v[120:123], v[184:199]
	ds_read_b64_tr_b16 v[6:7], v253 offset:2048
	ds_read_b64_tr_b16 v[8:9], v253 offset:3072
	v_exp_f32_e32 v90, v90
	v_add_f32_e32 v0, v0, v89
	v_exp_f32_e32 v91, v91
	v_add_f32_e32 v0, v0, v90
	v_exp_f32_e32 v92, v92
	v_add_f32_e32 v0, v0, v91
	v_exp_f32_e32 v93, v93
	v_add_f32_e32 v0, v0, v92
	v_exp_f32_e32 v94, v94
	v_mfma_f32_32x32x16_bf16 v[168:183], v[208:211], v[124:127], v[168:183]
	ds_read_b64_tr_b16 v[10:11], v253 offset:4096
	ds_read_b64_tr_b16 v[12:13], v253 offset:5120
	v_add_f32_e32 v0, v0, v93
	v_exp_f32_e32 v95, v95
	v_add_f32_e32 v0, v0, v94
	v_exp_f32_e32 v96, v96
	v_add_f32_e32 v0, v0, v95
	v_exp_f32_e32 v97, v97
	v_add_f32_e32 v0, v0, v96
	v_exp_f32_e32 v98, v98
	v_add_f32_e32 v0, v0, v97
	v_mfma_f32_32x32x16_bf16 v[184:199], v[212:215], v[124:127], v[184:199]
	ds_read_b64_tr_b16 v[18:19], v253 offset:6144
	ds_read_b64_tr_b16 v[20:21], v253 offset:7168
	v_exp_f32_e32 v99, v99
	v_add_f32_e32 v0, v0, v98
	v_exp_f32_e32 v100, v100
	v_add_f32_e32 v0, v0, v99
	v_exp_f32_e32 v101, v101
	v_add_f32_e32 v0, v0, v100
	v_exp_f32_e32 v102, v102
	v_add_f32_e32 v0, v0, v101
	v_exp_f32_e32 v103, v103
	s_waitcnt lgkmcnt(8)
	v_mfma_f32_32x32x16_bf16 v[168:183], v[216:219], v[128:131], v[168:183]
	ds_read_b64_tr_b16 v[22:23], v163
	ds_read_b64_tr_b16 v[24:25], v163 offset:1024
	v_add_f32_e32 v0, v0, v102
	v_exp_f32_e32 v104, v104
	v_add_f32_e32 v0, v0, v103
	v_exp_f32_e32 v105, v105
	v_add_f32_e32 v0, v0, v104
	v_exp_f32_e32 v106, v106
	v_add_f32_e32 v0, v0, v105
	v_exp_f32_e32 v107, v107
	v_add_f32_e32 v0, v0, v106
	v_mfma_f32_32x32x16_bf16 v[184:199], v[220:223], v[128:131], v[184:199]
	ds_read_b64_tr_b16 v[26:27], v163 offset:2048
	ds_read_b64_tr_b16 v[28:29], v163 offset:3072
	v_exp_f32_e32 v108, v108
	v_add_f32_e32 v0, v0, v107
	v_exp_f32_e32 v109, v109
	v_add_f32_e32 v0, v0, v108
	v_exp_f32_e32 v110, v110
	v_add_f32_e32 v0, v0, v109
	v_exp_f32_e32 v111, v111
	v_add_f32_e32 v0, v0, v110
	v_add_f32_e32 v0, v0, v111
	v_mfma_f32_32x32x16_bf16 v[168:183], v[224:227], v[132:135], v[168:183]
	ds_read_b64_tr_b16 v[164:165], v163 offset:4096
	ds_read_b64_tr_b16 v[166:167], v163 offset:5120
	v_cvt_pk_bf16_f32 v80, v80, v81
	v_cvt_pk_bf16_f32 v81, v82, v83
	v_cvt_pk_bf16_f32 v82, v84, v85
	v_cvt_pk_bf16_f32 v83, v86, v87
	v_cvt_pk_bf16_f32 v84, v88, v89
	v_cvt_pk_bf16_f32 v85, v90, v91
	v_cvt_pk_bf16_f32 v86, v92, v93
	v_cvt_pk_bf16_f32 v87, v94, v95
	v_cvt_pk_bf16_f32 v88, v96, v97
	v_mfma_f32_32x32x16_bf16 v[184:199], v[228:231], v[132:135], v[184:199]
	ds_read_b64_tr_b16 v[232:233], v163 offset:6144
	ds_read_b64_tr_b16 v[234:235], v163 offset:7168
	v_cvt_pk_bf16_f32 v89, v98, v99
	v_cvt_pk_bf16_f32 v90, v100, v101
	v_cvt_pk_bf16_f32 v91, v102, v103
	v_cvt_pk_bf16_f32 v92, v104, v105
	v_cvt_pk_bf16_f32 v93, v106, v107
	v_cvt_pk_bf16_f32 v94, v108, v109
	v_cvt_pk_bf16_f32 v95, v110, v111
	v_cmp_nge_f32_e32 vcc, s86, v0
	s_cmp_eq_u64 vcc, 0
	s_cbranch_scc0 .Lmla_slow0
; #define LAS __attribute__((address_space(3)))
; __device__ __forceinline__ unsigned cvt_pk_bf16(float lo, float hi) { unsigned r; asm volatile("v_cvt_pk_bf16_f32 %0, %1, %2" : "=v"(r) : "v"(lo), "v"(hi)); return r; }
; template <int MODE, int DQK, int DV>
; __device__ __forceinline__ void attn_pass(LAS unsigned char* lds, const Tens& T, size_t rowbase, int q0, f32x16 (&o)[DV / 32], float& l_out, const int wave, QPre* qp = nullptr) {
;     ...
;             psum = 0.f;
; #pragma unroll
;             for (int rg = 0; rg < 16; ++rg) { const float e0 = __builtin_amdgcn_exp2f(p[0][rg]), e1 = __builtin_amdgcn_exp2f(p[1][rg]); p[0][rg] = e0; p[1][rg] = e1; psum += e0; psum += e1; }
;             if (!POSTHOC || redo) break;
;             if (__builtin_expect(!__any(!(psum <= BIG)), 1)) break;
;             redo = true;
;             }
;             l += psum;
;             bf16x8 pf[4];
; #pragma unroll
;             for (int kb = 0; kb < 2; ++kb)
; #pragma unroll
;                 for (int s = 0; s < 2; ++s) {
;                     u32x4 w;
;                     w.x = pg8::cvt_pk_bf16(p[kb][8 * s + 0], p[kb][8 * s + 1]); w.y = pg8::cvt_pk_bf16(p[kb][8 * s + 2], p[kb][8 * s + 3]);
;                     w.z = pg8::cvt_pk_bf16(p[kb][8 * s + 4], p[kb][8 * s + 5]); w.w = pg8::cvt_pk_bf16(p[kb][8 * s + 6], p[kb][8 * s + 7]);
;                     pf[2 * kb + s] = __builtin_bit_cast(bf16x8, w);
;                 }
; #pragma unroll
;             for (int db = 0; db < NDB; ++db) {
; #pragma unroll
;                 for (int ks = 0; ks < 4; ++ks) {
;                     const LAS unsigned char* vp = vfa[db] + sl * VSL + sub * VB_T + (16 * ks) * VROW;
;                     const s16x4 lo = __builtin_bit_cast(s16x4, __builtin_amdgcn_ds_read_tr16_b64_v4i16((LAS s16x4*)(vp)));
;                     const s16x4 hi = __builtin_bit_cast(s16x4, __builtin_amdgcn_ds_read_tr16_b64_v4i16((LAS s16x4*)(vp + 8 * VROW)));
;                     const bf16x8 a = {lo[0], lo[1], lo[2], lo[3], hi[0], hi[1], hi[2], hi[3]};
;                     o[db] = __builtin_amdgcn_mfma_f32_32x32x16_bf16(a, pf[ks], o[db], 0, 0, 0);
;                 }
;             }
	v_add_f32_e32 v161, v161, v0
	s_waitcnt lgkmcnt(8)
	v_mfma_f32_32x32x16_bf16 v[48:63], v[2:5], v[80:83], v[48:63]
	ds_read_b64_tr_b16 v[96:97], v253 offset:8192
	ds_read_b64_tr_b16 v[98:99], v253 offset:9216
	v_exp_f32_e32 v168, v168
	v_exp_f32_e32 v169, v169
	v_exp_f32_e32 v170, v170
	v_add_f32_e32 v0, v168, v169
	v_exp_f32_e32 v171, v171
	v_add_f32_e32 v0, v0, v170
	v_exp_f32_e32 v172, v172
	v_add_f32_e32 v0, v0, v171
	v_exp_f32_e32 v173, v173
	v_add_f32_e32 v0, v0, v172
	v_mfma_f32_32x32x16_bf16 v[48:63], v[6:9], v[84:87], v[48:63]
	ds_read_b64_tr_b16 v[100:101], v253 offset:10240
	ds_read_b64_tr_b16 v[102:103], v253 offset:11264
	v_exp_f32_e32 v174, v174
	v_add_f32_e32 v0, v0, v173
	v_exp_f32_e32 v175, v175
	v_add_f32_e32 v0, v0, v174
	v_exp_f32_e32 v176, v176
	v_add_f32_e32 v0, v0, v175
	v_exp_f32_e32 v177, v177
	v_add_f32_e32 v0, v0, v176
	v_exp_f32_e32 v178, v178
	v_add_f32_e32 v0, v0, v177
	v_mfma_f32_32x32x16_bf16 v[48:63], v[10:13], v[88:91], v[48:63]
	ds_read_b64_tr_b16 v[104:105], v253 offset:12288
	ds_read_b64_tr_b16 v[106:107], v253 offset:13312
	v_exp_f32_e32 v179, v179
	v_add_f32_e32 v0, v0, v178
	v_exp_f32_e32 v180, v180
	v_add_f32_e32 v0, v0, v179
	v_exp_f32_e32 v181, v181
	v_add_f32_e32 v0, v0, v180
	v_exp_f32_e32 v182, v182
	v_add_f32_e32 v0, v0, v181
	v_exp_f32_e32 v183, v183
	v_add_f32_e32 v0, v0, v182
	v_mfma_f32_32x32x16_bf16 v[48:63], v[18:21], v[92:95], v[48:63]
	ds_read_b64_tr_b16 v[108:109], v253 offset:14336
	ds_read_b64_tr_b16 v[110:111], v253 offset:15360
	v_exp_f32_e32 v184, v184
	v_add_f32_e32 v0, v0, v183
	v_exp_f32_e32 v185, v185
	v_add_f32_e32 v0, v0, v184
	v_exp_f32_e32 v186, v186
	v_add_f32_e32 v0, v0, v185
	v_exp_f32_e32 v187, v187
	v_add_f32_e32 v0, v0, v186
	v_exp_f32_e32 v188, v188
	v_add_f32_e32 v0, v0, v187
	s_waitcnt lgkmcnt(8)
	v_mfma_f32_32x32x16_bf16 v[32:47], v[22:25], v[80:83], v[32:47]
	ds_read_b64_tr_b16 v[236:237], v163 offset:8192
	ds_read_b64_tr_b16 v[238:239], v163 offset:9216
	v_exp_f32_e32 v189, v189
	v_add_f32_e32 v0, v0, v188
	v_exp_f32_e32 v190, v190
	v_add_f32_e32 v0, v0, v189
	v_exp_f32_e32 v191, v191
	v_add_f32_e32 v0, v0, v190
	v_exp_f32_e32 v192, v192
	v_add_f32_e32 v0, v0, v191
	v_exp_f32_e32 v193, v193
	v_add_f32_e32 v0, v0, v192
	v_mfma_f32_32x32x16_bf16 v[32:47], v[26:29], v[84:87], v[32:47]
	ds_read_b64_tr_b16 v[240:241], v163 offset:10240
	ds_read_b64_tr_b16 v[242:243], v163 offset:11264
	v_exp_f32_e32 v194, v194
	v_add_f32_e32 v0, v0, v193
	v_exp_f32_e32 v195, v195
	v_add_f32_e32 v0, v0, v194
	v_exp_f32_e32 v196, v196
	v_add_f32_e32 v0, v0, v195
	v_exp_f32_e32 v197, v197
	v_add_f32_e32 v0, v0, v196
	v_exp_f32_e32 v198, v198
	v_add_f32_e32 v0, v0, v197
	v_mfma_f32_32x32x16_bf16 v[32:47], v[164:167], v[88:91], v[32:47]
	ds_read_b64_tr_b16 v[244:245], v163 offset:12288
	ds_read_b64_tr_b16 v[246:247], v163 offset:13312
	v_exp_f32_e32 v199, v199
	v_add_f32_e32 v0, v0, v198
	v_add_f32_e32 v0, v0, v199
	v_cvt_pk_bf16_f32 v168, v168, v169
	v_cvt_pk_bf16_f32 v169, v170, v171
	v_cvt_pk_bf16_f32 v170, v172, v173
	v_cvt_pk_bf16_f32 v171, v174, v175
	v_cvt_pk_bf16_f32 v172, v176, v177
	v_cvt_pk_bf16_f32 v173, v178, v179
	v_cvt_pk_bf16_f32 v174, v180, v181
	v_mfma_f32_32x32x16_bf16 v[32:47], v[232:235], v[92:95], v[32:47]
	ds_read_b64_tr_b16 v[248:249], v163 offset:14336
	ds_read_b64_tr_b16 v[250:251], v163 offset:15360
	v_cvt_pk_bf16_f32 v175, v182, v183
	v_cvt_pk_bf16_f32 v176, v184, v185
	v_cvt_pk_bf16_f32 v177, v186, v187
	v_cvt_pk_bf16_f32 v178, v188, v189
	v_cvt_pk_bf16_f32 v179, v190, v191
	v_cvt_pk_bf16_f32 v180, v192, v193
	v_cvt_pk_bf16_f32 v181, v194, v195
	v_cvt_pk_bf16_f32 v182, v196, v197
	v_cvt_pk_bf16_f32 v183, v198, v199
	v_cmp_nge_f32_e32 vcc, s86, v0
	s_cmp_eq_u64 vcc, 0
	s_cbranch_scc0 .LBB0_2557
	v_add_f32_e32 v161, v161, v0
	s_waitcnt lgkmcnt(8)
	v_mfma_f32_32x32x16_bf16 v[48:63], v[96:99], v[168:171], v[48:63]
	v_mfma_f32_32x32x16_bf16 v[48:63], v[100:103], v[172:175], v[48:63]
	v_mfma_f32_32x32x16_bf16 v[48:63], v[104:107], v[176:179], v[48:63]
	v_mfma_f32_32x32x16_bf16 v[48:63], v[108:111], v[180:183], v[48:63]
	s_waitcnt lgkmcnt(0)
	v_mfma_f32_32x32x16_bf16 v[32:47], v[236:239], v[168:171], v[32:47]
	v_mfma_f32_32x32x16_bf16 v[32:47], v[240:243], v[172:175], v[32:47]
	v_mfma_f32_32x32x16_bf16 v[32:47], v[244:247], v[176:179], v[32:47]
	v_mfma_f32_32x32x16_bf16 v[32:47], v[248:251], v[180:183], v[32:47]
	s_branch .LBB0_2543
; template <int MODE, int DQK, int DV>
; __device__ __forceinline__ void attn_pass(LAS unsigned char* lds, const Tens& T, size_t rowbase, int q0, f32x16 (&o)[DV / 32], float& l_out, const int wave, QPre* qp = nullptr) {
;     ...
;             for (;;) {
; #pragma unroll
;             for (int kb = 0; kb < 2; ++kb) {
;                 if (MODE == AM_FOX) {
;                     const float ctm = ct2 - m;
; #pragma unroll
;                     for (int g = 0; g < 4; ++g) {
;                         const f32x4 c = *(const LAS f32x4*)(lds + OFF_CS + (sl * NSUB + sub) * 256 + (32 * kb + 8 * g + 4 * h) * 4);
;                         p[kb][4 * g + 0] = fmaf(-LOG2E, c.x, ctm); p[kb][4 * g + 1] = fmaf(-LOG2E, c.y, ctm); p[kb][4 * g + 2] = fmaf(-LOG2E, c.z, ctm); p[kb][4 * g + 3] = fmaf(-LOG2E, c.w, ctm);
;                     }
;                 } else if (MODE == AM_DSA) {
; #pragma unroll
;                     for (int g = 0; g < 4; ++g) {
;                         const unsigned nib = __builtin_amdgcn_ubfe(mw[kb], (unsigned)(8 * g + 4 * h), 4u);
;                         const f32x4 t4 = *(const LAS f32x4*)(lds + OFF_LUT + 768 + nib * 16);
;                         p[kb][4 * g + 0] = t4.x; p[kb][4 * g + 1] = t4.y; p[kb][4 * g + 2] = t4.z; p[kb][4 * g + 3] = t4.w;
;                     }
;                     p[kb] = __builtin_amdgcn_mfma_f32_32x32x16_bf16(kone, qm, p[kb], 0, 0, 0);
;                 }
; #pragma unroll
;                 for (int s = 0; s < NSTEP; ++s) {
;                     bf16x8 a;
;                     if (s < 4) a = *(const LAS bf16x8*)(kfa[s] + sl * KSL + sub * KB_T + kb * 4096);
;                     else       a = *(const LAS bf16x8*)(kfa[s] + sl * KSL + sub * KB_T + kb * 2048);
;                     if ((MODE == AM_DIFF || MODE == AM_MLA) && s == 0)
;                         asm("v_mfma_f32_32x32x16_bf16 %0, %1, %2, %3" : "=&v"(p[kb]) : "v"(a), "v"(qf[0]), "v"(negm));
;                     else
;                         p[kb] = __builtin_amdgcn_mfma_f32_32x32x16_bf16(a, qf[s], p[kb], 0, 0, 0);
;                 }
;             }
;     ...
;             psum = 0.f;
; #pragma unroll
;             for (int rg = 0; rg < 16; ++rg) { const float e0 = __builtin_amdgcn_exp2f(p[0][rg]), e1 = __builtin_amdgcn_exp2f(p[1][rg]); p[0][rg] = e0; p[1][rg] = e1; psum += e0; psum += e1; }
;             if (!POSTHOC || redo) break;
.Lmla_fast1:
	v_add_u32_e32 v14, 0x6000, v144
	v_add_u32_e32 v15, 0x6000, v145
	v_add_u32_e32 v17, 0x6000, v146
	v_add_u32_e32 v30, 0x6000, v147
	v_add_u32_e32 v31, 0x6000, v148
	v_add_u32_e32 v252, 0x6000, v149
	v_add_u32_e32 v253, 0x4000, v151
	v_add_u32_e32 v163, 0x4000, v152
	ds_read_b128 v[200:203], v14
	ds_read_b128 v[204:207], v14 offset:4096
	ds_read_b128 v[208:211], v15
	ds_read_b128 v[212:215], v15 offset:4096
	ds_read_b128 v[216:219], v17
	ds_read_b128 v[220:223], v17 offset:4096
	ds_read_b128 v[224:227], v30
	ds_read_b128 v[228:231], v30 offset:4096
	s_waitcnt lgkmcnt(4)
	v_mfma_f32_32x32x16_bf16 v[80:95], v[200:203], v[112:115], v[64:79]
	ds_read_b128 v[200:203], v31
	v_mfma_f32_32x32x16_bf16 v[96:111], v[204:207], v[112:115], v[64:79]
	ds_read_b128 v[204:207], v31 offset:2048
	v_mfma_f32_32x32x16_bf16 v[80:95], v[208:211], v[116:119], v[80:95]
	ds_read_b128 v[208:211], v252
	v_mfma_f32_32x32x16_bf16 v[96:111], v[212:215], v[116:119], v[96:111]
	ds_read_b128 v[212:215], v252 offset:2048
	s_waitcnt lgkmcnt(4)
	v_mfma_f32_32x32x16_bf16 v[80:95], v[216:219], v[120:123], v[80:95]
	ds_read_b128 v[216:219], v14 offset:12288
	v_mfma_f32_32x32x16_bf16 v[96:111], v[220:223], v[120:123], v[96:111]
	ds_read_b128 v[220:223], v14 offset:16384
	v_mfma_f32_32x32x16_bf16 v[80:95], v[224:227], v[124:127], v[80:95]
	ds_read_b128 v[224:227], v15 offset:12288
	v_mfma_f32_32x32x16_bf16 v[96:111], v[228:231], v[124:127], v[96:111]
	ds_read_b128 v[228:231], v15 offset:16384
	s_waitcnt lgkmcnt(4)
	v_mfma_f32_32x32x16_bf16 v[80:95], v[200:203], v[128:131], v[80:95]
	ds_read_b128 v[200:203], v17 offset:12288
	v_mfma_f32_32x32x16_bf16 v[96:111], v[204:207], v[128:131], v[96:111]
	ds_read_b128 v[204:207], v17 offset:16384
	v_mfma_f32_32x32x16_bf16 v[80:95], v[208:211], v[132:135], v[80:95]
	ds_read_b128 v[208:211], v30 offset:12288
	v_mfma_f32_32x32x16_bf16 v[96:111], v[212:215], v[132:135], v[96:111]
	ds_read_b128 v[212:215], v30 offset:16384
	s_waitcnt lgkmcnt(4)
	v_mfma_f32_32x32x16_bf16 v[168:183], v[216:219], v[112:115], v[64:79]
	ds_read_b128 v[216:219], v31 offset:12288
	v_mfma_f32_32x32x16_bf16 v[184:199], v[220:223], v[112:115], v[64:79]
	ds_read_b128 v[220:223], v31 offset:14336
	v_mfma_f32_32x32x16_bf16 v[168:183], v[224:227], v[116:119], v[168:183]
	ds_read_b128 v[224:227], v252 offset:12288
	v_mfma_f32_32x32x16_bf16 v[184:199], v[228:231], v[116:119], v[184:199]
	ds_read_b128 v[228:231], v252 offset:14336
	v_exp_f32_e32 v80, v80
	v_exp_f32_e32 v81, v81
	v_exp_f32_e32 v82, v82
	v_add_f32_e32 v0, v80, v81
	v_exp_f32_e32 v83, v83
	v_add_f32_e32 v0, v0, v82
	v_exp_f32_e32 v84, v84
	v_add_f32_e32 v0, v0, v83
	v_exp_f32_e32 v85, v85
	s_waitcnt lgkmcnt(4)
	v_mfma_f32_32x32x16_bf16 v[168:183], v[200:203], v[120:123], v[168:183]
	ds_read_b64_tr_b16 v[2:3], v253
	ds_read_b64_tr_b16 v[4:5], v253 offset:1024
	v_add_f32_e32 v0, v0, v84
	v_exp_f32_e32 v86, v86
	v_add_f32_e32 v0, v0, v85
	v_exp_f32_e32 v87, v87
	v_add_f32_e32 v0, v0, v86
	v_exp_f32_e32 v88, v88
	v_add_f32_e32 v0, v0, v87
	v_exp_f32_e32 v89, v89
	v_add_f32_e32 v0, v0, v88
	v_mfma_f32_32x32x16_bf16 v[184:199], v[204:207], v[120:123], v[184:199]
	ds_read_b64_tr_b16 v[6:7], v253 offset:2048
	ds_read_b64_tr_b16 v[8:9], v253 offset:3072
	v_exp_f32_e32 v90, v90
	v_add_f32_e32 v0, v0, v89
	v_exp_f32_e32 v91, v91
	v_add_f32_e32 v0, v0, v90
	v_exp_f32_e32 v92, v92
	v_add_f32_e32 v0, v0, v91
	v_exp_f32_e32 v93, v93
	v_add_f32_e32 v0, v0, v92
	v_exp_f32_e32 v94, v94
	v_mfma_f32_32x32x16_bf16 v[168:183], v[208:211], v[124:127], v[168:183]
	ds_read_b64_tr_b16 v[10:11], v253 offset:4096
	ds_read_b64_tr_b16 v[12:13], v253 offset:5120
	v_add_f32_e32 v0, v0, v93
	v_exp_f32_e32 v95, v95
	v_add_f32_e32 v0, v0, v94
	v_exp_f32_e32 v96, v96
	v_add_f32_e32 v0, v0, v95
	v_exp_f32_e32 v97, v97
	v_add_f32_e32 v0, v0, v96
	v_exp_f32_e32 v98, v98
	v_add_f32_e32 v0, v0, v97
	v_mfma_f32_32x32x16_bf16 v[184:199], v[212:215], v[124:127], v[184:199]
	ds_read_b64_tr_b16 v[18:19], v253 offset:6144
	ds_read_b64_tr_b16 v[20:21], v253 offset:7168
	v_exp_f32_e32 v99, v99
	v_add_f32_e32 v0, v0, v98
	v_exp_f32_e32 v100, v100
	v_add_f32_e32 v0, v0, v99
	v_exp_f32_e32 v101, v101
	v_add_f32_e32 v0, v0, v100
	v_exp_f32_e32 v102, v102
	v_add_f32_e32 v0, v0, v101
	v_exp_f32_e32 v103, v103
	s_waitcnt lgkmcnt(8)
	v_mfma_f32_32x32x16_bf16 v[168:183], v[216:219], v[128:131], v[168:183]
	ds_read_b64_tr_b16 v[22:23], v163
	ds_read_b64_tr_b16 v[24:25], v163 offset:1024
	v_add_f32_e32 v0, v0, v102
	v_exp_f32_e32 v104, v104
	v_add_f32_e32 v0, v0, v103
	v_exp_f32_e32 v105, v105
	v_add_f32_e32 v0, v0, v104
	v_exp_f32_e32 v106, v106
	v_add_f32_e32 v0, v0, v105
	v_exp_f32_e32 v107, v107
	v_add_f32_e32 v0, v0, v106
	v_mfma_f32_32x32x16_bf16 v[184:199], v[220:223], v[128:131], v[184:199]
	ds_read_b64_tr_b16 v[26:27], v163 offset:2048
	ds_read_b64_tr_b16 v[28:29], v163 offset:3072
	v_exp_f32_e32 v108, v108
	v_add_f32_e32 v0, v0, v107
	v_exp_f32_e32 v109, v109
	v_add_f32_e32 v0, v0, v108
	v_exp_f32_e32 v110, v110
	v_add_f32_e32 v0, v0, v109
	v_exp_f32_e32 v111, v111
	v_add_f32_e32 v0, v0, v110
	v_add_f32_e32 v0, v0, v111
	v_mfma_f32_32x32x16_bf16 v[168:183], v[224:227], v[132:135], v[168:183]
	ds_read_b64_tr_b16 v[164:165], v163 offset:4096
	ds_read_b64_tr_b16 v[166:167], v163 offset:5120
	v_cvt_pk_bf16_f32 v80, v80, v81
	v_cvt_pk_bf16_f32 v81, v82, v83
	v_cvt_pk_bf16_f32 v82, v84, v85
	v_cvt_pk_bf16_f32 v83, v86, v87
	v_cvt_pk_bf16_f32 v84, v88, v89
	v_cvt_pk_bf16_f32 v85, v90, v91
	v_cvt_pk_bf16_f32 v86, v92, v93
	v_cvt_pk_bf16_f32 v87, v94, v95
	v_cvt_pk_bf16_f32 v88, v96, v97
	v_mfma_f32_32x32x16_bf16 v[184:199], v[228:231], v[132:135], v[184:199]
	ds_read_b64_tr_b16 v[232:233], v163 offset:6144
	ds_read_b64_tr_b16 v[234:235], v163 offset:7168
	v_cvt_pk_bf16_f32 v89, v98, v99
	v_cvt_pk_bf16_f32 v90, v100, v101
	v_cvt_pk_bf16_f32 v91, v102, v103
	v_cvt_pk_bf16_f32 v92, v104, v105
	v_cvt_pk_bf16_f32 v93, v106, v107
	v_cvt_pk_bf16_f32 v94, v108, v109
	v_cvt_pk_bf16_f32 v95, v110, v111
	v_cmp_nge_f32_e32 vcc, s86, v0
	s_cmp_eq_u64 vcc, 0
	s_cbranch_scc0 .Lmla_slow1
; #define LAS __attribute__((address_space(3)))
; __device__ __forceinline__ unsigned cvt_pk_bf16(float lo, float hi) { unsigned r; asm volatile("v_cvt_pk_bf16_f32 %0, %1, %2" : "=v"(r) : "v"(lo), "v"(hi)); return r; }
; template <int MODE, int DQK, int DV>
; __device__ __forceinline__ void attn_pass(LAS unsigned char* lds, const Tens& T, size_t rowbase, int q0, f32x16 (&o)[DV / 32], float& l_out, const int wave, QPre* qp = nullptr) {
;     ...
;             psum = 0.f;
; #pragma unroll
;             for (int rg = 0; rg < 16; ++rg) { const float e0 = __builtin_amdgcn_exp2f(p[0][rg]), e1 = __builtin_amdgcn_exp2f(p[1][rg]); p[0][rg] = e0; p[1][rg] = e1; psum += e0; psum += e1; }
;             if (!POSTHOC || redo) break;
;             if (__builtin_expect(!__any(!(psum <= BIG)), 1)) break;
;             redo = true;
;             }
;             l += psum;
;             bf16x8 pf[4];
; #pragma unroll
;             for (int kb = 0; kb < 2; ++kb)
; #pragma unroll
;                 for (int s = 0; s < 2; ++s) {
;                     u32x4 w;
;                     w.x = pg8::cvt_pk_bf16(p[kb][8 * s + 0], p[kb][8 * s + 1]); w.y = pg8::cvt_pk_bf16(p[kb][8 * s + 2], p[kb][8 * s + 3]);
;                     w.z = pg8::cvt_pk_bf16(p[kb][8 * s + 4], p[kb][8 * s + 5]); w.w = pg8::cvt_pk_bf16(p[kb][8 * s + 6], p[kb][8 * s + 7]);
;                     pf[2 * kb + s] = __builtin_bit_cast(bf16x8, w);
;                 }
; #pragma unroll
;             for (int db = 0; db < NDB; ++db) {
; #pragma unroll
;                 for (int ks = 0; ks < 4; ++ks) {
;                     const LAS unsigned char* vp = vfa[db] + sl * VSL + sub * VB_T + (16 * ks) * VROW;
;                     const s16x4 lo = __builtin_bit_cast(s16x4, __builtin_amdgcn_ds_read_tr16_b64_v4i16((LAS s16x4*)(vp)));
;                     const s16x4 hi = __builtin_bit_cast(s16x4, __builtin_amdgcn_ds_read_tr16_b64_v4i16((LAS s16x4*)(vp + 8 * VROW)));
;                     const bf16x8 a = {lo[0], lo[1], lo[2], lo[3], hi[0], hi[1], hi[2], hi[3]};
;                     o[db] = __builtin_amdgcn_mfma_f32_32x32x16_bf16(a, pf[ks], o[db], 0, 0, 0);
;                 }
;             }
	v_add_f32_e32 v161, v161, v0
	s_waitcnt lgkmcnt(8)
	v_mfma_f32_32x32x16_bf16 v[48:63], v[2:5], v[80:83], v[48:63]
	ds_read_b64_tr_b16 v[96:97], v253 offset:8192
	ds_read_b64_tr_b16 v[98:99], v253 offset:9216
	v_exp_f32_e32 v168, v168
	v_exp_f32_e32 v169, v169
	v_exp_f32_e32 v170, v170
	v_add_f32_e32 v0, v168, v169
	v_exp_f32_e32 v171, v171
	v_add_f32_e32 v0, v0, v170
	v_exp_f32_e32 v172, v172
	v_add_f32_e32 v0, v0, v171
	v_exp_f32_e32 v173, v173
	v_add_f32_e32 v0, v0, v172
	v_mfma_f32_32x32x16_bf16 v[48:63], v[6:9], v[84:87], v[48:63]
	ds_read_b64_tr_b16 v[100:101], v253 offset:10240
	ds_read_b64_tr_b16 v[102:103], v253 offset:11264
	v_exp_f32_e32 v174, v174
	v_add_f32_e32 v0, v0, v173
	v_exp_f32_e32 v175, v175
	v_add_f32_e32 v0, v0, v174
	v_exp_f32_e32 v176, v176
	v_add_f32_e32 v0, v0, v175
	v_exp_f32_e32 v177, v177
	v_add_f32_e32 v0, v0, v176
	v_exp_f32_e32 v178, v178
	v_add_f32_e32 v0, v0, v177
	v_mfma_f32_32x32x16_bf16 v[48:63], v[10:13], v[88:91], v[48:63]
	ds_read_b64_tr_b16 v[104:105], v253 offset:12288
	ds_read_b64_tr_b16 v[106:107], v253 offset:13312
	v_exp_f32_e32 v179, v179
	v_add_f32_e32 v0, v0, v178
	v_exp_f32_e32 v180, v180
	v_add_f32_e32 v0, v0, v179
	v_exp_f32_e32 v181, v181
	v_add_f32_e32 v0, v0, v180
	v_exp_f32_e32 v182, v182
	v_add_f32_e32 v0, v0, v181
	v_exp_f32_e32 v183, v183
	v_add_f32_e32 v0, v0, v182
	v_mfma_f32_32x32x16_bf16 v[48:63], v[18:21], v[92:95], v[48:63]
	ds_read_b64_tr_b16 v[108:109], v253 offset:14336
	ds_read_b64_tr_b16 v[110:111], v253 offset:15360
	v_exp_f32_e32 v184, v184
	v_add_f32_e32 v0, v0, v183
	v_exp_f32_e32 v185, v185
	v_add_f32_e32 v0, v0, v184
	v_exp_f32_e32 v186, v186
	v_add_f32_e32 v0, v0, v185
	v_exp_f32_e32 v187, v187
	v_add_f32_e32 v0, v0, v186
	v_exp_f32_e32 v188, v188
	v_add_f32_e32 v0, v0, v187
	s_waitcnt lgkmcnt(8)
	v_mfma_f32_32x32x16_bf16 v[32:47], v[22:25], v[80:83], v[32:47]
	ds_read_b64_tr_b16 v[236:237], v163 offset:8192
	ds_read_b64_tr_b16 v[238:239], v163 offset:9216
	v_exp_f32_e32 v189, v189
	v_add_f32_e32 v0, v0, v188
	v_exp_f32_e32 v190, v190
	v_add_f32_e32 v0, v0, v189
	v_exp_f32_e32 v191, v191
	v_add_f32_e32 v0, v0, v190
	v_exp_f32_e32 v192, v192
	v_add_f32_e32 v0, v0, v191
	v_exp_f32_e32 v193, v193
	v_add_f32_e32 v0, v0, v192
	v_mfma_f32_32x32x16_bf16 v[32:47], v[26:29], v[84:87], v[32:47]
	ds_read_b64_tr_b16 v[240:241], v163 offset:10240
	ds_read_b64_tr_b16 v[242:243], v163 offset:11264
	v_exp_f32_e32 v194, v194
	v_add_f32_e32 v0, v0, v193
	v_exp_f32_e32 v195, v195
	v_add_f32_e32 v0, v0, v194
	v_exp_f32_e32 v196, v196
	v_add_f32_e32 v0, v0, v195
	v_exp_f32_e32 v197, v197
	v_add_f32_e32 v0, v0, v196
	v_exp_f32_e32 v198, v198
	v_add_f32_e32 v0, v0, v197
	v_mfma_f32_32x32x16_bf16 v[32:47], v[164:167], v[88:91], v[32:47]
	ds_read_b64_tr_b16 v[244:245], v163 offset:12288
	ds_read_b64_tr_b16 v[246:247], v163 offset:13312
	v_exp_f32_e32 v199, v199
	v_add_f32_e32 v0, v0, v198
	v_add_f32_e32 v0, v0, v199
	v_cvt_pk_bf16_f32 v168, v168, v169
	v_cvt_pk_bf16_f32 v169, v170, v171
	v_cvt_pk_bf16_f32 v170, v172, v173
	v_cvt_pk_bf16_f32 v171, v174, v175
	v_cvt_pk_bf16_f32 v172, v176, v177
	v_cvt_pk_bf16_f32 v173, v178, v179
	v_cvt_pk_bf16_f32 v174, v180, v181
	v_mfma_f32_32x32x16_bf16 v[32:47], v[232:235], v[92:95], v[32:47]
	ds_read_b64_tr_b16 v[248:249], v163 offset:14336
	ds_read_b64_tr_b16 v[250:251], v163 offset:15360
	v_cvt_pk_bf16_f32 v175, v182, v183
	v_cvt_pk_bf16_f32 v176, v184, v185
	v_cvt_pk_bf16_f32 v177, v186, v187
	v_cvt_pk_bf16_f32 v178, v188, v189
	v_cvt_pk_bf16_f32 v179, v190, v191
	v_cvt_pk_bf16_f32 v180, v192, v193
	v_cvt_pk_bf16_f32 v181, v194, v195
	v_cvt_pk_bf16_f32 v182, v196, v197
	v_cvt_pk_bf16_f32 v183, v198, v199
	v_cmp_nge_f32_e32 vcc, s86, v0
	s_cmp_eq_u64 vcc, 0
	s_cbranch_scc0 .LBB0_2595
	v_add_f32_e32 v161, v161, v0
	s_waitcnt lgkmcnt(8)
	v_mfma_f32_32x32x16_bf16 v[48:63], v[96:99], v[168:171], v[48:63]
	v_mfma_f32_32x32x16_bf16 v[48:63], v[100:103], v[172:175], v[48:63]
	v_mfma_f32_32x32x16_bf16 v[48:63], v[104:107], v[176:179], v[48:63]
	v_mfma_f32_32x32x16_bf16 v[48:63], v[108:111], v[180:183], v[48:63]
	s_waitcnt lgkmcnt(0)
	v_mfma_f32_32x32x16_bf16 v[32:47], v[236:239], v[168:171], v[32:47]
	v_mfma_f32_32x32x16_bf16 v[32:47], v[240:243], v[172:175], v[32:47]
	v_mfma_f32_32x32x16_bf16 v[32:47], v[244:247], v[176:179], v[32:47]
	v_mfma_f32_32x32x16_bf16 v[32:47], v[248:251], v[180:183], v[32:47]
	s_branch .LBB0_2581
; template <int MODE, int DQK, int DV>
; __device__ __forceinline__ void attn_pass(LAS unsigned char* lds, const Tens& T, size_t rowbase, int q0, f32x16 (&o)[DV / 32], float& l_out, const int wave, QPre* qp = nullptr) {
;     ...
;             for (;;) {
; #pragma unroll
;             for (int kb = 0; kb < 2; ++kb) {
;                 if (MODE == AM_FOX) {
;                     const float ctm = ct2 - m;
; #pragma unroll
;                     for (int g = 0; g < 4; ++g) {
;                         const f32x4 c = *(const LAS f32x4*)(lds + OFF_CS + (sl * NSUB + sub) * 256 + (32 * kb + 8 * g + 4 * h) * 4);
;                         p[kb][4 * g + 0] = fmaf(-LOG2E, c.x, ctm); p[kb][4 * g + 1] = fmaf(-LOG2E, c.y, ctm); p[kb][4 * g + 2] = fmaf(-LOG2E, c.z, ctm); p[kb][4 * g + 3] = fmaf(-LOG2E, c.w, ctm);
;                     }
;                 } else if (MODE == AM_DSA) {
; #pragma unroll
;                     for (int g = 0; g < 4; ++g) {
;                         const unsigned nib = __builtin_amdgcn_ubfe(mw[kb], (unsigned)(8 * g + 4 * h), 4u);
;                         const f32x4 t4 = *(const LAS f32x4*)(lds + OFF_LUT + 768 + nib * 16);
;                         p[kb][4 * g + 0] = t4.x; p[kb][4 * g + 1] = t4.y; p[kb][4 * g + 2] = t4.z; p[kb][4 * g + 3] = t4.w;
;                     }
;                     p[kb] = __builtin_amdgcn_mfma_f32_32x32x16_bf16(kone, qm, p[kb], 0, 0, 0);
;                 }
; #pragma unroll
;                 for (int s = 0; s < NSTEP; ++s) {
;                     bf16x8 a;
;                     if (s < 4) a = *(const LAS bf16x8*)(kfa[s] + sl * KSL + sub * KB_T + kb * 4096);
;                     else       a = *(const LAS bf16x8*)(kfa[s] + sl * KSL + sub * KB_T + kb * 2048);
;                     if ((MODE == AM_DIFF || MODE == AM_MLA) && s == 0)
;                         asm("v_mfma_f32_32x32x16_bf16 %0, %1, %2, %3" : "=&v"(p[kb]) : "v"(a), "v"(qf[0]), "v"(negm));
;                     else
;                         p[kb] = __builtin_amdgcn_mfma_f32_32x32x16_bf16(a, qf[s], p[kb], 0, 0, 0);
;                 }
;             }
;     ...
;             psum = 0.f;
; #pragma unroll
;             for (int rg = 0; rg < 16; ++rg) { const float e0 = __builtin_amdgcn_exp2f(p[0][rg]), e1 = __builtin_amdgcn_exp2f(p[1][rg]); p[0][rg] = e0; p[1][rg] = e1; psum += e0; psum += e1; }
;             if (!POSTHOC || redo) break;
.Lmla_fast2:
	v_add_u32_e32 v14, 0xc000, v144
	v_add_u32_e32 v15, 0xc000, v145
	v_add_u32_e32 v17, 0xc000, v146
	v_add_u32_e32 v30, 0xc000, v147
	v_add_u32_e32 v31, 0xc000, v148
	v_add_u32_e32 v252, 0xc000, v149
	v_add_u32_e32 v253, 0x8000, v151
	v_add_u32_e32 v163, 0x8000, v152
	ds_read_b128 v[200:203], v14
	ds_read_b128 v[204:207], v14 offset:4096
	ds_read_b128 v[208:211], v15
	ds_read_b128 v[212:215], v15 offset:4096
	ds_read_b128 v[216:219], v17
	ds_read_b128 v[220:223], v17 offset:4096
	ds_read_b128 v[224:227], v30
	ds_read_b128 v[228:231], v30 offset:4096
	s_waitcnt lgkmcnt(4)
	v_mfma_f32_32x32x16_bf16 v[80:95], v[200:203], v[112:115], v[64:79]
	ds_read_b128 v[200:203], v31
	v_mfma_f32_32x32x16_bf16 v[96:111], v[204:207], v[112:115], v[64:79]
	ds_read_b128 v[204:207], v31 offset:2048
	v_mfma_f32_32x32x16_bf16 v[80:95], v[208:211], v[116:119], v[80:95]
	ds_read_b128 v[208:211], v252
	v_mfma_f32_32x32x16_bf16 v[96:111], v[212:215], v[116:119], v[96:111]
	ds_read_b128 v[212:215], v252 offset:2048
	s_waitcnt lgkmcnt(4)
	v_mfma_f32_32x32x16_bf16 v[80:95], v[216:219], v[120:123], v[80:95]
	ds_read_b128 v[216:219], v14 offset:12288
	v_mfma_f32_32x32x16_bf16 v[96:111], v[220:223], v[120:123], v[96:111]
	ds_read_b128 v[220:223], v14 offset:16384
	v_mfma_f32_32x32x16_bf16 v[80:95], v[224:227], v[124:127], v[80:95]
	ds_read_b128 v[224:227], v15 offset:12288
	v_mfma_f32_32x32x16_bf16 v[96:111], v[228:231], v[124:127], v[96:111]
	ds_read_b128 v[228:231], v15 offset:16384
	s_waitcnt lgkmcnt(4)
	v_mfma_f32_32x32x16_bf16 v[80:95], v[200:203], v[128:131], v[80:95]
	ds_read_b128 v[200:203], v17 offset:12288
	v_mfma_f32_32x32x16_bf16 v[96:111], v[204:207], v[128:131], v[96:111]
	ds_read_b128 v[204:207], v17 offset:16384
	v_mfma_f32_32x32x16_bf16 v[80:95], v[208:211], v[132:135], v[80:95]
	ds_read_b128 v[208:211], v30 offset:12288
	v_mfma_f32_32x32x16_bf16 v[96:111], v[212:215], v[132:135], v[96:111]
	ds_read_b128 v[212:215], v30 offset:16384
	s_waitcnt lgkmcnt(4)
	v_mfma_f32_32x32x16_bf16 v[168:183], v[216:219], v[112:115], v[64:79]
	ds_read_b128 v[216:219], v31 offset:12288
	v_mfma_f32_32x32x16_bf16 v[184:199], v[220:223], v[112:115], v[64:79]
	ds_read_b128 v[220:223], v31 offset:14336
	v_mfma_f32_32x32x16_bf16 v[168:183], v[224:227], v[116:119], v[168:183]
	ds_read_b128 v[224:227], v252 offset:12288
	v_mfma_f32_32x32x16_bf16 v[184:199], v[228:231], v[116:119], v[184:199]
	ds_read_b128 v[228:231], v252 offset:14336
	v_exp_f32_e32 v80, v80
	v_exp_f32_e32 v81, v81
	v_exp_f32_e32 v82, v82
	v_add_f32_e32 v0, v80, v81
	v_exp_f32_e32 v83, v83
	v_add_f32_e32 v0, v0, v82
	v_exp_f32_e32 v84, v84
	v_add_f32_e32 v0, v0, v83
	v_exp_f32_e32 v85, v85
	s_waitcnt lgkmcnt(4)
	v_mfma_f32_32x32x16_bf16 v[168:183], v[200:203], v[120:123], v[168:183]
	ds_read_b64_tr_b16 v[2:3], v253
	ds_read_b64_tr_b16 v[4:5], v253 offset:1024
	v_add_f32_e32 v0, v0, v84
	v_exp_f32_e32 v86, v86
	v_add_f32_e32 v0, v0, v85
	v_exp_f32_e32 v87, v87
	v_add_f32_e32 v0, v0, v86
	v_exp_f32_e32 v88, v88
	v_add_f32_e32 v0, v0, v87
	v_exp_f32_e32 v89, v89
	v_add_f32_e32 v0, v0, v88
	v_mfma_f32_32x32x16_bf16 v[184:199], v[204:207], v[120:123], v[184:199]
	ds_read_b64_tr_b16 v[6:7], v253 offset:2048
	ds_read_b64_tr_b16 v[8:9], v253 offset:3072
	v_exp_f32_e32 v90, v90
	v_add_f32_e32 v0, v0, v89
	v_exp_f32_e32 v91, v91
	v_add_f32_e32 v0, v0, v90
	v_exp_f32_e32 v92, v92
	v_add_f32_e32 v0, v0, v91
	v_exp_f32_e32 v93, v93
	v_add_f32_e32 v0, v0, v92
	v_exp_f32_e32 v94, v94
	v_mfma_f32_32x32x16_bf16 v[168:183], v[208:211], v[124:127], v[168:183]
	ds_read_b64_tr_b16 v[10:11], v253 offset:4096
	ds_read_b64_tr_b16 v[12:13], v253 offset:5120
	v_add_f32_e32 v0, v0, v93
	v_exp_f32_e32 v95, v95
	v_add_f32_e32 v0, v0, v94
	v_exp_f32_e32 v96, v96
	v_add_f32_e32 v0, v0, v95
	v_exp_f32_e32 v97, v97
	v_add_f32_e32 v0, v0, v96
	v_exp_f32_e32 v98, v98
	v_add_f32_e32 v0, v0, v97
	v_mfma_f32_32x32x16_bf16 v[184:199], v[212:215], v[124:127], v[184:199]
	ds_read_b64_tr_b16 v[18:19], v253 offset:6144
	ds_read_b64_tr_b16 v[20:21], v253 offset:7168
	v_exp_f32_e32 v99, v99
	v_add_f32_e32 v0, v0, v98
	v_exp_f32_e32 v100, v100
	v_add_f32_e32 v0, v0, v99
	v_exp_f32_e32 v101, v101
	v_add_f32_e32 v0, v0, v100
	v_exp_f32_e32 v102, v102
	v_add_f32_e32 v0, v0, v101
	v_exp_f32_e32 v103, v103
	s_waitcnt lgkmcnt(8)
	v_mfma_f32_32x32x16_bf16 v[168:183], v[216:219], v[128:131], v[168:183]
	ds_read_b64_tr_b16 v[22:23], v163
	ds_read_b64_tr_b16 v[24:25], v163 offset:1024
	v_add_f32_e32 v0, v0, v102
	v_exp_f32_e32 v104, v104
	v_add_f32_e32 v0, v0, v103
	v_exp_f32_e32 v105, v105
	v_add_f32_e32 v0, v0, v104
	v_exp_f32_e32 v106, v106
	v_add_f32_e32 v0, v0, v105
	v_exp_f32_e32 v107, v107
	v_add_f32_e32 v0, v0, v106
	v_mfma_f32_32x32x16_bf16 v[184:199], v[220:223], v[128:131], v[184:199]
	ds_read_b64_tr_b16 v[26:27], v163 offset:2048
	ds_read_b64_tr_b16 v[28:29], v163 offset:3072
	v_exp_f32_e32 v108, v108
	v_add_f32_e32 v0, v0, v107
	v_exp_f32_e32 v109, v109
	v_add_f32_e32 v0, v0, v108
	v_exp_f32_e32 v110, v110
	v_add_f32_e32 v0, v0, v109
	v_exp_f32_e32 v111, v111
	v_add_f32_e32 v0, v0, v110
	v_add_f32_e32 v0, v0, v111
	v_mfma_f32_32x32x16_bf16 v[168:183], v[224:227], v[132:135], v[168:183]
	ds_read_b64_tr_b16 v[164:165], v163 offset:4096
	ds_read_b64_tr_b16 v[166:167], v163 offset:5120
	v_cvt_pk_bf16_f32 v80, v80, v81
	v_cvt_pk_bf16_f32 v81, v82, v83
	v_cvt_pk_bf16_f32 v82, v84, v85
	v_cvt_pk_bf16_f32 v83, v86, v87
	v_cvt_pk_bf16_f32 v84, v88, v89
	v_cvt_pk_bf16_f32 v85, v90, v91
	v_cvt_pk_bf16_f32 v86, v92, v93
	v_cvt_pk_bf16_f32 v87, v94, v95
	v_cvt_pk_bf16_f32 v88, v96, v97
	v_mfma_f32_32x32x16_bf16 v[184:199], v[228:231], v[132:135], v[184:199]
	ds_read_b64_tr_b16 v[232:233], v163 offset:6144
	ds_read_b64_tr_b16 v[234:235], v163 offset:7168
	v_cvt_pk_bf16_f32 v89, v98, v99
	v_cvt_pk_bf16_f32 v90, v100, v101
	v_cvt_pk_bf16_f32 v91, v102, v103
	v_cvt_pk_bf16_f32 v92, v104, v105
	v_cvt_pk_bf16_f32 v93, v106, v107
	v_cvt_pk_bf16_f32 v94, v108, v109
	v_cvt_pk_bf16_f32 v95, v110, v111
	v_cmp_nge_f32_e32 vcc, s86, v0
	s_cmp_eq_u64 vcc, 0
	s_cbranch_scc0 .Lmla_slow2
; #define LAS __attribute__((address_space(3)))
; __device__ __forceinline__ unsigned cvt_pk_bf16(float lo, float hi) { unsigned r; asm volatile("v_cvt_pk_bf16_f32 %0, %1, %2" : "=v"(r) : "v"(lo), "v"(hi)); return r; }
; template <int MODE, int DQK, int DV>
; __device__ __forceinline__ void attn_pass(LAS unsigned char* lds, const Tens& T, size_t rowbase, int q0, f32x16 (&o)[DV / 32], float& l_out, const int wave, QPre* qp = nullptr) {
;     ...
;             psum = 0.f;
; #pragma unroll
;             for (int rg = 0; rg < 16; ++rg) { const float e0 = __builtin_amdgcn_exp2f(p[0][rg]), e1 = __builtin_amdgcn_exp2f(p[1][rg]); p[0][rg] = e0; p[1][rg] = e1; psum += e0; psum += e1; }
;             if (!POSTHOC || redo) break;
;             if (__builtin_expect(!__any(!(psum <= BIG)), 1)) break;
;             redo = true;
;             }
;             l += psum;
;             bf16x8 pf[4];
; #pragma unroll
;             for (int kb = 0; kb < 2; ++kb)
; #pragma unroll
;                 for (int s = 0; s < 2; ++s) {
;                     u32x4 w;
;                     w.x = pg8::cvt_pk_bf16(p[kb][8 * s + 0], p[kb][8 * s + 1]); w.y = pg8::cvt_pk_bf16(p[kb][8 * s + 2], p[kb][8 * s + 3]);
;                     w.z = pg8::cvt_pk_bf16(p[kb][8 * s + 4], p[kb][8 * s + 5]); w.w = pg8::cvt_pk_bf16(p[kb][8 * s + 6], p[kb][8 * s + 7]);
;                     pf[2 * kb + s] = __builtin_bit_cast(bf16x8, w);
;                 }
; #pragma unroll
;             for (int db = 0; db < NDB; ++db) {
; #pragma unroll
;                 for (int ks = 0; ks < 4; ++ks) {
;                     const LAS unsigned char* vp = vfa[db] + sl * VSL + sub * VB_T + (16 * ks) * VROW;
;                     const s16x4 lo = __builtin_bit_cast(s16x4, __builtin_amdgcn_ds_read_tr16_b64_v4i16((LAS s16x4*)(vp)));
;                     const s16x4 hi = __builtin_bit_cast(s16x4, __builtin_amdgcn_ds_read_tr16_b64_v4i16((LAS s16x4*)(vp + 8 * VROW)));
;                     const bf16x8 a = {lo[0], lo[1], lo[2], lo[3], hi[0], hi[1], hi[2], hi[3]};
;                     o[db] = __builtin_amdgcn_mfma_f32_32x32x16_bf16(a, pf[ks], o[db], 0, 0, 0);
;                 }
;             }
	v_add_f32_e32 v161, v161, v0
	s_waitcnt lgkmcnt(8)
	v_mfma_f32_32x32x16_bf16 v[48:63], v[2:5], v[80:83], v[48:63]
	ds_read_b64_tr_b16 v[96:97], v253 offset:8192
	ds_read_b64_tr_b16 v[98:99], v253 offset:9216
	v_exp_f32_e32 v168, v168
	v_exp_f32_e32 v169, v169
	v_exp_f32_e32 v170, v170
	v_add_f32_e32 v0, v168, v169
	v_exp_f32_e32 v171, v171
	v_add_f32_e32 v0, v0, v170
	v_exp_f32_e32 v172, v172
	v_add_f32_e32 v0, v0, v171
	v_exp_f32_e32 v173, v173
	v_add_f32_e32 v0, v0, v172
	v_mfma_f32_32x32x16_bf16 v[48:63], v[6:9], v[84:87], v[48:63]
	ds_read_b64_tr_b16 v[100:101], v253 offset:10240
	ds_read_b64_tr_b16 v[102:103], v253 offset:11264
	v_exp_f32_e32 v174, v174
	v_add_f32_e32 v0, v0, v173
	v_exp_f32_e32 v175, v175
	v_add_f32_e32 v0, v0, v174
	v_exp_f32_e32 v176, v176
	v_add_f32_e32 v0, v0, v175
	v_exp_f32_e32 v177, v177
	v_add_f32_e32 v0, v0, v176
	v_exp_f32_e32 v178, v178
	v_add_f32_e32 v0, v0, v177
	v_mfma_f32_32x32x16_bf16 v[48:63], v[10:13], v[88:91], v[48:63]
	ds_read_b64_tr_b16 v[104:105], v253 offset:12288
	ds_read_b64_tr_b16 v[106:107], v253 offset:13312
	v_exp_f32_e32 v179, v179
	v_add_f32_e32 v0, v0, v178
	v_exp_f32_e32 v180, v180
	v_add_f32_e32 v0, v0, v179
	v_exp_f32_e32 v181, v181
	v_add_f32_e32 v0, v0, v180
	v_exp_f32_e32 v182, v182
	v_add_f32_e32 v0, v0, v181
	v_exp_f32_e32 v183, v183
	v_add_f32_e32 v0, v0, v182
	v_mfma_f32_32x32x16_bf16 v[48:63], v[18:21], v[92:95], v[48:63]
	ds_read_b64_tr_b16 v[108:109], v253 offset:14336
	ds_read_b64_tr_b16 v[110:111], v253 offset:15360
	v_exp_f32_e32 v184, v184
	v_add_f32_e32 v0, v0, v183
	v_exp_f32_e32 v185, v185
	v_add_f32_e32 v0, v0, v184
	v_exp_f32_e32 v186, v186
	v_add_f32_e32 v0, v0, v185
	v_exp_f32_e32 v187, v187
	v_add_f32_e32 v0, v0, v186
	v_exp_f32_e32 v188, v188
	v_add_f32_e32 v0, v0, v187
	s_waitcnt lgkmcnt(8)
	v_mfma_f32_32x32x16_bf16 v[32:47], v[22:25], v[80:83], v[32:47]
	ds_read_b64_tr_b16 v[236:237], v163 offset:8192
	ds_read_b64_tr_b16 v[238:239], v163 offset:9216
	v_exp_f32_e32 v189, v189
	v_add_f32_e32 v0, v0, v188
	v_exp_f32_e32 v190, v190
	v_add_f32_e32 v0, v0, v189
	v_exp_f32_e32 v191, v191
	v_add_f32_e32 v0, v0, v190
	v_exp_f32_e32 v192, v192
	v_add_f32_e32 v0, v0, v191
	v_exp_f32_e32 v193, v193
	v_add_f32_e32 v0, v0, v192
	v_mfma_f32_32x32x16_bf16 v[32:47], v[26:29], v[84:87], v[32:47]
	ds_read_b64_tr_b16 v[240:241], v163 offset:10240
	ds_read_b64_tr_b16 v[242:243], v163 offset:11264
	v_exp_f32_e32 v194, v194
	v_add_f32_e32 v0, v0, v193
	v_exp_f32_e32 v195, v195
	v_add_f32_e32 v0, v0, v194
	v_exp_f32_e32 v196, v196
	v_add_f32_e32 v0, v0, v195
	v_exp_f32_e32 v197, v197
	v_add_f32_e32 v0, v0, v196
	v_exp_f32_e32 v198, v198
	v_add_f32_e32 v0, v0, v197
	v_mfma_f32_32x32x16_bf16 v[32:47], v[164:167], v[88:91], v[32:47]
	ds_read_b64_tr_b16 v[244:245], v163 offset:12288
	ds_read_b64_tr_b16 v[246:247], v163 offset:13312
	v_exp_f32_e32 v199, v199
	v_add_f32_e32 v0, v0, v198
	v_add_f32_e32 v0, v0, v199
	v_cvt_pk_bf16_f32 v168, v168, v169
	v_cvt_pk_bf16_f32 v169, v170, v171
	v_cvt_pk_bf16_f32 v170, v172, v173
	v_cvt_pk_bf16_f32 v171, v174, v175
	v_cvt_pk_bf16_f32 v172, v176, v177
	v_cvt_pk_bf16_f32 v173, v178, v179
	v_cvt_pk_bf16_f32 v174, v180, v181
	v_mfma_f32_32x32x16_bf16 v[32:47], v[232:235], v[92:95], v[32:47]
	ds_read_b64_tr_b16 v[248:249], v163 offset:14336
	ds_read_b64_tr_b16 v[250:251], v163 offset:15360
	v_cvt_pk_bf16_f32 v175, v182, v183
	v_cvt_pk_bf16_f32 v176, v184, v185
	v_cvt_pk_bf16_f32 v177, v186, v187
	v_cvt_pk_bf16_f32 v178, v188, v189
	v_cvt_pk_bf16_f32 v179, v190, v191
	v_cvt_pk_bf16_f32 v180, v192, v193
	v_cvt_pk_bf16_f32 v181, v194, v195
	v_cvt_pk_bf16_f32 v182, v196, v197
	v_cvt_pk_bf16_f32 v183, v198, v199
	v_cmp_nge_f32_e32 vcc, s86, v0
	s_cmp_eq_u64 vcc, 0
	s_cbranch_scc0 .LBB0_2634
	v_add_f32_e32 v161, v161, v0
	s_waitcnt lgkmcnt(8)
	v_mfma_f32_32x32x16_bf16 v[48:63], v[96:99], v[168:171], v[48:63]
	v_mfma_f32_32x32x16_bf16 v[48:63], v[100:103], v[172:175], v[48:63]
	v_mfma_f32_32x32x16_bf16 v[48:63], v[104:107], v[176:179], v[48:63]
	v_mfma_f32_32x32x16_bf16 v[48:63], v[108:111], v[180:183], v[48:63]
	s_waitcnt lgkmcnt(0)
	v_mfma_f32_32x32x16_bf16 v[32:47], v[236:239], v[168:171], v[32:47]
	v_mfma_f32_32x32x16_bf16 v[32:47], v[240:243], v[172:175], v[32:47]
	v_mfma_f32_32x32x16_bf16 v[32:47], v[244:247], v[176:179], v[32:47]
	v_mfma_f32_32x32x16_bf16 v[32:47], v[248:251], v[180:183], v[32:47]
	s_branch .LBB0_2619

; #define PG8_STAGE(bufoff, gbase, voff) do { _Pragma("unroll") for (int _i = 0; _i < 2; ++_i) \
;         __builtin_amdgcn_global_load_lds((const unsigned*)((const char*)(gbase) + (voff)[_i]), (PG8_LAS unsigned*)(lds + (bufoff) + ldsw + _i * 8192), 16, 0, 0); } while (0)
; #define PG8_LDA(dst, b, h) do { _Pragma("unroll") for (int m = 0; m < 4; ++m) _Pragma("unroll") for (int k = 0; k < 2; ++k) dst[m][k] = *(const PG8_LAS bf16x8*)(lds + PG8_SA(b, h) + aoff + m * 2048 + k * 1024); } while (0)
; #define PG8_LDB(dst, b, h) do { _Pragma("unroll") for (int n = 0; n < 2; ++n) _Pragma("unroll") for (int k = 0; k < 2; ++k) dst[n][k] = *(const PG8_LAS bf16x8*)(lds + PG8_SB(b, h) + boff + n * 2048 + k * 1024); } while (0)
; #define PG8_MMA(ai, bj, At, Bt) do { __builtin_amdgcn_s_setprio(1); _Pragma("unroll") for (int m = 0; m < 4; ++m) _Pragma("unroll") for (int n = 0; n < 2; ++n) _Pragma("unroll") for (int k = 0; k < 2; ++k) \
;         acc[ai][bj][m][n] = __builtin_amdgcn_mfma_f32_16x16x32_bf16(Bt[n][k], At[m][k], acc[ai][bj][m][n], 0, 0, 0); __builtin_amdgcn_s_setprio(0); } while (0)
; #define PG8_WAIT_V(n) asm volatile("s_waitcnt vmcnt(" #n ")" ::: "memory")
; #define PG8_WAIT_L(n) asm volatile("s_waitcnt lgkmcnt(" #n ")" ::: "memory")
; #define PG8_BAR __builtin_amdgcn_s_barrier()
; template <class Epi, class Sched, bool ALIGN_EPI = false, bool SP2 = false>
; __device__ __forceinline__ void gemm_phase(PG8_LAS unsigned char* lds, const Gemm g, const Sched& S, const Epi& E, const int wid) {
;     ...
;             const char* a1 = cA + (size_t)(t + 1) * kstep;
;             const char* a2 = last ? nA : cA + (size_t)(t + 2) * kstep; const char* b2 = last ? nB : cB + (size_t)(t + 2) * kstep;
;             const char* a3 = a2 + kstep; const char* b3 = b2 + kstep;
;             if (last && has_next) S.a_ready(nxt);
;             if constexpr (SP2) {
;             PG8_LDB(B0, 0, 0); PG8_LDB(B1, 0, 1); PG8_SCHED; PG8_LDA(At, 0, 0); PG8_STAGE(PG8_SA(1, 1), a1 + hstepA, voffA);
;             PG8_WAIT_V(8); PG8_WAIT_L(0); PG8_BAR; PG8_MMA(0, 0, At, B0); PG8_MMA(0, 1, At, B1); PG8_BAR; PG8_SCHED;
;             PG8_LDA(At, 0, 1); PG8_STAGE(PG8_SB(0, 0), b2, voffB); PG8_STAGE(PG8_SB(0, 1), b2 + hstepB, voffB); PG8_STAGE(PG8_SA(0, 0), a2, voffA);
;             PG8_WAIT_V(8); PG8_WAIT_L(0); PG8_BAR; PG8_MMA(1, 0, At, B0); PG8_MMA(1, 1, At, B1); PG8_BAR; PG8_SCHED;
.LBB0_2725:
	ds_read_b128 v[128:131], v190
	ds_read_b128 v[132:135], v190 offset:1024
	ds_read_b128 v[136:139], v190 offset:2048
	ds_read_b128 v[140:143], v190 offset:3072
	ds_read_b128 v[144:147], v191
	ds_read_b128 v[148:151], v191 offset:1024
	ds_read_b128 v[172:175], v191 offset:2048
	ds_read_b128 v[176:179], v191 offset:3072
	s_add_u32 s34, s30, 0xfffc0080
	s_addc_u32 s35, s31, -1
	s_cmp_eq_u32 s60, 12
	s_cselect_b32 s37, s21, s35
	s_cselect_b32 s36, s27, s34
	s_cselect_b32 s35, s19, s59
	s_cselect_b32 s34, s29, s58
	s_add_i32 m0, s40, 0xc000
	ds_read_b128 v[180:183], v192
	ds_read_b128 v[184:187], v192 offset:1024
	ds_read_b128 v[194:197], v192 offset:2048
	ds_read_b128 v[198:201], v192 offset:3072
	ds_read_b128 v[202:205], v192 offset:4096
	ds_read_b128 v[206:209], v192 offset:5120
	ds_read_b128 v[210:213], v192 offset:6144
	ds_read_b128 v[214:217], v192 offset:7168
	global_load_lds_dwordx4 v164, s[30:31]
	s_add_i32 m0, s40, 0xe000
	s_nop 0
	global_load_lds_dwordx4 v166, s[30:31]
	s_waitcnt vmcnt(8) lgkmcnt(0)
	s_barrier
	s_setprio 1
	v_mfma_f32_16x16x32_bf16 v[124:127], v[128:131], v[180:183], v[124:127]
	v_mfma_f32_16x16x32_bf16 v[120:123], v[136:139], v[180:183], v[120:123]
	v_mfma_f32_16x16x32_bf16 v[108:111], v[128:131], v[194:197], v[108:111]
	v_mfma_f32_16x16x32_bf16 v[104:107], v[136:139], v[194:197], v[104:107]
	v_mfma_f32_16x16x32_bf16 v[92:95], v[128:131], v[202:205], v[92:95]
	v_mfma_f32_16x16x32_bf16 v[88:91], v[136:139], v[202:205], v[88:91]
	v_mfma_f32_16x16x32_bf16 v[76:79], v[128:131], v[210:213], v[76:79]
	v_mfma_f32_16x16x32_bf16 v[72:75], v[136:139], v[210:213], v[72:75]
	v_mfma_f32_16x16x32_bf16 v[124:127], v[132:135], v[184:187], v[124:127]
	v_mfma_f32_16x16x32_bf16 v[120:123], v[140:143], v[184:187], v[120:123]
	v_mfma_f32_16x16x32_bf16 v[108:111], v[132:135], v[198:201], v[108:111]
	v_mfma_f32_16x16x32_bf16 v[104:107], v[140:143], v[198:201], v[104:107]
	v_mfma_f32_16x16x32_bf16 v[92:95], v[132:135], v[206:209], v[92:95]
	v_mfma_f32_16x16x32_bf16 v[88:91], v[140:143], v[206:209], v[88:91]
	v_mfma_f32_16x16x32_bf16 v[76:79], v[132:135], v[214:217], v[76:79]
	v_mfma_f32_16x16x32_bf16 v[72:75], v[140:143], v[214:217], v[72:75]
	s_setprio 0
	s_setprio 1
	v_mfma_f32_16x16x32_bf16 v[116:119], v[144:147], v[180:183], v[116:119]
	v_mfma_f32_16x16x32_bf16 v[112:115], v[172:175], v[180:183], v[112:115]
	v_mfma_f32_16x16x32_bf16 v[100:103], v[144:147], v[194:197], v[100:103]
	v_mfma_f32_16x16x32_bf16 v[96:99], v[172:175], v[194:197], v[96:99]
	v_mfma_f32_16x16x32_bf16 v[84:87], v[144:147], v[202:205], v[84:87]
	v_mfma_f32_16x16x32_bf16 v[80:83], v[172:175], v[202:205], v[80:83]
	v_mfma_f32_16x16x32_bf16 v[68:71], v[144:147], v[210:213], v[68:71]
	v_mfma_f32_16x16x32_bf16 v[64:67], v[172:175], v[210:213], v[64:67]
	v_mfma_f32_16x16x32_bf16 v[116:119], v[148:151], v[184:187], v[116:119]
	v_mfma_f32_16x16x32_bf16 v[112:115], v[176:179], v[184:187], v[112:115]
	v_mfma_f32_16x16x32_bf16 v[100:103], v[148:151], v[198:201], v[100:103]
	v_mfma_f32_16x16x32_bf16 v[96:99], v[176:179], v[198:201], v[96:99]
	v_mfma_f32_16x16x32_bf16 v[84:87], v[148:151], v[206:209], v[84:87]
	v_mfma_f32_16x16x32_bf16 v[80:83], v[176:179], v[206:209], v[80:83]
	v_mfma_f32_16x16x32_bf16 v[68:71], v[148:151], v[214:217], v[68:71]
	v_mfma_f32_16x16x32_bf16 v[64:67], v[176:179], v[214:217], v[64:67]
	s_setprio 0
	s_barrier
	s_add_i32 s61, s49, s39
	v_lshl_add_u64 v[218:219], s[34:35], 0, v[154:155]
	s_mov_b32 m0, s61
	ds_read_b128 v[180:183], v192 offset:16384
	ds_read_b128 v[184:187], v192 offset:17408
	ds_read_b128 v[194:197], v192 offset:18432
	ds_read_b128 v[198:201], v192 offset:19456
	ds_read_b128 v[202:205], v192 offset:20480
	ds_read_b128 v[206:209], v192 offset:21504
	ds_read_b128 v[210:213], v192 offset:22528
	ds_read_b128 v[214:217], v192 offset:23552
	global_load_lds_dwordx4 v154, s[34:35]
	s_add_i32 m0, s61, 0x2000
	s_add_u32 s62, s34, 0x40000
	v_lshl_add_u64 v[220:221], s[34:35], 0, v[158:159]
	s_addc_u32 s63, s35, 0
	s_add_i32 s61, s56, s39
	global_load_lds_dwordx4 v158, s[34:35]
	s_mov_b32 m0, s61
	v_lshl_add_u64 v[224:225], s[36:37], 0, v[156:157]
	global_load_lds_dwordx4 v154, s[62:63]
	s_add_i32 m0, s61, 0x2000
	s_nop 0
	global_load_lds_dwordx4 v158, s[62:63]
	v_lshl_add_u64 v[222:223], s[36:37], 0, v[152:153]
	s_mov_b32 m0, s40
	s_nop 0
	global_load_lds_dwordx4 v152, s[36:37]
	s_mov_b32 m0, s41
	s_nop 0
	global_load_lds_dwordx4 v156, s[36:37]
	s_waitcnt vmcnt(8) lgkmcnt(0)
	s_barrier
	s_setprio 1
	v_mfma_f32_16x16x32_bf16 v[60:63], v[128:131], v[180:183], v[60:63]
	v_mfma_f32_16x16x32_bf16 v[56:59], v[136:139], v[180:183], v[56:59]
	v_mfma_f32_16x16x32_bf16 v[44:47], v[128:131], v[194:197], v[44:47]
	v_mfma_f32_16x16x32_bf16 v[40:43], v[136:139], v[194:197], v[40:43]
	v_mfma_f32_16x16x32_bf16 v[28:31], v[128:131], v[202:205], v[28:31]
	v_mfma_f32_16x16x32_bf16 v[24:27], v[136:139], v[202:205], v[24:27]
	v_mfma_f32_16x16x32_bf16 v[12:15], v[128:131], v[210:213], v[12:15]
	v_mfma_f32_16x16x32_bf16 v[8:11], v[136:139], v[210:213], v[8:11]
	v_mfma_f32_16x16x32_bf16 v[60:63], v[132:135], v[184:187], v[60:63]
	v_mfma_f32_16x16x32_bf16 v[56:59], v[140:143], v[184:187], v[56:59]
	v_mfma_f32_16x16x32_bf16 v[44:47], v[132:135], v[198:201], v[44:47]
	v_mfma_f32_16x16x32_bf16 v[40:43], v[140:143], v[198:201], v[40:43]
	v_mfma_f32_16x16x32_bf16 v[28:31], v[132:135], v[206:209], v[28:31]
	v_mfma_f32_16x16x32_bf16 v[24:27], v[140:143], v[206:209], v[24:27]
	v_mfma_f32_16x16x32_bf16 v[12:15], v[132:135], v[214:217], v[12:15]
	v_mfma_f32_16x16x32_bf16 v[8:11], v[140:143], v[214:217], v[8:11]
	s_setprio 0
	s_setprio 1
	v_mfma_f32_16x16x32_bf16 v[52:55], v[144:147], v[180:183], v[52:55]
	v_mfma_f32_16x16x32_bf16 v[48:51], v[172:175], v[180:183], v[48:51]
	v_mfma_f32_16x16x32_bf16 v[36:39], v[144:147], v[194:197], v[36:39]
	v_mfma_f32_16x16x32_bf16 v[32:35], v[172:175], v[194:197], v[32:35]
	v_mfma_f32_16x16x32_bf16 v[20:23], v[144:147], v[202:205], v[20:23]
	v_mfma_f32_16x16x32_bf16 v[16:19], v[172:175], v[202:205], v[16:19]
	v_mfma_f32_16x16x32_bf16 v[4:7], v[144:147], v[210:213], v[4:7]
	v_mfma_f32_16x16x32_bf16 v[0:3], v[172:175], v[210:213], v[0:3]
	v_mfma_f32_16x16x32_bf16 v[52:55], v[148:151], v[184:187], v[52:55]
	v_mfma_f32_16x16x32_bf16 v[48:51], v[176:179], v[184:187], v[48:51]
	v_mfma_f32_16x16x32_bf16 v[36:39], v[148:151], v[198:201], v[36:39]
	v_mfma_f32_16x16x32_bf16 v[32:35], v[176:179], v[198:201], v[32:35]
	v_mfma_f32_16x16x32_bf16 v[20:23], v[148:151], v[206:209], v[20:23]
	v_mfma_f32_16x16x32_bf16 v[16:19], v[176:179], v[206:209], v[16:19]
	v_mfma_f32_16x16x32_bf16 v[4:7], v[148:151], v[214:217], v[4:7]
	v_mfma_f32_16x16x32_bf16 v[0:3], v[176:179], v[214:217], v[0:3]
	s_setprio 0
	s_barrier
; #define PG8_STAGE(bufoff, gbase, voff) do { _Pragma("unroll") for (int _i = 0; _i < 2; ++_i) \
;         __builtin_amdgcn_global_load_lds((const unsigned*)((const char*)(gbase) + (voff)[_i]), (PG8_LAS unsigned*)(lds + (bufoff) + ldsw + _i * 8192), 16, 0, 0); } while (0)
; #define PG8_LDA(dst, b, h) do { _Pragma("unroll") for (int m = 0; m < 4; ++m) _Pragma("unroll") for (int k = 0; k < 2; ++k) dst[m][k] = *(const PG8_LAS bf16x8*)(lds + PG8_SA(b, h) + aoff + m * 2048 + k * 1024); } while (0)
; #define PG8_WAIT_V(n) asm volatile("s_waitcnt vmcnt(" #n ")" ::: "memory")
; #define PG8_WAIT_L(n) asm volatile("s_waitcnt lgkmcnt(" #n ")" ::: "memory")
; #define PG8_BAR __builtin_amdgcn_s_barrier()
; template <class Epi, class Sched, bool ALIGN_EPI = false, bool SP2 = false>
; __device__ __forceinline__ void gemm_phase(PG8_LAS unsigned char* lds, const Gemm g, const Sched& S, const Epi& E, const int wid) {
;     ...
;         for (int t = 0; t < nt; t += 2) {
;             const bool last = (t == nt - 2);
;             const char* a1 = cA + (size_t)(t + 1) * kstep;
;             const char* a2 = last ? nA : cA + (size_t)(t + 2) * kstep; const char* b2 = last ? nB : cB + (size_t)(t + 2) * kstep;
;             const char* a3 = a2 + kstep; const char* b3 = b2 + kstep;
;             if (last && has_next) S.a_ready(nxt);
;             if constexpr (SP2) {
;             PG8_LDB(B0, 0, 0); PG8_LDB(B1, 0, 1); PG8_SCHED; PG8_LDA(At, 0, 0); PG8_STAGE(PG8_SA(1, 1), a1 + hstepA, voffA);
;             PG8_WAIT_V(8); PG8_WAIT_L(0); PG8_BAR; PG8_MMA(0, 0, At, B0); PG8_MMA(0, 1, At, B1); PG8_BAR; PG8_SCHED;
;             PG8_LDA(At, 0, 1); PG8_STAGE(PG8_SB(0, 0), b2, voffB); PG8_STAGE(PG8_SB(0, 1), b2 + hstepB, voffB); PG8_STAGE(PG8_SA(0, 0), a2, voffA);
;             PG8_WAIT_V(8); PG8_WAIT_L(0); PG8_BAR; PG8_MMA(1, 0, At, B0); PG8_MMA(1, 1, At, B1); PG8_BAR; PG8_SCHED;
;             PG8_LDB(B0, 1, 0); PG8_LDB(B1, 1, 1); PG8_SCHED; PG8_LDA(At, 1, 0); PG8_STAGE(PG8_SA(0, 1), a2 + hstepA, voffA);
;             PG8_WAIT_V(8); PG8_WAIT_L(0); PG8_BAR; PG8_MMA(0, 0, At, B0); PG8_MMA(0, 1, At, B1); PG8_BAR; PG8_SCHED;
;             PG8_LDA(At, 1, 1); PG8_STAGE(PG8_SB(1, 0), b3, voffB); PG8_STAGE(PG8_SB(1, 1), b3 + hstepB, voffB); PG8_STAGE(PG8_SA(1, 0), a3, voffA);
;             PG8_WAIT_V(8); PG8_WAIT_L(0); PG8_BAR; PG8_MMA(1, 0, At, B0); PG8_MMA(1, 1, At, B1); PG8_BAR; PG8_SCHED;
	s_add_i32 s61, 0, 0x18000
	s_add_i32 s62, 0, 0x1c000
	v_add_u32_e32 v140, s61, v189
	v_add_u32_e32 v176, s62, v189
	ds_read_b128 v[128:131], v140
	ds_read_b128 v[132:135], v140 offset:1024
	ds_read_b128 v[136:139], v140 offset:2048
	ds_read_b128 v[140:143], v140 offset:3072
	ds_read_b128 v[144:147], v176
	ds_read_b128 v[148:151], v176 offset:1024
	ds_read_b128 v[172:175], v176 offset:2048
	ds_read_b128 v[176:179], v176 offset:3072
	s_add_u32 s36, s36, 0x40000
	s_addc_u32 s37, s37, 0
	s_mov_b32 m0, s42
	ds_read_b128 v[180:183], v192 offset:32768
	ds_read_b128 v[184:187], v192 offset:33792
	ds_read_b128 v[194:197], v192 offset:34816
	ds_read_b128 v[198:201], v192 offset:35840
	ds_read_b128 v[202:205], v192 offset:36864
	ds_read_b128 v[206:209], v192 offset:37888
	ds_read_b128 v[210:213], v192 offset:38912
	ds_read_b128 v[214:217], v192 offset:39936
	global_load_lds_dwordx4 v152, s[36:37]
	s_mov_b32 m0, s43
	s_nop 0
	global_load_lds_dwordx4 v156, s[36:37]
	s_waitcnt vmcnt(8) lgkmcnt(0)
	s_barrier
	s_setprio 1
	v_mfma_f32_16x16x32_bf16 v[124:127], v[128:131], v[180:183], v[124:127]
	v_mfma_f32_16x16x32_bf16 v[120:123], v[136:139], v[180:183], v[120:123]
	v_mfma_f32_16x16x32_bf16 v[108:111], v[128:131], v[194:197], v[108:111]
	v_mfma_f32_16x16x32_bf16 v[104:107], v[136:139], v[194:197], v[104:107]
	v_mfma_f32_16x16x32_bf16 v[92:95], v[128:131], v[202:205], v[92:95]
	v_mfma_f32_16x16x32_bf16 v[88:91], v[136:139], v[202:205], v[88:91]
	v_mfma_f32_16x16x32_bf16 v[76:79], v[128:131], v[210:213], v[76:79]
	v_mfma_f32_16x16x32_bf16 v[72:75], v[136:139], v[210:213], v[72:75]
	v_mfma_f32_16x16x32_bf16 v[124:127], v[132:135], v[184:187], v[124:127]
	v_mfma_f32_16x16x32_bf16 v[120:123], v[140:143], v[184:187], v[120:123]
	v_mfma_f32_16x16x32_bf16 v[108:111], v[132:135], v[198:201], v[108:111]
	v_mfma_f32_16x16x32_bf16 v[104:107], v[140:143], v[198:201], v[104:107]
	v_mfma_f32_16x16x32_bf16 v[92:95], v[132:135], v[206:209], v[92:95]
	v_mfma_f32_16x16x32_bf16 v[88:91], v[140:143], v[206:209], v[88:91]
	v_mfma_f32_16x16x32_bf16 v[76:79], v[132:135], v[214:217], v[76:79]
	v_mfma_f32_16x16x32_bf16 v[72:75], v[140:143], v[214:217], v[72:75]
	s_setprio 0
	s_setprio 1
	v_mfma_f32_16x16x32_bf16 v[116:119], v[144:147], v[180:183], v[116:119]
	v_mfma_f32_16x16x32_bf16 v[112:115], v[172:175], v[180:183], v[112:115]
	v_mfma_f32_16x16x32_bf16 v[100:103], v[144:147], v[194:197], v[100:103]
	v_mfma_f32_16x16x32_bf16 v[96:99], v[172:175], v[194:197], v[96:99]
	v_mfma_f32_16x16x32_bf16 v[84:87], v[144:147], v[202:205], v[84:87]
	v_mfma_f32_16x16x32_bf16 v[80:83], v[172:175], v[202:205], v[80:83]
	v_mfma_f32_16x16x32_bf16 v[68:71], v[144:147], v[210:213], v[68:71]
	v_mfma_f32_16x16x32_bf16 v[64:67], v[172:175], v[210:213], v[64:67]
	v_mfma_f32_16x16x32_bf16 v[116:119], v[148:151], v[184:187], v[116:119]
	v_mfma_f32_16x16x32_bf16 v[112:115], v[176:179], v[184:187], v[112:115]
	v_mfma_f32_16x16x32_bf16 v[100:103], v[148:151], v[198:201], v[100:103]
	v_mfma_f32_16x16x32_bf16 v[96:99], v[176:179], v[198:201], v[96:99]
	v_mfma_f32_16x16x32_bf16 v[84:87], v[148:151], v[206:209], v[84:87]
	v_mfma_f32_16x16x32_bf16 v[80:83], v[176:179], v[206:209], v[80:83]
	v_mfma_f32_16x16x32_bf16 v[68:71], v[148:151], v[214:217], v[68:71]
	v_mfma_f32_16x16x32_bf16 v[64:67], v[176:179], v[214:217], v[64:67]
	s_setprio 0
	s_barrier
	s_add_i32 s36, s61, s39
	v_lshl_add_u64 v[218:219], v[218:219], 0, s[14:15]
	s_mov_b32 m0, s36
	ds_read_b128 v[180:183], v192 offset:49152
	ds_read_b128 v[184:187], v192 offset:50176
	ds_read_b128 v[194:197], v192 offset:51200
	ds_read_b128 v[198:201], v192 offset:52224
	ds_read_b128 v[202:205], v192 offset:53248
	ds_read_b128 v[206:209], v192 offset:54272
	ds_read_b128 v[210:213], v192 offset:55296
	ds_read_b128 v[214:217], v192 offset:56320
	global_load_lds_dwordx4 v[218:219], off
	s_add_i32 m0, s36, 0x2000
	s_add_u32 s34, s34, 0x40080
	v_lshl_add_u64 v[218:219], v[220:221], 0, s[14:15]
	s_addc_u32 s35, s35, 0
	s_add_i32 s36, s62, s39
	global_load_lds_dwordx4 v[218:219], off
	s_mov_b32 m0, s36
	s_nop 0
	global_load_lds_dwordx4 v154, s[34:35]
	v_lshl_add_u64 v[218:219], s[34:35], 0, v[158:159]
	s_add_i32 m0, s36, 0x2000
	s_nop 0
	global_load_lds_dwordx4 v158, s[34:35]
	v_lshl_add_u64 v[218:219], v[222:223], 0, s[14:15]
	s_mov_b32 m0, s45
	s_nop 0
	global_load_lds_dwordx4 v[218:219], off
	v_lshl_add_u64 v[218:219], v[224:225], 0, s[14:15]
	s_mov_b32 m0, s46
	s_nop 0
	global_load_lds_dwordx4 v[218:219], off
	s_waitcnt vmcnt(8) lgkmcnt(0)
	s_barrier
	s_setprio 1
	v_mfma_f32_16x16x32_bf16 v[60:63], v[128:131], v[180:183], v[60:63]
	v_mfma_f32_16x16x32_bf16 v[56:59], v[136:139], v[180:183], v[56:59]
	v_mfma_f32_16x16x32_bf16 v[44:47], v[128:131], v[194:197], v[44:47]
	v_mfma_f32_16x16x32_bf16 v[40:43], v[136:139], v[194:197], v[40:43]
	v_mfma_f32_16x16x32_bf16 v[28:31], v[128:131], v[202:205], v[28:31]
	v_mfma_f32_16x16x32_bf16 v[24:27], v[136:139], v[202:205], v[24:27]
	v_mfma_f32_16x16x32_bf16 v[12:15], v[128:131], v[210:213], v[12:15]
	v_mfma_f32_16x16x32_bf16 v[8:11], v[136:139], v[210:213], v[8:11]
	v_mfma_f32_16x16x32_bf16 v[60:63], v[132:135], v[184:187], v[60:63]
	v_mfma_f32_16x16x32_bf16 v[56:59], v[140:143], v[184:187], v[56:59]
	v_mfma_f32_16x16x32_bf16 v[44:47], v[132:135], v[198:201], v[44:47]
	v_mfma_f32_16x16x32_bf16 v[40:43], v[140:143], v[198:201], v[40:43]
	v_mfma_f32_16x16x32_bf16 v[28:31], v[132:135], v[206:209], v[28:31]
	v_mfma_f32_16x16x32_bf16 v[24:27], v[140:143], v[206:209], v[24:27]
	v_mfma_f32_16x16x32_bf16 v[12:15], v[132:135], v[214:217], v[12:15]
	v_mfma_f32_16x16x32_bf16 v[8:11], v[140:143], v[214:217], v[8:11]
	s_setprio 0
	s_setprio 1
	v_mfma_f32_16x16x32_bf16 v[52:55], v[144:147], v[180:183], v[52:55]
	v_mfma_f32_16x16x32_bf16 v[48:51], v[172:175], v[180:183], v[48:51]
	v_mfma_f32_16x16x32_bf16 v[36:39], v[144:147], v[194:197], v[36:39]
	v_mfma_f32_16x16x32_bf16 v[32:35], v[172:175], v[194:197], v[32:35]
	v_mfma_f32_16x16x32_bf16 v[20:23], v[144:147], v[202:205], v[20:23]
	v_mfma_f32_16x16x32_bf16 v[16:19], v[172:175], v[202:205], v[16:19]
	v_mfma_f32_16x16x32_bf16 v[4:7], v[144:147], v[210:213], v[4:7]
	v_mfma_f32_16x16x32_bf16 v[0:3], v[172:175], v[210:213], v[0:3]
	v_mfma_f32_16x16x32_bf16 v[52:55], v[148:151], v[184:187], v[52:55]
	v_mfma_f32_16x16x32_bf16 v[48:51], v[176:179], v[184:187], v[48:51]
	v_mfma_f32_16x16x32_bf16 v[36:39], v[148:151], v[198:201], v[36:39]
	v_mfma_f32_16x16x32_bf16 v[32:35], v[176:179], v[198:201], v[32:35]
	v_mfma_f32_16x16x32_bf16 v[20:23], v[148:151], v[206:209], v[20:23]
	v_mfma_f32_16x16x32_bf16 v[16:19], v[176:179], v[206:209], v[16:19]
	v_mfma_f32_16x16x32_bf16 v[4:7], v[148:151], v[214:217], v[4:7]
	v_mfma_f32_16x16x32_bf16 v[0:3], v[176:179], v[214:217], v[0:3]
	s_setprio 0
	s_barrier
	s_add_i32 s60, s60, 2
	s_add_u32 s30, s30, 0x100
	s_addc_u32 s31, s31, 0
	s_add_u32 s58, s58, 0x100
	s_addc_u32 s59, s59, 0
	s_cmp_gt_u32 s60, 13
	s_cbranch_scc0 .LBB0_2725
	s_and_b64 vcc, exec, s[16:17]
	s_cbranch_vccz .LBB0_2728
	s_barrier

; #define PG8_STAGE(bufoff, gbase, voff) do { _Pragma("unroll") for (int _i = 0; _i < 2; ++_i) \
;         __builtin_amdgcn_global_load_lds((const unsigned*)((const char*)(gbase) + (voff)[_i]), (PG8_LAS unsigned*)(lds + (bufoff) + ldsw + _i * 8192), 16, 0, 0); } while (0)
; #define PG8_LDA(dst, b, h) do { _Pragma("unroll") for (int m = 0; m < 4; ++m) _Pragma("unroll") for (int k = 0; k < 2; ++k) dst[m][k] = *(const PG8_LAS bf16x8*)(lds + PG8_SA(b, h) + aoff + m * 2048 + k * 1024); } while (0)
; #define PG8_LDB(dst, b, h) do { _Pragma("unroll") for (int n = 0; n < 2; ++n) _Pragma("unroll") for (int k = 0; k < 2; ++k) dst[n][k] = *(const PG8_LAS bf16x8*)(lds + PG8_SB(b, h) + boff + n * 2048 + k * 1024); } while (0)
; #define PG8_MMA(ai, bj, At, Bt) do { __builtin_amdgcn_s_setprio(1); _Pragma("unroll") for (int m = 0; m < 4; ++m) _Pragma("unroll") for (int n = 0; n < 2; ++n) _Pragma("unroll") for (int k = 0; k < 2; ++k) \
;         acc[ai][bj][m][n] = __builtin_amdgcn_mfma_f32_16x16x32_bf16(Bt[n][k], At[m][k], acc[ai][bj][m][n], 0, 0, 0); __builtin_amdgcn_s_setprio(0); } while (0)
; #define PG8_WAIT_V(n) asm volatile("s_waitcnt vmcnt(" #n ")" ::: "memory")
; #define PG8_WAIT_L(n) asm volatile("s_waitcnt lgkmcnt(" #n ")" ::: "memory")
; #define PG8_BAR __builtin_amdgcn_s_barrier()
; template <class Epi, class Sched, bool ALIGN_EPI = false, bool SP2 = false>
; __device__ __forceinline__ void gemm_phase(PG8_LAS unsigned char* lds, const Gemm g, const Sched& S, const Epi& E, const int wid) {
;     ...
;             const char* a1 = cA + (size_t)(t + 1) * kstep;
;             const char* a2 = last ? nA : cA + (size_t)(t + 2) * kstep; const char* b2 = last ? nB : cB + (size_t)(t + 2) * kstep;
;             const char* a3 = a2 + kstep; const char* b3 = b2 + kstep;
;             if (last && has_next) S.a_ready(nxt);
;             if constexpr (SP2) {
;             PG8_LDB(B0, 0, 0); PG8_LDB(B1, 0, 1); PG8_SCHED; PG8_LDA(At, 0, 0); PG8_STAGE(PG8_SA(1, 1), a1 + hstepA, voffA);
;             PG8_WAIT_V(8); PG8_WAIT_L(0); PG8_BAR; PG8_MMA(0, 0, At, B0); PG8_MMA(0, 1, At, B1); PG8_BAR; PG8_SCHED;
;             PG8_LDA(At, 0, 1); PG8_STAGE(PG8_SB(0, 0), b2, voffB); PG8_STAGE(PG8_SB(0, 1), b2 + hstepB, voffB); PG8_STAGE(PG8_SA(0, 0), a2, voffA);
;             PG8_WAIT_V(8); PG8_WAIT_L(0); PG8_BAR; PG8_MMA(1, 0, At, B0); PG8_MMA(1, 1, At, B1); PG8_BAR; PG8_SCHED;
.LBB0_2812:
	ds_read_b128 v[148:151], v166
	ds_read_b128 v[152:155], v166 offset:1024
	ds_read_b128 v[156:159], v166 offset:2048
	ds_read_b128 v[160:163], v166 offset:3072
	ds_read_b128 v[172:175], v167
	ds_read_b128 v[176:179], v167 offset:1024
	ds_read_b128 v[180:183], v167 offset:2048
	ds_read_b128 v[184:187], v167 offset:3072
	s_add_u32 s26, s24, 0xfffc0080
	s_addc_u32 s27, s25, -1
	s_cmp_eq_u32 s57, 12
	s_cselect_b32 s29, s17, s27
	s_cselect_b32 s28, s47, s26
	s_cselect_b32 s27, s15, s56
	s_cselect_b32 s26, s48, s49
	s_add_i32 m0, s36, 0xc000
	ds_read_b128 v[188:191], v168
	ds_read_b128 v[192:195], v168 offset:1024
	ds_read_b128 v[196:199], v168 offset:2048
	ds_read_b128 v[200:203], v168 offset:3072
	ds_read_b128 v[204:207], v168 offset:4096
	ds_read_b128 v[208:211], v168 offset:5120
	ds_read_b128 v[212:215], v168 offset:6144
	ds_read_b128 v[216:219], v168 offset:7168
	global_load_lds_dwordx4 v140, s[24:25]
	s_add_i32 m0, s36, 0xe000
	s_nop 0
	global_load_lds_dwordx4 v142, s[24:25]
	s_waitcnt vmcnt(8) lgkmcnt(0)
	s_barrier
	s_setprio 1
	v_mfma_f32_16x16x32_bf16 v[124:127], v[148:151], v[188:191], v[124:127]
	v_mfma_f32_16x16x32_bf16 v[116:119], v[156:159], v[188:191], v[116:119]
	v_mfma_f32_16x16x32_bf16 v[108:111], v[148:151], v[196:199], v[108:111]
	v_mfma_f32_16x16x32_bf16 v[100:103], v[156:159], v[196:199], v[100:103]
	v_mfma_f32_16x16x32_bf16 v[92:95], v[148:151], v[204:207], v[92:95]
	v_mfma_f32_16x16x32_bf16 v[84:87], v[156:159], v[204:207], v[84:87]
	v_mfma_f32_16x16x32_bf16 v[76:79], v[148:151], v[212:215], v[76:79]
	v_mfma_f32_16x16x32_bf16 v[68:71], v[156:159], v[212:215], v[68:71]
	v_mfma_f32_16x16x32_bf16 v[124:127], v[152:155], v[192:195], v[124:127]
	v_mfma_f32_16x16x32_bf16 v[116:119], v[160:163], v[192:195], v[116:119]
	v_mfma_f32_16x16x32_bf16 v[108:111], v[152:155], v[200:203], v[108:111]
	v_mfma_f32_16x16x32_bf16 v[100:103], v[160:163], v[200:203], v[100:103]
	v_mfma_f32_16x16x32_bf16 v[92:95], v[152:155], v[208:211], v[92:95]
	v_mfma_f32_16x16x32_bf16 v[84:87], v[160:163], v[208:211], v[84:87]
	v_mfma_f32_16x16x32_bf16 v[76:79], v[152:155], v[216:219], v[76:79]
	v_mfma_f32_16x16x32_bf16 v[68:71], v[160:163], v[216:219], v[68:71]
	s_setprio 0
	s_setprio 1
	v_mfma_f32_16x16x32_bf16 v[120:123], v[172:175], v[188:191], v[120:123]
	v_mfma_f32_16x16x32_bf16 v[112:115], v[180:183], v[188:191], v[112:115]
	v_mfma_f32_16x16x32_bf16 v[104:107], v[172:175], v[196:199], v[104:107]
	v_mfma_f32_16x16x32_bf16 v[96:99], v[180:183], v[196:199], v[96:99]
	v_mfma_f32_16x16x32_bf16 v[88:91], v[172:175], v[204:207], v[88:91]
	v_mfma_f32_16x16x32_bf16 v[80:83], v[180:183], v[204:207], v[80:83]
	v_mfma_f32_16x16x32_bf16 v[72:75], v[172:175], v[212:215], v[72:75]
	v_mfma_f32_16x16x32_bf16 v[64:67], v[180:183], v[212:215], v[64:67]
	v_mfma_f32_16x16x32_bf16 v[120:123], v[176:179], v[192:195], v[120:123]
	v_mfma_f32_16x16x32_bf16 v[112:115], v[184:187], v[192:195], v[112:115]
	v_mfma_f32_16x16x32_bf16 v[104:107], v[176:179], v[200:203], v[104:107]
	v_mfma_f32_16x16x32_bf16 v[96:99], v[184:187], v[200:203], v[96:99]
	v_mfma_f32_16x16x32_bf16 v[88:91], v[176:179], v[208:211], v[88:91]
	v_mfma_f32_16x16x32_bf16 v[80:83], v[184:187], v[208:211], v[80:83]
	v_mfma_f32_16x16x32_bf16 v[72:75], v[176:179], v[216:219], v[72:75]
	v_mfma_f32_16x16x32_bf16 v[64:67], v[184:187], v[216:219], v[64:67]
	s_setprio 0
	s_barrier
	s_add_i32 s58, s43, s33
	v_lshl_add_u64 v[220:221], s[26:27], 0, v[132:133]
	s_mov_b32 m0, s58
	ds_read_b128 v[188:191], v168 offset:16384
	ds_read_b128 v[192:195], v168 offset:17408
	ds_read_b128 v[196:199], v168 offset:18432
	ds_read_b128 v[200:203], v168 offset:19456
	ds_read_b128 v[204:207], v168 offset:20480
	ds_read_b128 v[208:211], v168 offset:21504
	ds_read_b128 v[212:215], v168 offset:22528
	ds_read_b128 v[216:219], v168 offset:23552
	global_load_lds_dwordx4 v132, s[26:27]
	s_add_i32 m0, s58, 0x2000
	s_add_u32 s58, s26, 0x40000
	v_lshl_add_u64 v[222:223], s[26:27], 0, v[128:129]
	s_addc_u32 s59, s27, 0
	s_add_i32 s60, s44, s33
	global_load_lds_dwordx4 v128, s[26:27]
	s_mov_b32 m0, s60
	v_lshl_add_u64 v[226:227], s[28:29], 0, v[130:131]
	global_load_lds_dwordx4 v132, s[58:59]
	s_add_i32 m0, s60, 0x2000
	s_nop 0
	global_load_lds_dwordx4 v128, s[58:59]
	v_lshl_add_u64 v[224:225], s[28:29], 0, v[134:135]
	s_mov_b32 m0, s36
	s_nop 0
	global_load_lds_dwordx4 v134, s[28:29]
	s_mov_b32 m0, s37
	s_nop 0
	global_load_lds_dwordx4 v130, s[28:29]
	s_waitcnt vmcnt(8) lgkmcnt(0)
	s_barrier
	s_setprio 1
	v_mfma_f32_16x16x32_bf16 v[60:63], v[148:151], v[188:191], v[60:63]
	v_mfma_f32_16x16x32_bf16 v[52:55], v[156:159], v[188:191], v[52:55]
	v_mfma_f32_16x16x32_bf16 v[44:47], v[148:151], v[196:199], v[44:47]
	v_mfma_f32_16x16x32_bf16 v[36:39], v[156:159], v[196:199], v[36:39]
	v_mfma_f32_16x16x32_bf16 v[28:31], v[148:151], v[204:207], v[28:31]
	v_mfma_f32_16x16x32_bf16 v[20:23], v[156:159], v[204:207], v[20:23]
	v_mfma_f32_16x16x32_bf16 v[12:15], v[148:151], v[212:215], v[12:15]
	v_mfma_f32_16x16x32_bf16 v[4:7], v[156:159], v[212:215], v[4:7]
	v_mfma_f32_16x16x32_bf16 v[60:63], v[152:155], v[192:195], v[60:63]
	v_mfma_f32_16x16x32_bf16 v[52:55], v[160:163], v[192:195], v[52:55]
	v_mfma_f32_16x16x32_bf16 v[44:47], v[152:155], v[200:203], v[44:47]
	v_mfma_f32_16x16x32_bf16 v[36:39], v[160:163], v[200:203], v[36:39]
	v_mfma_f32_16x16x32_bf16 v[28:31], v[152:155], v[208:211], v[28:31]
	v_mfma_f32_16x16x32_bf16 v[20:23], v[160:163], v[208:211], v[20:23]
	v_mfma_f32_16x16x32_bf16 v[12:15], v[152:155], v[216:219], v[12:15]
	v_mfma_f32_16x16x32_bf16 v[4:7], v[160:163], v[216:219], v[4:7]
	s_setprio 0
	s_setprio 1
	v_mfma_f32_16x16x32_bf16 v[56:59], v[172:175], v[188:191], v[56:59]
	v_mfma_f32_16x16x32_bf16 v[48:51], v[180:183], v[188:191], v[48:51]
	v_mfma_f32_16x16x32_bf16 v[40:43], v[172:175], v[196:199], v[40:43]
	v_mfma_f32_16x16x32_bf16 v[32:35], v[180:183], v[196:199], v[32:35]
	v_mfma_f32_16x16x32_bf16 v[24:27], v[172:175], v[204:207], v[24:27]
	v_mfma_f32_16x16x32_bf16 v[16:19], v[180:183], v[204:207], v[16:19]
	v_mfma_f32_16x16x32_bf16 v[8:11], v[172:175], v[212:215], v[8:11]
	v_mfma_f32_16x16x32_bf16 v[0:3], v[180:183], v[212:215], v[0:3]
	v_mfma_f32_16x16x32_bf16 v[56:59], v[176:179], v[192:195], v[56:59]
	v_mfma_f32_16x16x32_bf16 v[48:51], v[184:187], v[192:195], v[48:51]
	v_mfma_f32_16x16x32_bf16 v[40:43], v[176:179], v[200:203], v[40:43]
	v_mfma_f32_16x16x32_bf16 v[32:35], v[184:187], v[200:203], v[32:35]
	v_mfma_f32_16x16x32_bf16 v[24:27], v[176:179], v[208:211], v[24:27]
	v_mfma_f32_16x16x32_bf16 v[16:19], v[184:187], v[208:211], v[16:19]
	v_mfma_f32_16x16x32_bf16 v[8:11], v[176:179], v[216:219], v[8:11]
	v_mfma_f32_16x16x32_bf16 v[0:3], v[184:187], v[216:219], v[0:3]
	s_setprio 0
	s_barrier
; #define PG8_STAGE(bufoff, gbase, voff) do { _Pragma("unroll") for (int _i = 0; _i < 2; ++_i) \
;         __builtin_amdgcn_global_load_lds((const unsigned*)((const char*)(gbase) + (voff)[_i]), (PG8_LAS unsigned*)(lds + (bufoff) + ldsw + _i * 8192), 16, 0, 0); } while (0)
; #define PG8_LDA(dst, b, h) do { _Pragma("unroll") for (int m = 0; m < 4; ++m) _Pragma("unroll") for (int k = 0; k < 2; ++k) dst[m][k] = *(const PG8_LAS bf16x8*)(lds + PG8_SA(b, h) + aoff + m * 2048 + k * 1024); } while (0)
; #define PG8_WAIT_V(n) asm volatile("s_waitcnt vmcnt(" #n ")" ::: "memory")
; #define PG8_WAIT_L(n) asm volatile("s_waitcnt lgkmcnt(" #n ")" ::: "memory")
; #define PG8_BAR __builtin_amdgcn_s_barrier()
; template <class Epi, class Sched, bool ALIGN_EPI = false, bool SP2 = false>
; __device__ __forceinline__ void gemm_phase(PG8_LAS unsigned char* lds, const Gemm g, const Sched& S, const Epi& E, const int wid) {
;     ...
;         for (int t = 0; t < nt; t += 2) {
;             const bool last = (t == nt - 2);
;             const char* a1 = cA + (size_t)(t + 1) * kstep;
;             const char* a2 = last ? nA : cA + (size_t)(t + 2) * kstep; const char* b2 = last ? nB : cB + (size_t)(t + 2) * kstep;
;             const char* a3 = a2 + kstep; const char* b3 = b2 + kstep;
;             if (last && has_next) S.a_ready(nxt);
;             if constexpr (SP2) {
;             PG8_LDB(B0, 0, 0); PG8_LDB(B1, 0, 1); PG8_SCHED; PG8_LDA(At, 0, 0); PG8_STAGE(PG8_SA(1, 1), a1 + hstepA, voffA);
;             PG8_WAIT_V(8); PG8_WAIT_L(0); PG8_BAR; PG8_MMA(0, 0, At, B0); PG8_MMA(0, 1, At, B1); PG8_BAR; PG8_SCHED;
;             PG8_LDA(At, 0, 1); PG8_STAGE(PG8_SB(0, 0), b2, voffB); PG8_STAGE(PG8_SB(0, 1), b2 + hstepB, voffB); PG8_STAGE(PG8_SA(0, 0), a2, voffA);
;             PG8_WAIT_V(8); PG8_WAIT_L(0); PG8_BAR; PG8_MMA(1, 0, At, B0); PG8_MMA(1, 1, At, B1); PG8_BAR; PG8_SCHED;
;             PG8_LDB(B0, 1, 0); PG8_LDB(B1, 1, 1); PG8_SCHED; PG8_LDA(At, 1, 0); PG8_STAGE(PG8_SA(0, 1), a2 + hstepA, voffA);
;             PG8_WAIT_V(8); PG8_WAIT_L(0); PG8_BAR; PG8_MMA(0, 0, At, B0); PG8_MMA(0, 1, At, B1); PG8_BAR; PG8_SCHED;
;             PG8_LDA(At, 1, 1); PG8_STAGE(PG8_SB(1, 0), b3, voffB); PG8_STAGE(PG8_SB(1, 1), b3 + hstepB, voffB); PG8_STAGE(PG8_SA(1, 0), a3, voffA);
;             PG8_WAIT_V(8); PG8_WAIT_L(0); PG8_BAR; PG8_MMA(1, 0, At, B0); PG8_MMA(1, 1, At, B1); PG8_BAR; PG8_SCHED;
	s_add_i32 s58, 0, 0x18000
	s_add_i32 s59, 0, 0x1c000
	v_add_u32_e32 v160, s58, v165
	v_add_u32_e32 v171, s59, v165
	ds_read_b128 v[148:151], v160
	ds_read_b128 v[152:155], v160 offset:1024
	ds_read_b128 v[156:159], v160 offset:2048
	ds_read_b128 v[160:163], v160 offset:3072
	ds_read_b128 v[172:175], v171
	ds_read_b128 v[176:179], v171 offset:1024
	ds_read_b128 v[180:183], v171 offset:2048
	ds_read_b128 v[184:187], v171 offset:3072
	s_add_u32 s28, s28, 0x40000
	s_addc_u32 s29, s29, 0
	s_mov_b32 m0, s38
	ds_read_b128 v[188:191], v168 offset:32768
	ds_read_b128 v[192:195], v168 offset:33792
	ds_read_b128 v[196:199], v168 offset:34816
	ds_read_b128 v[200:203], v168 offset:35840
	ds_read_b128 v[204:207], v168 offset:36864
	ds_read_b128 v[208:211], v168 offset:37888
	ds_read_b128 v[212:215], v168 offset:38912
	ds_read_b128 v[216:219], v168 offset:39936
	global_load_lds_dwordx4 v134, s[28:29]
	s_mov_b32 m0, s39
	s_nop 0
	global_load_lds_dwordx4 v130, s[28:29]
	s_waitcnt vmcnt(8) lgkmcnt(0)
	s_barrier
	s_setprio 1
	v_mfma_f32_16x16x32_bf16 v[124:127], v[148:151], v[188:191], v[124:127]
	v_mfma_f32_16x16x32_bf16 v[116:119], v[156:159], v[188:191], v[116:119]
	v_mfma_f32_16x16x32_bf16 v[108:111], v[148:151], v[196:199], v[108:111]
	v_mfma_f32_16x16x32_bf16 v[100:103], v[156:159], v[196:199], v[100:103]
	v_mfma_f32_16x16x32_bf16 v[92:95], v[148:151], v[204:207], v[92:95]
	v_mfma_f32_16x16x32_bf16 v[84:87], v[156:159], v[204:207], v[84:87]
	v_mfma_f32_16x16x32_bf16 v[76:79], v[148:151], v[212:215], v[76:79]
	v_mfma_f32_16x16x32_bf16 v[68:71], v[156:159], v[212:215], v[68:71]
	v_mfma_f32_16x16x32_bf16 v[124:127], v[152:155], v[192:195], v[124:127]
	v_mfma_f32_16x16x32_bf16 v[116:119], v[160:163], v[192:195], v[116:119]
	v_mfma_f32_16x16x32_bf16 v[108:111], v[152:155], v[200:203], v[108:111]
	v_mfma_f32_16x16x32_bf16 v[100:103], v[160:163], v[200:203], v[100:103]
	v_mfma_f32_16x16x32_bf16 v[92:95], v[152:155], v[208:211], v[92:95]
	v_mfma_f32_16x16x32_bf16 v[84:87], v[160:163], v[208:211], v[84:87]
	v_mfma_f32_16x16x32_bf16 v[76:79], v[152:155], v[216:219], v[76:79]
	v_mfma_f32_16x16x32_bf16 v[68:71], v[160:163], v[216:219], v[68:71]
	s_setprio 0
	s_setprio 1
	v_mfma_f32_16x16x32_bf16 v[120:123], v[172:175], v[188:191], v[120:123]
	v_mfma_f32_16x16x32_bf16 v[112:115], v[180:183], v[188:191], v[112:115]
	v_mfma_f32_16x16x32_bf16 v[104:107], v[172:175], v[196:199], v[104:107]
	v_mfma_f32_16x16x32_bf16 v[96:99], v[180:183], v[196:199], v[96:99]
	v_mfma_f32_16x16x32_bf16 v[88:91], v[172:175], v[204:207], v[88:91]
	v_mfma_f32_16x16x32_bf16 v[80:83], v[180:183], v[204:207], v[80:83]
	v_mfma_f32_16x16x32_bf16 v[72:75], v[172:175], v[212:215], v[72:75]
	v_mfma_f32_16x16x32_bf16 v[64:67], v[180:183], v[212:215], v[64:67]
	v_mfma_f32_16x16x32_bf16 v[120:123], v[176:179], v[192:195], v[120:123]
	v_mfma_f32_16x16x32_bf16 v[112:115], v[184:187], v[192:195], v[112:115]
	v_mfma_f32_16x16x32_bf16 v[104:107], v[176:179], v[200:203], v[104:107]
	v_mfma_f32_16x16x32_bf16 v[96:99], v[184:187], v[200:203], v[96:99]
	v_mfma_f32_16x16x32_bf16 v[88:91], v[176:179], v[208:211], v[88:91]
	v_mfma_f32_16x16x32_bf16 v[80:83], v[184:187], v[208:211], v[80:83]
	v_mfma_f32_16x16x32_bf16 v[72:75], v[176:179], v[216:219], v[72:75]
	v_mfma_f32_16x16x32_bf16 v[64:67], v[184:187], v[216:219], v[64:67]
	s_setprio 0
	s_barrier
	s_add_i32 s28, s58, s33
	v_lshl_add_u64 v[220:221], v[220:221], 0, s[10:11]
	s_mov_b32 m0, s28
	ds_read_b128 v[188:191], v168 offset:49152
	ds_read_b128 v[192:195], v168 offset:50176
	ds_read_b128 v[196:199], v168 offset:51200
	ds_read_b128 v[200:203], v168 offset:52224
	ds_read_b128 v[204:207], v168 offset:53248
	ds_read_b128 v[208:211], v168 offset:54272
	ds_read_b128 v[212:215], v168 offset:55296
	ds_read_b128 v[216:219], v168 offset:56320
	global_load_lds_dwordx4 v[220:221], off
	s_add_i32 m0, s28, 0x2000
	s_add_u32 s26, s26, 0x40080
	v_lshl_add_u64 v[220:221], v[222:223], 0, s[10:11]
	s_addc_u32 s27, s27, 0
	s_add_i32 s28, s59, s33
	global_load_lds_dwordx4 v[220:221], off
	s_mov_b32 m0, s28
	s_nop 0
	global_load_lds_dwordx4 v132, s[26:27]
	v_lshl_add_u64 v[220:221], s[26:27], 0, v[128:129]
	s_add_i32 m0, s28, 0x2000
	s_nop 0
	global_load_lds_dwordx4 v128, s[26:27]
	v_lshl_add_u64 v[220:221], v[224:225], 0, s[10:11]
	s_mov_b32 m0, s40
	s_nop 0
	global_load_lds_dwordx4 v[220:221], off
	v_lshl_add_u64 v[220:221], v[226:227], 0, s[10:11]
	s_mov_b32 m0, s41
	s_nop 0
	global_load_lds_dwordx4 v[220:221], off
	s_waitcnt vmcnt(8) lgkmcnt(0)
	s_barrier
	s_setprio 1
	v_mfma_f32_16x16x32_bf16 v[60:63], v[148:151], v[188:191], v[60:63]
	v_mfma_f32_16x16x32_bf16 v[52:55], v[156:159], v[188:191], v[52:55]
	v_mfma_f32_16x16x32_bf16 v[44:47], v[148:151], v[196:199], v[44:47]
	v_mfma_f32_16x16x32_bf16 v[36:39], v[156:159], v[196:199], v[36:39]
	v_mfma_f32_16x16x32_bf16 v[28:31], v[148:151], v[204:207], v[28:31]
	v_mfma_f32_16x16x32_bf16 v[20:23], v[156:159], v[204:207], v[20:23]
	v_mfma_f32_16x16x32_bf16 v[12:15], v[148:151], v[212:215], v[12:15]
	v_mfma_f32_16x16x32_bf16 v[4:7], v[156:159], v[212:215], v[4:7]
	v_mfma_f32_16x16x32_bf16 v[60:63], v[152:155], v[192:195], v[60:63]
	v_mfma_f32_16x16x32_bf16 v[52:55], v[160:163], v[192:195], v[52:55]
	v_mfma_f32_16x16x32_bf16 v[44:47], v[152:155], v[200:203], v[44:47]
	v_mfma_f32_16x16x32_bf16 v[36:39], v[160:163], v[200:203], v[36:39]
	v_mfma_f32_16x16x32_bf16 v[28:31], v[152:155], v[208:211], v[28:31]
	v_mfma_f32_16x16x32_bf16 v[20:23], v[160:163], v[208:211], v[20:23]
	v_mfma_f32_16x16x32_bf16 v[12:15], v[152:155], v[216:219], v[12:15]
	v_mfma_f32_16x16x32_bf16 v[4:7], v[160:163], v[216:219], v[4:7]
	s_setprio 0
	s_setprio 1
	v_mfma_f32_16x16x32_bf16 v[56:59], v[172:175], v[188:191], v[56:59]
	v_mfma_f32_16x16x32_bf16 v[48:51], v[180:183], v[188:191], v[48:51]
	v_mfma_f32_16x16x32_bf16 v[40:43], v[172:175], v[196:199], v[40:43]
	v_mfma_f32_16x16x32_bf16 v[32:35], v[180:183], v[196:199], v[32:35]
	v_mfma_f32_16x16x32_bf16 v[24:27], v[172:175], v[204:207], v[24:27]
	v_mfma_f32_16x16x32_bf16 v[16:19], v[180:183], v[204:207], v[16:19]
	v_mfma_f32_16x16x32_bf16 v[8:11], v[172:175], v[212:215], v[8:11]
	v_mfma_f32_16x16x32_bf16 v[0:3], v[180:183], v[212:215], v[0:3]
	v_mfma_f32_16x16x32_bf16 v[56:59], v[176:179], v[192:195], v[56:59]
	v_mfma_f32_16x16x32_bf16 v[48:51], v[184:187], v[192:195], v[48:51]
	v_mfma_f32_16x16x32_bf16 v[40:43], v[176:179], v[200:203], v[40:43]
	v_mfma_f32_16x16x32_bf16 v[32:35], v[184:187], v[200:203], v[32:35]
	v_mfma_f32_16x16x32_bf16 v[24:27], v[176:179], v[208:211], v[24:27]
	v_mfma_f32_16x16x32_bf16 v[16:19], v[184:187], v[208:211], v[16:19]
	v_mfma_f32_16x16x32_bf16 v[8:11], v[176:179], v[216:219], v[8:11]
	v_mfma_f32_16x16x32_bf16 v[0:3], v[184:187], v[216:219], v[0:3]
	s_setprio 0
	s_barrier
	s_add_i32 s57, s57, 2
	s_add_u32 s24, s24, 0x100
	s_addc_u32 s25, s25, 0
	s_add_u32 s49, s49, 0x100
	s_addc_u32 s56, s56, 0
	s_cmp_gt_u32 s57, 13
	s_cbranch_scc0 .LBB0_2812
	s_and_b64 vcc, exec, s[12:13]
	s_cbranch_vccz .LBB0_2815
	s_barrier

; #define PG8_STAGE(bufoff, gbase, voff) do { _Pragma("unroll") for (int _i = 0; _i < 2; ++_i) \
;         __builtin_amdgcn_global_load_lds((const unsigned*)((const char*)(gbase) + (voff)[_i]), (PG8_LAS unsigned*)(lds + (bufoff) + ldsw + _i * 8192), 16, 0, 0); } while (0)
; #define PG8_LDA(dst, b, h) do { _Pragma("unroll") for (int m = 0; m < 4; ++m) _Pragma("unroll") for (int k = 0; k < 2; ++k) dst[m][k] = *(const PG8_LAS bf16x8*)(lds + PG8_SA(b, h) + aoff + m * 2048 + k * 1024); } while (0)
; #define PG8_LDB(dst, b, h) do { _Pragma("unroll") for (int n = 0; n < 2; ++n) _Pragma("unroll") for (int k = 0; k < 2; ++k) dst[n][k] = *(const PG8_LAS bf16x8*)(lds + PG8_SB(b, h) + boff + n * 2048 + k * 1024); } while (0)
; #define PG8_MMA(ai, bj, At, Bt) do { __builtin_amdgcn_s_setprio(1); _Pragma("unroll") for (int m = 0; m < 4; ++m) _Pragma("unroll") for (int n = 0; n < 2; ++n) _Pragma("unroll") for (int k = 0; k < 2; ++k) \
;         acc[ai][bj][m][n] = __builtin_amdgcn_mfma_f32_16x16x32_bf16(Bt[n][k], At[m][k], acc[ai][bj][m][n], 0, 0, 0); __builtin_amdgcn_s_setprio(0); } while (0)
; #define PG8_WAIT_V(n) asm volatile("s_waitcnt vmcnt(" #n ")" ::: "memory")
; #define PG8_WAIT_L(n) asm volatile("s_waitcnt lgkmcnt(" #n ")" ::: "memory")
; #define PG8_BAR __builtin_amdgcn_s_barrier()
; template <class Epi, class Sched, bool ALIGN_EPI = false, bool SP2 = false>
; __device__ __forceinline__ void gemm_phase(PG8_LAS unsigned char* lds, const Gemm g, const Sched& S, const Epi& E, const int wid) {
;     ...
;             const char* a1 = cA + (size_t)(t + 1) * kstep;
;             const char* a2 = last ? nA : cA + (size_t)(t + 2) * kstep; const char* b2 = last ? nB : cB + (size_t)(t + 2) * kstep;
;             const char* a3 = a2 + kstep; const char* b3 = b2 + kstep;
;             if (last && has_next) S.a_ready(nxt);
;             if constexpr (SP2) {
;             PG8_LDB(B0, 0, 0); PG8_LDB(B1, 0, 1); PG8_SCHED; PG8_LDA(At, 0, 0); PG8_STAGE(PG8_SA(1, 1), a1 + hstepA, voffA);
;             PG8_WAIT_V(8); PG8_WAIT_L(0); PG8_BAR; PG8_MMA(0, 0, At, B0); PG8_MMA(0, 1, At, B1); PG8_BAR; PG8_SCHED;
;             PG8_LDA(At, 0, 1); PG8_STAGE(PG8_SB(0, 0), b2, voffB); PG8_STAGE(PG8_SB(0, 1), b2 + hstepB, voffB); PG8_STAGE(PG8_SA(0, 0), a2, voffA);
;             PG8_WAIT_V(8); PG8_WAIT_L(0); PG8_BAR; PG8_MMA(1, 0, At, B0); PG8_MMA(1, 1, At, B1); PG8_BAR; PG8_SCHED;
.LBB0_2897:
	ds_read_b128 v[128:131], v190
	ds_read_b128 v[132:135], v190 offset:1024
	ds_read_b128 v[136:139], v190 offset:2048
	ds_read_b128 v[140:143], v190 offset:3072
	ds_read_b128 v[144:147], v191
	ds_read_b128 v[148:151], v191 offset:1024
	ds_read_b128 v[172:175], v191 offset:2048
	ds_read_b128 v[176:179], v191 offset:3072
	s_add_u32 s24, s22, 0x100
	s_addc_u32 s25, s23, 0
	s_cmp_eq_u32 s58, 40
	s_cselect_b32 s29, s7, s25
	s_cselect_b32 s28, s6, s24
	s_cselect_b32 s27, s21, s57
	s_cselect_b32 s26, s20, s56
	s_add_i32 m0, s34, 0xc000
	ds_read_b128 v[180:183], v192
	ds_read_b128 v[184:187], v192 offset:1024
	ds_read_b128 v[194:197], v192 offset:2048
	ds_read_b128 v[198:201], v192 offset:3072
	ds_read_b128 v[202:205], v192 offset:4096
	ds_read_b128 v[206:209], v192 offset:5120
	ds_read_b128 v[210:213], v192 offset:6144
	ds_read_b128 v[214:217], v192 offset:7168
	global_load_lds_dwordx4 v164, s[22:23]
	s_add_i32 m0, s34, 0xe000
	s_nop 0
	global_load_lds_dwordx4 v166, s[22:23]
	s_waitcnt vmcnt(8) lgkmcnt(0)
	s_barrier
	s_setprio 1
	v_mfma_f32_16x16x32_bf16 v[124:127], v[128:131], v[180:183], v[124:127]
	v_mfma_f32_16x16x32_bf16 v[120:123], v[136:139], v[180:183], v[120:123]
	v_mfma_f32_16x16x32_bf16 v[108:111], v[128:131], v[194:197], v[108:111]
	v_mfma_f32_16x16x32_bf16 v[104:107], v[136:139], v[194:197], v[104:107]
	v_mfma_f32_16x16x32_bf16 v[92:95], v[128:131], v[202:205], v[92:95]
	v_mfma_f32_16x16x32_bf16 v[88:91], v[136:139], v[202:205], v[88:91]
	v_mfma_f32_16x16x32_bf16 v[76:79], v[128:131], v[210:213], v[76:79]
	v_mfma_f32_16x16x32_bf16 v[72:75], v[136:139], v[210:213], v[72:75]
	v_mfma_f32_16x16x32_bf16 v[124:127], v[132:135], v[184:187], v[124:127]
	v_mfma_f32_16x16x32_bf16 v[120:123], v[140:143], v[184:187], v[120:123]
	v_mfma_f32_16x16x32_bf16 v[108:111], v[132:135], v[198:201], v[108:111]
	v_mfma_f32_16x16x32_bf16 v[104:107], v[140:143], v[198:201], v[104:107]
	v_mfma_f32_16x16x32_bf16 v[92:95], v[132:135], v[206:209], v[92:95]
	v_mfma_f32_16x16x32_bf16 v[88:91], v[140:143], v[206:209], v[88:91]
	v_mfma_f32_16x16x32_bf16 v[76:79], v[132:135], v[214:217], v[76:79]
	v_mfma_f32_16x16x32_bf16 v[72:75], v[140:143], v[214:217], v[72:75]
	s_setprio 0
	s_setprio 1
	v_mfma_f32_16x16x32_bf16 v[116:119], v[144:147], v[180:183], v[116:119]
	v_mfma_f32_16x16x32_bf16 v[112:115], v[172:175], v[180:183], v[112:115]
	v_mfma_f32_16x16x32_bf16 v[100:103], v[144:147], v[194:197], v[100:103]
	v_mfma_f32_16x16x32_bf16 v[96:99], v[172:175], v[194:197], v[96:99]
	v_mfma_f32_16x16x32_bf16 v[84:87], v[144:147], v[202:205], v[84:87]
	v_mfma_f32_16x16x32_bf16 v[80:83], v[172:175], v[202:205], v[80:83]
	v_mfma_f32_16x16x32_bf16 v[68:71], v[144:147], v[210:213], v[68:71]
	v_mfma_f32_16x16x32_bf16 v[64:67], v[172:175], v[210:213], v[64:67]
	v_mfma_f32_16x16x32_bf16 v[116:119], v[148:151], v[184:187], v[116:119]
	v_mfma_f32_16x16x32_bf16 v[112:115], v[176:179], v[184:187], v[112:115]
	v_mfma_f32_16x16x32_bf16 v[100:103], v[148:151], v[198:201], v[100:103]
	v_mfma_f32_16x16x32_bf16 v[96:99], v[176:179], v[198:201], v[96:99]
	v_mfma_f32_16x16x32_bf16 v[84:87], v[148:151], v[206:209], v[84:87]
	v_mfma_f32_16x16x32_bf16 v[80:83], v[176:179], v[206:209], v[80:83]
	v_mfma_f32_16x16x32_bf16 v[68:71], v[148:151], v[214:217], v[68:71]
	v_mfma_f32_16x16x32_bf16 v[64:67], v[176:179], v[214:217], v[64:67]
	s_setprio 0
	s_barrier
	s_add_i32 s22, s43, s33
	v_lshl_add_u64 v[218:219], s[26:27], 0, v[154:155]
	s_mov_b32 m0, s22
	ds_read_b128 v[180:183], v192 offset:16384
	ds_read_b128 v[184:187], v192 offset:17408
	ds_read_b128 v[194:197], v192 offset:18432
	ds_read_b128 v[198:201], v192 offset:19456
	ds_read_b128 v[202:205], v192 offset:20480
	ds_read_b128 v[206:209], v192 offset:21504
	ds_read_b128 v[210:213], v192 offset:22528
	ds_read_b128 v[214:217], v192 offset:23552
	global_load_lds_dwordx4 v154, s[26:27]
	s_add_i32 m0, s22, 0x2000
	s_add_u32 s22, s26, 0xb0000
	v_lshl_add_u64 v[220:221], s[26:27], 0, v[158:159]
	s_addc_u32 s23, s27, 0
	s_add_i32 s59, s44, s33
	global_load_lds_dwordx4 v158, s[26:27]
	s_mov_b32 m0, s59
	v_lshl_add_u64 v[224:225], s[28:29], 0, v[156:157]
	global_load_lds_dwordx4 v154, s[22:23]
	s_add_i32 m0, s59, 0x2000
	s_nop 0
	global_load_lds_dwordx4 v158, s[22:23]
	v_lshl_add_u64 v[222:223], s[28:29], 0, v[152:153]
	s_mov_b32 m0, s34
	s_nop 0
	global_load_lds_dwordx4 v152, s[28:29]
	s_mov_b32 m0, s35
	s_nop 0
	global_load_lds_dwordx4 v156, s[28:29]
	s_waitcnt vmcnt(8) lgkmcnt(0)
	s_barrier
	s_setprio 1
	v_mfma_f32_16x16x32_bf16 v[60:63], v[128:131], v[180:183], v[60:63]
	v_mfma_f32_16x16x32_bf16 v[56:59], v[136:139], v[180:183], v[56:59]
	v_mfma_f32_16x16x32_bf16 v[44:47], v[128:131], v[194:197], v[44:47]
	v_mfma_f32_16x16x32_bf16 v[40:43], v[136:139], v[194:197], v[40:43]
	v_mfma_f32_16x16x32_bf16 v[28:31], v[128:131], v[202:205], v[28:31]
	v_mfma_f32_16x16x32_bf16 v[24:27], v[136:139], v[202:205], v[24:27]
	v_mfma_f32_16x16x32_bf16 v[12:15], v[128:131], v[210:213], v[12:15]
	v_mfma_f32_16x16x32_bf16 v[8:11], v[136:139], v[210:213], v[8:11]
	v_mfma_f32_16x16x32_bf16 v[60:63], v[132:135], v[184:187], v[60:63]
	v_mfma_f32_16x16x32_bf16 v[56:59], v[140:143], v[184:187], v[56:59]
	v_mfma_f32_16x16x32_bf16 v[44:47], v[132:135], v[198:201], v[44:47]
	v_mfma_f32_16x16x32_bf16 v[40:43], v[140:143], v[198:201], v[40:43]
	v_mfma_f32_16x16x32_bf16 v[28:31], v[132:135], v[206:209], v[28:31]
	v_mfma_f32_16x16x32_bf16 v[24:27], v[140:143], v[206:209], v[24:27]
	v_mfma_f32_16x16x32_bf16 v[12:15], v[132:135], v[214:217], v[12:15]
	v_mfma_f32_16x16x32_bf16 v[8:11], v[140:143], v[214:217], v[8:11]
	s_setprio 0
	s_setprio 1
	v_mfma_f32_16x16x32_bf16 v[52:55], v[144:147], v[180:183], v[52:55]
	v_mfma_f32_16x16x32_bf16 v[48:51], v[172:175], v[180:183], v[48:51]
	v_mfma_f32_16x16x32_bf16 v[36:39], v[144:147], v[194:197], v[36:39]
	v_mfma_f32_16x16x32_bf16 v[32:35], v[172:175], v[194:197], v[32:35]
	v_mfma_f32_16x16x32_bf16 v[20:23], v[144:147], v[202:205], v[20:23]
	v_mfma_f32_16x16x32_bf16 v[16:19], v[172:175], v[202:205], v[16:19]
	v_mfma_f32_16x16x32_bf16 v[4:7], v[144:147], v[210:213], v[4:7]
	v_mfma_f32_16x16x32_bf16 v[0:3], v[172:175], v[210:213], v[0:3]
	v_mfma_f32_16x16x32_bf16 v[52:55], v[148:151], v[184:187], v[52:55]
	v_mfma_f32_16x16x32_bf16 v[48:51], v[176:179], v[184:187], v[48:51]
	v_mfma_f32_16x16x32_bf16 v[36:39], v[148:151], v[198:201], v[36:39]
	v_mfma_f32_16x16x32_bf16 v[32:35], v[176:179], v[198:201], v[32:35]
	v_mfma_f32_16x16x32_bf16 v[20:23], v[148:151], v[206:209], v[20:23]
	v_mfma_f32_16x16x32_bf16 v[16:19], v[176:179], v[206:209], v[16:19]
	v_mfma_f32_16x16x32_bf16 v[4:7], v[148:151], v[214:217], v[4:7]
	v_mfma_f32_16x16x32_bf16 v[0:3], v[176:179], v[214:217], v[0:3]
	s_setprio 0
	s_barrier
; #define PG8_STAGE(bufoff, gbase, voff) do { _Pragma("unroll") for (int _i = 0; _i < 2; ++_i) \
;         __builtin_amdgcn_global_load_lds((const unsigned*)((const char*)(gbase) + (voff)[_i]), (PG8_LAS unsigned*)(lds + (bufoff) + ldsw + _i * 8192), 16, 0, 0); } while (0)
; #define PG8_LDA(dst, b, h) do { _Pragma("unroll") for (int m = 0; m < 4; ++m) _Pragma("unroll") for (int k = 0; k < 2; ++k) dst[m][k] = *(const PG8_LAS bf16x8*)(lds + PG8_SA(b, h) + aoff + m * 2048 + k * 1024); } while (0)
; #define PG8_WAIT_V(n) asm volatile("s_waitcnt vmcnt(" #n ")" ::: "memory")
; #define PG8_WAIT_L(n) asm volatile("s_waitcnt lgkmcnt(" #n ")" ::: "memory")
; #define PG8_BAR __builtin_amdgcn_s_barrier()
; template <class Epi, class Sched, bool ALIGN_EPI = false, bool SP2 = false>
; __device__ __forceinline__ void gemm_phase(PG8_LAS unsigned char* lds, const Gemm g, const Sched& S, const Epi& E, const int wid) {
;     ...
;         for (int t = 0; t < nt; t += 2) {
;             const bool last = (t == nt - 2);
;             const char* a1 = cA + (size_t)(t + 1) * kstep;
;             const char* a2 = last ? nA : cA + (size_t)(t + 2) * kstep; const char* b2 = last ? nB : cB + (size_t)(t + 2) * kstep;
;             const char* a3 = a2 + kstep; const char* b3 = b2 + kstep;
;             if (last && has_next) S.a_ready(nxt);
;             if constexpr (SP2) {
;             PG8_LDB(B0, 0, 0); PG8_LDB(B1, 0, 1); PG8_SCHED; PG8_LDA(At, 0, 0); PG8_STAGE(PG8_SA(1, 1), a1 + hstepA, voffA);
;             PG8_WAIT_V(8); PG8_WAIT_L(0); PG8_BAR; PG8_MMA(0, 0, At, B0); PG8_MMA(0, 1, At, B1); PG8_BAR; PG8_SCHED;
;             PG8_LDA(At, 0, 1); PG8_STAGE(PG8_SB(0, 0), b2, voffB); PG8_STAGE(PG8_SB(0, 1), b2 + hstepB, voffB); PG8_STAGE(PG8_SA(0, 0), a2, voffA);
;             PG8_WAIT_V(8); PG8_WAIT_L(0); PG8_BAR; PG8_MMA(1, 0, At, B0); PG8_MMA(1, 1, At, B1); PG8_BAR; PG8_SCHED;
;             PG8_LDB(B0, 1, 0); PG8_LDB(B1, 1, 1); PG8_SCHED; PG8_LDA(At, 1, 0); PG8_STAGE(PG8_SA(0, 1), a2 + hstepA, voffA);
;             PG8_WAIT_V(8); PG8_WAIT_L(0); PG8_BAR; PG8_MMA(0, 0, At, B0); PG8_MMA(0, 1, At, B1); PG8_BAR; PG8_SCHED;
;             PG8_LDA(At, 1, 1); PG8_STAGE(PG8_SB(1, 0), b3, voffB); PG8_STAGE(PG8_SB(1, 1), b3 + hstepB, voffB); PG8_STAGE(PG8_SA(1, 0), a3, voffA);
;             PG8_WAIT_V(8); PG8_WAIT_L(0); PG8_BAR; PG8_MMA(1, 0, At, B0); PG8_MMA(1, 1, At, B1); PG8_BAR; PG8_SCHED;
	s_add_i32 s59, 0, 0x18000
	s_add_i32 s60, 0, 0x1c000
	v_add_u32_e32 v140, s59, v189
	v_add_u32_e32 v176, s60, v189
	ds_read_b128 v[128:131], v140
	ds_read_b128 v[132:135], v140 offset:1024
	ds_read_b128 v[136:139], v140 offset:2048
	ds_read_b128 v[140:143], v140 offset:3072
	ds_read_b128 v[144:147], v176
	ds_read_b128 v[148:151], v176 offset:1024
	ds_read_b128 v[172:175], v176 offset:2048
	ds_read_b128 v[176:179], v176 offset:3072
	s_add_u32 s22, s28, 0xb0000
	s_addc_u32 s23, s29, 0
	s_mov_b32 m0, s36
	ds_read_b128 v[180:183], v192 offset:32768
	ds_read_b128 v[184:187], v192 offset:33792
	ds_read_b128 v[194:197], v192 offset:34816
	ds_read_b128 v[198:201], v192 offset:35840
	ds_read_b128 v[202:205], v192 offset:36864
	ds_read_b128 v[206:209], v192 offset:37888
	ds_read_b128 v[210:213], v192 offset:38912
	ds_read_b128 v[214:217], v192 offset:39936
	global_load_lds_dwordx4 v152, s[22:23]
	s_mov_b32 m0, s37
	s_nop 0
	global_load_lds_dwordx4 v156, s[22:23]
	s_waitcnt vmcnt(8) lgkmcnt(0)
	s_barrier
	s_setprio 1
	v_mfma_f32_16x16x32_bf16 v[124:127], v[128:131], v[180:183], v[124:127]
	v_mfma_f32_16x16x32_bf16 v[120:123], v[136:139], v[180:183], v[120:123]
	v_mfma_f32_16x16x32_bf16 v[108:111], v[128:131], v[194:197], v[108:111]
	v_mfma_f32_16x16x32_bf16 v[104:107], v[136:139], v[194:197], v[104:107]
	v_mfma_f32_16x16x32_bf16 v[92:95], v[128:131], v[202:205], v[92:95]
	v_mfma_f32_16x16x32_bf16 v[88:91], v[136:139], v[202:205], v[88:91]
	v_mfma_f32_16x16x32_bf16 v[76:79], v[128:131], v[210:213], v[76:79]
	v_mfma_f32_16x16x32_bf16 v[72:75], v[136:139], v[210:213], v[72:75]
	v_mfma_f32_16x16x32_bf16 v[124:127], v[132:135], v[184:187], v[124:127]
	v_mfma_f32_16x16x32_bf16 v[120:123], v[140:143], v[184:187], v[120:123]
	v_mfma_f32_16x16x32_bf16 v[108:111], v[132:135], v[198:201], v[108:111]
	v_mfma_f32_16x16x32_bf16 v[104:107], v[140:143], v[198:201], v[104:107]
	v_mfma_f32_16x16x32_bf16 v[92:95], v[132:135], v[206:209], v[92:95]
	v_mfma_f32_16x16x32_bf16 v[88:91], v[140:143], v[206:209], v[88:91]
	v_mfma_f32_16x16x32_bf16 v[76:79], v[132:135], v[214:217], v[76:79]
	v_mfma_f32_16x16x32_bf16 v[72:75], v[140:143], v[214:217], v[72:75]
	s_setprio 0
	s_setprio 1
	v_mfma_f32_16x16x32_bf16 v[116:119], v[144:147], v[180:183], v[116:119]
	v_mfma_f32_16x16x32_bf16 v[112:115], v[172:175], v[180:183], v[112:115]
	v_mfma_f32_16x16x32_bf16 v[100:103], v[144:147], v[194:197], v[100:103]
	v_mfma_f32_16x16x32_bf16 v[96:99], v[172:175], v[194:197], v[96:99]
	v_mfma_f32_16x16x32_bf16 v[84:87], v[144:147], v[202:205], v[84:87]
	v_mfma_f32_16x16x32_bf16 v[80:83], v[172:175], v[202:205], v[80:83]
	v_mfma_f32_16x16x32_bf16 v[68:71], v[144:147], v[210:213], v[68:71]
	v_mfma_f32_16x16x32_bf16 v[64:67], v[172:175], v[210:213], v[64:67]
	v_mfma_f32_16x16x32_bf16 v[116:119], v[148:151], v[184:187], v[116:119]
	v_mfma_f32_16x16x32_bf16 v[112:115], v[176:179], v[184:187], v[112:115]
	v_mfma_f32_16x16x32_bf16 v[100:103], v[148:151], v[198:201], v[100:103]
	v_mfma_f32_16x16x32_bf16 v[96:99], v[176:179], v[198:201], v[96:99]
	v_mfma_f32_16x16x32_bf16 v[84:87], v[148:151], v[206:209], v[84:87]
	v_mfma_f32_16x16x32_bf16 v[80:83], v[176:179], v[206:209], v[80:83]
	v_mfma_f32_16x16x32_bf16 v[68:71], v[148:151], v[214:217], v[68:71]
	v_mfma_f32_16x16x32_bf16 v[64:67], v[176:179], v[214:217], v[64:67]
	s_setprio 0
	s_barrier
	s_add_i32 s22, s59, s33
	v_lshl_add_u64 v[218:219], v[218:219], 0, s[16:17]
	s_mov_b32 m0, s22
	ds_read_b128 v[180:183], v192 offset:49152
	ds_read_b128 v[184:187], v192 offset:50176
	ds_read_b128 v[194:197], v192 offset:51200
	ds_read_b128 v[198:201], v192 offset:52224
	ds_read_b128 v[202:205], v192 offset:53248
	ds_read_b128 v[206:209], v192 offset:54272
	ds_read_b128 v[210:213], v192 offset:55296
	ds_read_b128 v[214:217], v192 offset:56320
	global_load_lds_dwordx4 v[218:219], off
	s_add_i32 m0, s22, 0x2000
	s_add_u32 s22, s26, 0xb0080
	v_lshl_add_u64 v[218:219], v[220:221], 0, s[16:17]
	s_addc_u32 s23, s27, 0
	s_add_i32 s26, s60, s33
	global_load_lds_dwordx4 v[218:219], off
	s_mov_b32 m0, s26
	s_nop 0
	global_load_lds_dwordx4 v154, s[22:23]
	v_lshl_add_u64 v[218:219], s[22:23], 0, v[158:159]
	s_add_i32 m0, s26, 0x2000
	s_nop 0
	global_load_lds_dwordx4 v158, s[22:23]
	v_lshl_add_u64 v[218:219], v[222:223], 0, s[16:17]
	s_mov_b32 m0, s39
	s_nop 0
	global_load_lds_dwordx4 v[218:219], off
	v_lshl_add_u64 v[218:219], v[224:225], 0, s[16:17]
	s_mov_b32 m0, s40
	s_nop 0
	global_load_lds_dwordx4 v[218:219], off
	s_waitcnt vmcnt(8) lgkmcnt(0)
	s_barrier
	s_setprio 1
	v_mfma_f32_16x16x32_bf16 v[60:63], v[128:131], v[180:183], v[60:63]
	v_mfma_f32_16x16x32_bf16 v[56:59], v[136:139], v[180:183], v[56:59]
	v_mfma_f32_16x16x32_bf16 v[44:47], v[128:131], v[194:197], v[44:47]
	v_mfma_f32_16x16x32_bf16 v[40:43], v[136:139], v[194:197], v[40:43]
	v_mfma_f32_16x16x32_bf16 v[28:31], v[128:131], v[202:205], v[28:31]
	v_mfma_f32_16x16x32_bf16 v[24:27], v[136:139], v[202:205], v[24:27]
	v_mfma_f32_16x16x32_bf16 v[12:15], v[128:131], v[210:213], v[12:15]
	v_mfma_f32_16x16x32_bf16 v[8:11], v[136:139], v[210:213], v[8:11]
	v_mfma_f32_16x16x32_bf16 v[60:63], v[132:135], v[184:187], v[60:63]
	v_mfma_f32_16x16x32_bf16 v[56:59], v[140:143], v[184:187], v[56:59]
	v_mfma_f32_16x16x32_bf16 v[44:47], v[132:135], v[198:201], v[44:47]
	v_mfma_f32_16x16x32_bf16 v[40:43], v[140:143], v[198:201], v[40:43]
	v_mfma_f32_16x16x32_bf16 v[28:31], v[132:135], v[206:209], v[28:31]
	v_mfma_f32_16x16x32_bf16 v[24:27], v[140:143], v[206:209], v[24:27]
	v_mfma_f32_16x16x32_bf16 v[12:15], v[132:135], v[214:217], v[12:15]
	v_mfma_f32_16x16x32_bf16 v[8:11], v[140:143], v[214:217], v[8:11]
	s_setprio 0
	s_setprio 1
	v_mfma_f32_16x16x32_bf16 v[52:55], v[144:147], v[180:183], v[52:55]
	v_mfma_f32_16x16x32_bf16 v[48:51], v[172:175], v[180:183], v[48:51]
	v_mfma_f32_16x16x32_bf16 v[36:39], v[144:147], v[194:197], v[36:39]
	v_mfma_f32_16x16x32_bf16 v[32:35], v[172:175], v[194:197], v[32:35]
	v_mfma_f32_16x16x32_bf16 v[20:23], v[144:147], v[202:205], v[20:23]
	v_mfma_f32_16x16x32_bf16 v[16:19], v[172:175], v[202:205], v[16:19]
	v_mfma_f32_16x16x32_bf16 v[4:7], v[144:147], v[210:213], v[4:7]
	v_mfma_f32_16x16x32_bf16 v[0:3], v[172:175], v[210:213], v[0:3]
	v_mfma_f32_16x16x32_bf16 v[52:55], v[148:151], v[184:187], v[52:55]
	v_mfma_f32_16x16x32_bf16 v[48:51], v[176:179], v[184:187], v[48:51]
	v_mfma_f32_16x16x32_bf16 v[36:39], v[148:151], v[198:201], v[36:39]
	v_mfma_f32_16x16x32_bf16 v[32:35], v[176:179], v[198:201], v[32:35]
	v_mfma_f32_16x16x32_bf16 v[20:23], v[148:151], v[206:209], v[20:23]
	v_mfma_f32_16x16x32_bf16 v[16:19], v[176:179], v[206:209], v[16:19]
	v_mfma_f32_16x16x32_bf16 v[4:7], v[148:151], v[214:217], v[4:7]
	v_mfma_f32_16x16x32_bf16 v[0:3], v[176:179], v[214:217], v[0:3]
	s_setprio 0
	s_barrier
	s_add_i32 s58, s58, 2
	s_add_u32 s56, s56, 0x100
	s_addc_u32 s57, s57, 0
	s_cmp_gt_u32 s58, 41
	s_mov_b64 s[22:23], s[24:25]
	s_cbranch_scc0 .LBB0_2897
	s_and_b64 vcc, exec, s[18:19]
	s_cbranch_vccz .LBB0_2900
	s_barrier
